# attn near-tile bias via padded LDS table; up GEMM epilogue full 128B-line stores (64 contiguous cols per wave + DPP row exchange); down GEMM tile order 4x8 per XCD round; removed mid-block s_setprio 0
# speedup vs baseline: 1.0022x; 1.0022x over previous
; #define PG8_STAGE(bufoff, gbase, voff) do { _Pragma("unroll") for (int _i = 0; _i < 2; ++_i) \
;         __builtin_amdgcn_global_load_lds((const unsigned*)((const char*)(gbase) + (voff)[_i]), (PG8_LAS unsigned*)(lds + (bufoff) + ldsw + _i * 8192), 16, 0, 0); } while (0)
; #define PG8_LDA(dst, b, h) do { _Pragma("unroll") for (int m = 0; m < 4; ++m) _Pragma("unroll") for (int k = 0; k < 2; ++k) dst[m][k] = *(const PG8_LAS bf16x8*)(lds + PG8_SA(b, h) + aoff + m * 2048 + k * 1024); } while (0)
; #define PG8_LDB(dst, b, h) do { _Pragma("unroll") for (int n = 0; n < 2; ++n) _Pragma("unroll") for (int k = 0; k < 2; ++k) dst[n][k] = *(const PG8_LAS bf16x8*)(lds + PG8_SB(b, h) + boff + n * 2048 + k * 1024); } while (0)
; #define PG8_MMA(ai, bj, At, Bt) do { __builtin_amdgcn_s_setprio(1); _Pragma("unroll") for (int m = 0; m < 4; ++m) _Pragma("unroll") for (int n = 0; n < 2; ++n) _Pragma("unroll") for (int k = 0; k < 2; ++k) \
;         acc[ai][bj][m][n] = mma16(Bt[n][k], At[m][k], acc[ai][bj][m][n]); __builtin_amdgcn_s_setprio(0); } while (0)
; template <class Epi, class Sched, bool ALIGN_EPI = false, bool SP2 = false>
; __device__ __forceinline__ void gemm_phase(PG8_LAS unsigned char* lds, const Gemm g, const Sched& S, const Epi& E, Stopwatch& sw) {
;     ...
;             const bool last = (t == nt - 2);
;             const char* a1 = cA + (size_t)(t + 1) * kstep;
;             const char* a2 = last ? nA : cA + (size_t)(t + 2) * kstep; const char* b2 = last ? nB : cB + (size_t)(t + 2) * kstep;
;             const char* a3 = a2 + kstep; const char* b3 = b2 + kstep;
;             if (last && has_next) S.a_ready(nxt);
;             if constexpr (SP2) {
;             int relax = __builtin_amdgcn_readfirstlane((int)((ui > 0) && (t == 0))); asm volatile("" : "+s"(relax));
;             PG8_LDB(B0, 0, 0); PG8_LDB(B1, 0, 1); PG8_SCHED; PG8_LDA(At, 0, 0); if (!relax) PG8_STAGE(PG8_SA(1, 1), a1 + hstep, voffA);
;             if (relax) PG8_WAIT_VN(8 + Epi::NST); else PG8_WAIT_V(8); PG8_WAIT_L(0); PG8_BAR; PG8_MMA(0, 0, At, B0); PG8_MMA(0, 1, At, B1); PG8_BAR; PG8_SCHED;
;             PG8_LDA(At, 0, 1); PG8_STAGE(PG8_SB(0, 0), b2, voffB); PG8_STAGE(PG8_SB(0, 1), b2 + hstep, voffB); PG8_STAGE(PG8_SA(0, 0), a2, voffA);
;             if (relax) PG8_WAIT_VN(8 + Epi::NST); else PG8_WAIT_V(8); PG8_WAIT_L(0); PG8_BAR; PG8_MMA(1, 0, At, B0); PG8_MMA(1, 1, At, B1); PG8_BAR; PG8_SCHED;
.LBB0_157:
	s_add_u32 s38, s56, s60
	s_addc_u32 s39, s57, s61
	s_add_u32 s68, s38, 0x100
	s_addc_u32 s69, s39, 0
	s_add_u32 s62, s76, s60
	s_addc_u32 s63, s77, s61
	s_cmpk_eq_i32 s60, 0x700
	s_cselect_b64 s[64:65], -1, 0
	s_waitcnt lgkmcnt(0)
	s_and_b64 s[38:39], s[64:65], exec
	s_cselect_b32 s63, s49, s63
	s_cselect_b32 s62, s82, s62
	s_cselect_b32 s69, s3, s69
	s_cselect_b32 s68, s51, s68
	s_barrier
	s_setprio 1
	s_waitcnt lgkmcnt(0)
	v_mfma_i32_16x16x64_i8 v[128:131], v[148:151], v[188:191], v[128:131]
	v_mfma_i32_16x16x64_i8 v[124:127], v[156:159], v[188:191], v[124:127]
	v_mfma_i32_16x16x64_i8 v[120:123], v[148:151], v[180:183], v[120:123]
	v_mfma_i32_16x16x64_i8 v[116:119], v[156:159], v[180:183], v[116:119]
	v_mfma_i32_16x16x64_i8 v[112:115], v[148:151], v[172:175], v[112:115]
	v_mfma_i32_16x16x64_i8 v[108:111], v[156:159], v[172:175], v[108:111]
	v_mfma_i32_16x16x64_i8 v[104:107], v[148:151], v[164:167], v[104:107]
	v_mfma_i32_16x16x64_i8 v[100:103], v[156:159], v[164:167], v[100:103]
	v_mfma_i32_16x16x64_i8 v[128:131], v[152:155], v[192:195], v[128:131]
	v_mfma_i32_16x16x64_i8 v[124:127], v[160:163], v[192:195], v[124:127]
	v_mfma_i32_16x16x64_i8 v[120:123], v[152:155], v[184:187], v[120:123]
	v_mfma_i32_16x16x64_i8 v[116:119], v[160:163], v[184:187], v[116:119]
	v_mfma_i32_16x16x64_i8 v[112:115], v[152:155], v[176:179], v[112:115]
	v_mfma_i32_16x16x64_i8 v[108:111], v[160:163], v[176:179], v[108:111]
	v_mfma_i32_16x16x64_i8 v[104:107], v[152:155], v[168:171], v[104:107]
	v_mfma_i32_16x16x64_i8 v[100:103], v[160:163], v[168:171], v[100:103]
	v_mfma_i32_16x16x64_i8 v[72:75], v[132:135], v[188:191], v[72:75]
	v_mfma_i32_16x16x64_i8 v[68:71], v[140:143], v[188:191], v[68:71]
	v_mfma_i32_16x16x64_i8 v[64:67], v[132:135], v[180:183], v[64:67]
	v_mfma_i32_16x16x64_i8 v[60:63], v[140:143], v[180:183], v[60:63]
	v_mfma_i32_16x16x64_i8 v[56:59], v[132:135], v[172:175], v[56:59]
	v_mfma_i32_16x16x64_i8 v[52:55], v[140:143], v[172:175], v[52:55]
	v_mfma_i32_16x16x64_i8 v[48:51], v[132:135], v[164:167], v[48:51]
	v_mfma_i32_16x16x64_i8 v[44:47], v[140:143], v[164:167], v[44:47]
	v_mfma_i32_16x16x64_i8 v[72:75], v[136:139], v[192:195], v[72:75]
	v_mfma_i32_16x16x64_i8 v[68:71], v[144:147], v[192:195], v[68:71]
	v_mfma_i32_16x16x64_i8 v[64:67], v[136:139], v[184:187], v[64:67]
	v_mfma_i32_16x16x64_i8 v[60:63], v[144:147], v[184:187], v[60:63]
	v_mfma_i32_16x16x64_i8 v[56:59], v[136:139], v[176:179], v[56:59]
	v_mfma_i32_16x16x64_i8 v[52:55], v[144:147], v[176:179], v[52:55]
	v_mfma_i32_16x16x64_i8 v[48:51], v[136:139], v[168:171], v[48:51]
	v_mfma_i32_16x16x64_i8 v[44:47], v[144:147], v[168:171], v[44:47]
	s_setprio 0
	s_barrier
	s_mov_b32 m0, s18
	v_lshl_add_u64 v[218:219], s[62:63], 0, v[2:3]
	s_add_u32 s38, s62, 0x40000
	ds_read_b128 v[188:191], v230 offset:16384
	ds_read_b128 v[192:195], v230 offset:17408
	ds_read_b128 v[180:183], v230 offset:18432
	ds_read_b128 v[184:187], v230 offset:19456
	ds_read_b128 v[172:175], v230 offset:20480
	ds_read_b128 v[176:179], v230 offset:21504
	ds_read_b128 v[164:167], v230 offset:22528
	ds_read_b128 v[168:171], v230 offset:23552
	global_load_lds_dwordx4 v[218:219], off
	v_lshl_add_u64 v[220:221], s[62:63], 0, v[196:197]
	s_mov_b32 m0, s19
	s_addc_u32 s39, s63, 0
	global_load_lds_dwordx4 v[220:221], off
	v_lshl_add_u64 v[222:223], s[38:39], 0, v[2:3]
	s_mov_b32 m0, s16
	v_lshl_add_u64 v[224:225], s[68:69], 0, v[202:203]
	global_load_lds_dwordx4 v[222:223], off
	v_lshl_add_u64 v[222:223], s[38:39], 0, v[196:197]
	s_mov_b32 m0, s90
	v_cndmask_b32_e64 v231, 0, 1, s[74:75]
	global_load_lds_dwordx4 v[222:223], off
	v_lshl_add_u64 v[222:223], s[68:69], 0, v[204:205]
	s_mov_b32 m0, s81
	v_cmp_ne_u32_e64 s[38:39], 1, v231
	global_load_lds_dwordx4 v[222:223], off
	s_mov_b32 m0, s72
	s_andn2_b64 vcc, exec, s[74:75]
	global_load_lds_dwordx4 v[224:225], off
	s_cbranch_vccnz .LBB0_166
	s_waitcnt vmcnt(24)
	s_cbranch_execnz .LBB0_160

; #define PG8_STAGE(bufoff, gbase, voff) do { _Pragma("unroll") for (int _i = 0; _i < 2; ++_i) \
;         __builtin_amdgcn_global_load_lds((const unsigned*)((const char*)(gbase) + (voff)[_i]), (PG8_LAS unsigned*)(lds + (bufoff) + ldsw + _i * 8192), 16, 0, 0); } while (0)
; #define PG8_LDA(dst, b, h) do { _Pragma("unroll") for (int m = 0; m < 4; ++m) _Pragma("unroll") for (int k = 0; k < 2; ++k) dst[m][k] = *(const PG8_LAS bf16x8*)(lds + PG8_SA(b, h) + aoff + m * 2048 + k * 1024); } while (0)
; #define PG8_LDB(dst, b, h) do { _Pragma("unroll") for (int n = 0; n < 2; ++n) _Pragma("unroll") for (int k = 0; k < 2; ++k) dst[n][k] = *(const PG8_LAS bf16x8*)(lds + PG8_SB(b, h) + boff + n * 2048 + k * 1024); } while (0)
; #define PG8_MMA(ai, bj, At, Bt) do { __builtin_amdgcn_s_setprio(1); _Pragma("unroll") for (int m = 0; m < 4; ++m) _Pragma("unroll") for (int n = 0; n < 2; ++n) _Pragma("unroll") for (int k = 0; k < 2; ++k) \
;         acc[ai][bj][m][n] = mma16(Bt[n][k], At[m][k], acc[ai][bj][m][n]); __builtin_amdgcn_s_setprio(0); } while (0)
; #define PG8_WAIT_V(n) asm volatile("s_waitcnt vmcnt(" #n ")" ::: "memory")
; #define PG8_WAIT_VN(n) asm volatile("s_waitcnt vmcnt(%0)" :: "n"(n) : "memory")
; #define PG8_WAIT_L(n) asm volatile("s_waitcnt lgkmcnt(" #n ")" ::: "memory")
; #define PG8_BAR __builtin_amdgcn_s_barrier()
; #define PG8_SCHED __builtin_amdgcn_sched_barrier(0)
; template <class Epi, class Sched, bool ALIGN_EPI = false, bool SP2 = false>
; __device__ __forceinline__ void gemm_phase(PG8_LAS unsigned char* lds, const Gemm g, const Sched& S, const Epi& E, Stopwatch& sw) {
;     ...
;             if (relax) PG8_WAIT_VN(8 + Epi::NST); else PG8_WAIT_V(8); PG8_WAIT_L(0); PG8_BAR; PG8_MMA(1, 0, At, B0); PG8_MMA(1, 1, At, B1); PG8_BAR; PG8_SCHED;
;             PG8_LDB(B0, 1, 0); PG8_LDB(B1, 1, 1); PG8_SCHED; PG8_LDA(At, 1, 0); PG8_STAGE(PG8_SA(0, 1), a2 + hstep, voffA);
;             if (relax) PG8_WAIT_VN(8 + Epi::NST); else PG8_WAIT_V(8); PG8_WAIT_L(0); PG8_BAR; PG8_MMA(0, 0, At, B0); PG8_MMA(0, 1, At, B1); PG8_BAR; PG8_SCHED;
.LBB0_160:
	s_waitcnt lgkmcnt(0)
	s_barrier
	s_setprio 1
	s_waitcnt lgkmcnt(0)
	v_mfma_i32_16x16x64_i8 v[96:99], v[148:151], v[188:191], v[96:99]
	v_mfma_i32_16x16x64_i8 v[92:95], v[156:159], v[188:191], v[92:95]
	v_mfma_i32_16x16x64_i8 v[88:91], v[148:151], v[180:183], v[88:91]
	v_mfma_i32_16x16x64_i8 v[84:87], v[156:159], v[180:183], v[84:87]
	v_mfma_i32_16x16x64_i8 v[80:83], v[148:151], v[172:175], v[80:83]
	v_mfma_i32_16x16x64_i8 v[76:79], v[156:159], v[172:175], v[76:79]
	v_mfma_i32_16x16x64_i8 v[40:43], v[148:151], v[164:167], v[40:43]
	v_mfma_i32_16x16x64_i8 v[36:39], v[156:159], v[164:167], v[36:39]
	v_mfma_i32_16x16x64_i8 v[96:99], v[152:155], v[192:195], v[96:99]
	v_mfma_i32_16x16x64_i8 v[92:95], v[160:163], v[192:195], v[92:95]
	v_mfma_i32_16x16x64_i8 v[88:91], v[152:155], v[184:187], v[88:91]
	v_mfma_i32_16x16x64_i8 v[84:87], v[160:163], v[184:187], v[84:87]
	v_mfma_i32_16x16x64_i8 v[80:83], v[152:155], v[176:179], v[80:83]
	v_mfma_i32_16x16x64_i8 v[76:79], v[160:163], v[176:179], v[76:79]
	v_mfma_i32_16x16x64_i8 v[40:43], v[152:155], v[168:171], v[40:43]
	v_mfma_i32_16x16x64_i8 v[36:39], v[160:163], v[168:171], v[36:39]
	v_mfma_i32_16x16x64_i8 v[32:35], v[132:135], v[188:191], v[32:35]
	v_mfma_i32_16x16x64_i8 v[28:31], v[140:143], v[188:191], v[28:31]
	v_mfma_i32_16x16x64_i8 v[24:27], v[132:135], v[180:183], v[24:27]
	v_mfma_i32_16x16x64_i8 v[20:23], v[140:143], v[180:183], v[20:23]
	v_mfma_i32_16x16x64_i8 v[16:19], v[132:135], v[172:175], v[16:19]
	v_mfma_i32_16x16x64_i8 v[12:15], v[140:143], v[172:175], v[12:15]
	v_mfma_i32_16x16x64_i8 v[8:11], v[132:135], v[164:167], v[8:11]
	v_mfma_i32_16x16x64_i8 v[4:7], v[140:143], v[164:167], v[4:7]
	v_mfma_i32_16x16x64_i8 v[32:35], v[136:139], v[192:195], v[32:35]
	v_mfma_i32_16x16x64_i8 v[28:31], v[144:147], v[192:195], v[28:31]
	v_mfma_i32_16x16x64_i8 v[24:27], v[136:139], v[184:187], v[24:27]
	v_mfma_i32_16x16x64_i8 v[20:23], v[144:147], v[184:187], v[20:23]
	v_mfma_i32_16x16x64_i8 v[16:19], v[136:139], v[176:179], v[16:19]
	v_mfma_i32_16x16x64_i8 v[12:15], v[144:147], v[176:179], v[12:15]
	v_mfma_i32_16x16x64_i8 v[8:11], v[136:139], v[168:171], v[8:11]
	v_mfma_i32_16x16x64_i8 v[4:7], v[144:147], v[168:171], v[4:7]
	s_setprio 0
	s_barrier
	v_add_u32_e32 v132, 0x18000, v227
	v_add_u32_e32 v144, 0x1c000, v227
	ds_read_b128 v[148:151], v132
	ds_read_b128 v[152:155], v132 offset:1024
	ds_read_b128 v[156:159], v132 offset:2048
	ds_read_b128 v[160:163], v132 offset:3072
	ds_read_b128 v[132:135], v144
	ds_read_b128 v[136:139], v144 offset:1024
	ds_read_b128 v[140:143], v144 offset:2048
	ds_read_b128 v[144:147], v144 offset:3072
	s_add_u32 s68, s68, 0x40000
	s_addc_u32 s69, s69, 0
	s_mov_b32 m0, s73
	v_lshl_add_u64 v[232:233], s[68:69], 0, v[204:205]
	ds_read_b128 v[188:191], v230 offset:32768
	ds_read_b128 v[192:195], v230 offset:33792
	ds_read_b128 v[180:183], v230 offset:34816
	ds_read_b128 v[184:187], v230 offset:35840
	ds_read_b128 v[172:175], v230 offset:36864
	ds_read_b128 v[176:179], v230 offset:37888
	ds_read_b128 v[164:167], v230 offset:38912
	ds_read_b128 v[168:171], v230 offset:39936
	global_load_lds_dwordx4 v[232:233], off
	v_lshl_add_u64 v[232:233], s[68:69], 0, v[202:203]
	s_mov_b32 m0, s4
	s_and_b64 vcc, exec, s[38:39]
	global_load_lds_dwordx4 v[232:233], off
	s_mov_b64 s[74:75], s[10:11]
	s_cbranch_vccnz .LBB0_167
	s_waitcnt vmcnt(24)
	s_cbranch_execnz .LBB0_163

; #define PG8_STAGE(bufoff, gbase, voff) do { _Pragma("unroll") for (int _i = 0; _i < 2; ++_i) \
;         __builtin_amdgcn_global_load_lds((const unsigned*)((const char*)(gbase) + (voff)[_i]), (PG8_LAS unsigned*)(lds + (bufoff) + ldsw + _i * 8192), 16, 0, 0); } while (0)
; #define PG8_LDA(dst, b, h) do { _Pragma("unroll") for (int m = 0; m < 4; ++m) _Pragma("unroll") for (int k = 0; k < 2; ++k) dst[m][k] = *(const PG8_LAS bf16x8*)(lds + PG8_SA(b, h) + aoff + m * 2048 + k * 1024); } while (0)
; #define PG8_MMA(ai, bj, At, Bt) do { __builtin_amdgcn_s_setprio(1); _Pragma("unroll") for (int m = 0; m < 4; ++m) _Pragma("unroll") for (int n = 0; n < 2; ++n) _Pragma("unroll") for (int k = 0; k < 2; ++k) \
;         acc[ai][bj][m][n] = mma16(Bt[n][k], At[m][k], acc[ai][bj][m][n]); __builtin_amdgcn_s_setprio(0); } while (0)
; #define PG8_WAIT_V(n) asm volatile("s_waitcnt vmcnt(" #n ")" ::: "memory")
; #define PG8_WAIT_VN(n) asm volatile("s_waitcnt vmcnt(%0)" :: "n"(n) : "memory")
; #define PG8_WAIT_L(n) asm volatile("s_waitcnt lgkmcnt(" #n ")" ::: "memory")
; #define PG8_BAR __builtin_amdgcn_s_barrier()
; #define PG8_SCHED __builtin_amdgcn_sched_barrier(0)
; template <class Epi, class Sched, bool ALIGN_EPI = false, bool SP2 = false>
; __device__ __forceinline__ void gemm_phase(PG8_LAS unsigned char* lds, const Gemm g, const Sched& S, const Epi& E, Stopwatch& sw) {
;     ...
;             if (relax) PG8_WAIT_VN(8 + Epi::NST); else PG8_WAIT_V(8); PG8_WAIT_L(0); PG8_BAR; PG8_MMA(0, 0, At, B0); PG8_MMA(0, 1, At, B1); PG8_BAR; PG8_SCHED;
;             PG8_LDA(At, 1, 1); PG8_STAGE(PG8_SB(1, 0), b3, voffB); PG8_STAGE(PG8_SB(1, 1), b3 + hstep, voffB); PG8_STAGE(PG8_SA(1, 0), a3, voffA);
;             PG8_WAIT_V(8); PG8_WAIT_L(0); PG8_BAR; PG8_MMA(1, 0, At, B0); PG8_MMA(1, 1, At, B1); PG8_BAR; PG8_SCHED;
;             if (last && has_next) PG8_STAGE(PG8_SA(1, 1), a3 + hstep, voffA);
.LBB0_163:
	s_waitcnt lgkmcnt(0)
	s_and_b64 s[38:39], s[36:37], s[64:65]
	s_barrier
	s_setprio 1
	s_waitcnt lgkmcnt(0)
	v_mfma_i32_16x16x64_i8 v[128:131], v[148:151], v[188:191], v[128:131]
	v_mfma_i32_16x16x64_i8 v[124:127], v[156:159], v[188:191], v[124:127]
	v_mfma_i32_16x16x64_i8 v[120:123], v[148:151], v[180:183], v[120:123]
	v_mfma_i32_16x16x64_i8 v[116:119], v[156:159], v[180:183], v[116:119]
	v_mfma_i32_16x16x64_i8 v[112:115], v[148:151], v[172:175], v[112:115]
	v_mfma_i32_16x16x64_i8 v[108:111], v[156:159], v[172:175], v[108:111]
	v_mfma_i32_16x16x64_i8 v[104:107], v[148:151], v[164:167], v[104:107]
	v_mfma_i32_16x16x64_i8 v[100:103], v[156:159], v[164:167], v[100:103]
	v_mfma_i32_16x16x64_i8 v[128:131], v[152:155], v[192:195], v[128:131]
	v_mfma_i32_16x16x64_i8 v[124:127], v[160:163], v[192:195], v[124:127]
	v_mfma_i32_16x16x64_i8 v[120:123], v[152:155], v[184:187], v[120:123]
	v_mfma_i32_16x16x64_i8 v[116:119], v[160:163], v[184:187], v[116:119]
	v_mfma_i32_16x16x64_i8 v[112:115], v[152:155], v[176:179], v[112:115]
	v_mfma_i32_16x16x64_i8 v[108:111], v[160:163], v[176:179], v[108:111]
	v_mfma_i32_16x16x64_i8 v[104:107], v[152:155], v[168:171], v[104:107]
	v_mfma_i32_16x16x64_i8 v[100:103], v[160:163], v[168:171], v[100:103]
	v_mfma_i32_16x16x64_i8 v[72:75], v[132:135], v[188:191], v[72:75]
	v_mfma_i32_16x16x64_i8 v[68:71], v[140:143], v[188:191], v[68:71]
	v_mfma_i32_16x16x64_i8 v[64:67], v[132:135], v[180:183], v[64:67]
	v_mfma_i32_16x16x64_i8 v[60:63], v[140:143], v[180:183], v[60:63]
	v_mfma_i32_16x16x64_i8 v[56:59], v[132:135], v[172:175], v[56:59]
	v_mfma_i32_16x16x64_i8 v[52:55], v[140:143], v[172:175], v[52:55]
	v_mfma_i32_16x16x64_i8 v[48:51], v[132:135], v[164:167], v[48:51]
	v_mfma_i32_16x16x64_i8 v[44:47], v[140:143], v[164:167], v[44:47]
	v_mfma_i32_16x16x64_i8 v[72:75], v[136:139], v[192:195], v[72:75]
	v_mfma_i32_16x16x64_i8 v[68:71], v[144:147], v[192:195], v[68:71]
	v_mfma_i32_16x16x64_i8 v[64:67], v[136:139], v[184:187], v[64:67]
	v_mfma_i32_16x16x64_i8 v[60:63], v[144:147], v[184:187], v[60:63]
	v_mfma_i32_16x16x64_i8 v[56:59], v[136:139], v[176:179], v[56:59]
	v_mfma_i32_16x16x64_i8 v[52:55], v[144:147], v[176:179], v[52:55]
	v_mfma_i32_16x16x64_i8 v[48:51], v[136:139], v[168:171], v[48:51]
	v_mfma_i32_16x16x64_i8 v[44:47], v[144:147], v[168:171], v[44:47]
	s_setprio 0
	s_barrier
	s_mov_b32 m0, s5
	v_lshl_add_u64 v[218:219], v[218:219], 0, s[20:21]
	s_add_u32 s62, s62, 0x40080
	ds_read_b128 v[164:167], v230 offset:49152
	ds_read_b128 v[168:171], v230 offset:50176
	ds_read_b128 v[172:175], v230 offset:51200
	ds_read_b128 v[176:179], v230 offset:52224
	ds_read_b128 v[180:183], v230 offset:53248
	ds_read_b128 v[184:187], v230 offset:54272
	ds_read_b128 v[188:191], v230 offset:55296
	ds_read_b128 v[192:195], v230 offset:56320
	global_load_lds_dwordx4 v[218:219], off
	v_lshl_add_u64 v[218:219], v[220:221], 0, s[20:21]
	s_mov_b32 m0, s34
	s_addc_u32 s63, s63, 0
	global_load_lds_dwordx4 v[218:219], off
	v_lshl_add_u64 v[218:219], s[62:63], 0, v[2:3]
	s_mov_b32 m0, s25
	s_nop 0
	global_load_lds_dwordx4 v[218:219], off
	v_lshl_add_u64 v[218:219], s[62:63], 0, v[196:197]
	s_mov_b32 m0, s94
	s_nop 0
	global_load_lds_dwordx4 v[218:219], off
	v_lshl_add_u64 v[218:219], v[222:223], 0, s[20:21]
	s_mov_b32 m0, s40
	s_nop 0
	global_load_lds_dwordx4 v[218:219], off
	v_lshl_add_u64 v[218:219], v[224:225], 0, s[20:21]
	s_mov_b32 m0, s41
	s_nop 0
	global_load_lds_dwordx4 v[218:219], off
	s_waitcnt vmcnt(8)
	s_waitcnt lgkmcnt(0)
	s_barrier
	s_setprio 1
	s_waitcnt lgkmcnt(0)
	v_mfma_i32_16x16x64_i8 v[96:99], v[148:151], v[164:167], v[96:99]
	v_mfma_i32_16x16x64_i8 v[92:95], v[156:159], v[164:167], v[92:95]
	v_mfma_i32_16x16x64_i8 v[88:91], v[148:151], v[172:175], v[88:91]
	v_mfma_i32_16x16x64_i8 v[84:87], v[156:159], v[172:175], v[84:87]
	v_mfma_i32_16x16x64_i8 v[80:83], v[148:151], v[180:183], v[80:83]
	v_mfma_i32_16x16x64_i8 v[76:79], v[156:159], v[180:183], v[76:79]
	v_mfma_i32_16x16x64_i8 v[40:43], v[148:151], v[188:191], v[40:43]
	v_mfma_i32_16x16x64_i8 v[36:39], v[156:159], v[188:191], v[36:39]
	v_mfma_i32_16x16x64_i8 v[96:99], v[152:155], v[168:171], v[96:99]
	v_mfma_i32_16x16x64_i8 v[92:95], v[160:163], v[168:171], v[92:95]
	v_mfma_i32_16x16x64_i8 v[88:91], v[152:155], v[176:179], v[88:91]
	v_mfma_i32_16x16x64_i8 v[84:87], v[160:163], v[176:179], v[84:87]
	v_mfma_i32_16x16x64_i8 v[80:83], v[152:155], v[184:187], v[80:83]
	v_mfma_i32_16x16x64_i8 v[76:79], v[160:163], v[184:187], v[76:79]
	v_mfma_i32_16x16x64_i8 v[40:43], v[152:155], v[192:195], v[40:43]
	v_mfma_i32_16x16x64_i8 v[36:39], v[160:163], v[192:195], v[36:39]
	v_mfma_i32_16x16x64_i8 v[32:35], v[132:135], v[164:167], v[32:35]
	v_mfma_i32_16x16x64_i8 v[28:31], v[140:143], v[164:167], v[28:31]
	v_mfma_i32_16x16x64_i8 v[24:27], v[132:135], v[172:175], v[24:27]
	v_mfma_i32_16x16x64_i8 v[20:23], v[140:143], v[172:175], v[20:23]
	v_mfma_i32_16x16x64_i8 v[16:19], v[132:135], v[180:183], v[16:19]
	v_mfma_i32_16x16x64_i8 v[12:15], v[140:143], v[180:183], v[12:15]
	v_mfma_i32_16x16x64_i8 v[8:11], v[132:135], v[188:191], v[8:11]
	v_mfma_i32_16x16x64_i8 v[4:7], v[140:143], v[188:191], v[4:7]
	v_mfma_i32_16x16x64_i8 v[32:35], v[136:139], v[168:171], v[32:35]
	v_mfma_i32_16x16x64_i8 v[28:31], v[144:147], v[168:171], v[28:31]
	v_mfma_i32_16x16x64_i8 v[24:27], v[136:139], v[176:179], v[24:27]
	v_mfma_i32_16x16x64_i8 v[20:23], v[144:147], v[176:179], v[20:23]
	v_mfma_i32_16x16x64_i8 v[16:19], v[136:139], v[184:187], v[16:19]
	v_mfma_i32_16x16x64_i8 v[12:15], v[144:147], v[184:187], v[12:15]
	v_mfma_i32_16x16x64_i8 v[8:11], v[136:139], v[192:195], v[8:11]
	v_mfma_i32_16x16x64_i8 v[4:7], v[144:147], v[192:195], v[4:7]
	s_setprio 0
	s_barrier
	s_andn2_b64 vcc, exec, s[38:39]
	s_cbranch_vccnz .LBB0_153
	s_add_i32 m0, s81, 0xc000
	s_nop 0
	global_load_lds_dwordx4 v[210:211], off
	s_add_i32 m0, s81, 0xe000
	s_nop 0
	global_load_lds_dwordx4 v[212:213], off
	s_branch .LBB0_153

; #define PG8_STAGE(bufoff, gbase, voff) do { _Pragma("unroll") for (int _i = 0; _i < 2; ++_i) \
;         __builtin_amdgcn_global_load_lds((const unsigned*)((const char*)(gbase) + (voff)[_i]), (PG8_LAS unsigned*)(lds + (bufoff) + ldsw + _i * 8192), 16, 0, 0); } while (0)
; #define PG8_LDA(dst, b, h) do { _Pragma("unroll") for (int m = 0; m < 4; ++m) _Pragma("unroll") for (int k = 0; k < 2; ++k) dst[m][k] = *(const PG8_LAS bf16x8*)(lds + PG8_SA(b, h) + aoff + m * 2048 + k * 1024); } while (0)
; #define PG8_LDB(dst, b, h) do { _Pragma("unroll") for (int n = 0; n < 2; ++n) _Pragma("unroll") for (int k = 0; k < 2; ++k) dst[n][k] = *(const PG8_LAS bf16x8*)(lds + PG8_SB(b, h) + boff + n * 2048 + k * 1024); } while (0)
; #define PG8_MMA(ai, bj, At, Bt) do { __builtin_amdgcn_s_setprio(1); _Pragma("unroll") for (int m = 0; m < 4; ++m) _Pragma("unroll") for (int n = 0; n < 2; ++n) _Pragma("unroll") for (int k = 0; k < 2; ++k) \
;         acc[ai][bj][m][n] = mma16(Bt[n][k], At[m][k], acc[ai][bj][m][n]); __builtin_amdgcn_s_setprio(0); } while (0)
; template <class Epi, class Sched, bool ALIGN_EPI = false, bool SP2 = false>
; __device__ __forceinline__ void gemm_phase(PG8_LAS unsigned char* lds, const Gemm g, const Sched& S, const Epi& E, Stopwatch& sw) {
;     ...
;             const bool last = (t == nt - 2);
;             const char* a1 = cA + (size_t)(t + 1) * kstep;
;             const char* a2 = last ? nA : cA + (size_t)(t + 2) * kstep; const char* b2 = last ? nB : cB + (size_t)(t + 2) * kstep;
;             const char* a3 = a2 + kstep; const char* b3 = b2 + kstep;
;             if (last && has_next) S.a_ready(nxt);
;             if constexpr (SP2) {
;             int relax = __builtin_amdgcn_readfirstlane((int)((ui > 0) && (t == 0))); asm volatile("" : "+s"(relax));
;             PG8_LDB(B0, 0, 0); PG8_LDB(B1, 0, 1); PG8_SCHED; PG8_LDA(At, 0, 0); if (!relax) PG8_STAGE(PG8_SA(1, 1), a1 + hstep, voffA);
;             if (relax) PG8_WAIT_VN(8 + Epi::NST); else PG8_WAIT_V(8); PG8_WAIT_L(0); PG8_BAR; PG8_MMA(0, 0, At, B0); PG8_MMA(0, 1, At, B1); PG8_BAR; PG8_SCHED;
;             PG8_LDA(At, 0, 1); PG8_STAGE(PG8_SB(0, 0), b2, voffB); PG8_STAGE(PG8_SB(0, 1), b2 + hstep, voffB); PG8_STAGE(PG8_SA(0, 0), a2, voffA);
;             if (relax) PG8_WAIT_VN(8 + Epi::NST); else PG8_WAIT_V(8); PG8_WAIT_L(0); PG8_BAR; PG8_MMA(1, 0, At, B0); PG8_MMA(1, 1, At, B1); PG8_BAR; PG8_SCHED;
.LBB0_780:
	s_add_u32 s0, s54, s58
	s_addc_u32 s3, s55, s59
	s_add_u32 s0, s0, 0x100
	s_addc_u32 s3, s3, 0
	s_add_u32 s34, s24, s58
	s_addc_u32 s60, s83, s59
	s_cmpk_eq_i32 s58, 0x1700
	s_cselect_b64 s[62:63], -1, 0
	s_waitcnt lgkmcnt(0)
	s_and_b64 s[42:43], s[62:63], exec
	s_cselect_b32 s61, s53, s60
	s_cselect_b32 s60, s52, s34
	s_cselect_b32 s65, s51, s3
	s_cselect_b32 s64, s50, s0
	s_barrier
	s_setprio 1
	s_waitcnt lgkmcnt(0)
	v_mfma_f32_16x16x32_bf16 v[130:133], v[150:153], v[190:193], v[130:133]
	v_mfma_f32_16x16x32_bf16 v[126:129], v[158:161], v[190:193], v[126:129]
	v_mfma_f32_16x16x32_bf16 v[114:117], v[150:153], v[182:185], v[114:117]
	v_mfma_f32_16x16x32_bf16 v[110:113], v[158:161], v[182:185], v[110:113]
	v_mfma_f32_16x16x32_bf16 v[98:101], v[150:153], v[174:177], v[98:101]
	v_mfma_f32_16x16x32_bf16 v[94:97], v[158:161], v[174:177], v[94:97]
	v_mfma_f32_16x16x32_bf16 v[82:85], v[150:153], v[166:169], v[82:85]
	v_mfma_f32_16x16x32_bf16 v[78:81], v[158:161], v[166:169], v[78:81]
	v_mfma_f32_16x16x32_bf16 v[130:133], v[154:157], v[194:197], v[130:133]
	v_mfma_f32_16x16x32_bf16 v[126:129], v[162:165], v[194:197], v[126:129]
	v_mfma_f32_16x16x32_bf16 v[114:117], v[154:157], v[186:189], v[114:117]
	v_mfma_f32_16x16x32_bf16 v[110:113], v[162:165], v[186:189], v[110:113]
	v_mfma_f32_16x16x32_bf16 v[98:101], v[154:157], v[178:181], v[98:101]
	v_mfma_f32_16x16x32_bf16 v[94:97], v[162:165], v[178:181], v[94:97]
	v_mfma_f32_16x16x32_bf16 v[82:85], v[154:157], v[170:173], v[82:85]
	v_mfma_f32_16x16x32_bf16 v[78:81], v[162:165], v[170:173], v[78:81]
	v_mfma_f32_16x16x32_bf16 v[122:125], v[134:137], v[190:193], v[122:125]
	v_mfma_f32_16x16x32_bf16 v[118:121], v[142:145], v[190:193], v[118:121]
	v_mfma_f32_16x16x32_bf16 v[106:109], v[134:137], v[182:185], v[106:109]
	v_mfma_f32_16x16x32_bf16 v[102:105], v[142:145], v[182:185], v[102:105]
	v_mfma_f32_16x16x32_bf16 v[90:93], v[134:137], v[174:177], v[90:93]
	v_mfma_f32_16x16x32_bf16 v[86:89], v[142:145], v[174:177], v[86:89]
	v_mfma_f32_16x16x32_bf16 v[74:77], v[134:137], v[166:169], v[74:77]
	v_mfma_f32_16x16x32_bf16 v[70:73], v[142:145], v[166:169], v[70:73]
	v_mfma_f32_16x16x32_bf16 v[122:125], v[138:141], v[194:197], v[122:125]
	v_mfma_f32_16x16x32_bf16 v[118:121], v[146:149], v[194:197], v[118:121]
	v_mfma_f32_16x16x32_bf16 v[106:109], v[138:141], v[186:189], v[106:109]
	v_mfma_f32_16x16x32_bf16 v[102:105], v[146:149], v[186:189], v[102:105]
	v_mfma_f32_16x16x32_bf16 v[90:93], v[138:141], v[178:181], v[90:93]
	v_mfma_f32_16x16x32_bf16 v[86:89], v[146:149], v[178:181], v[86:89]
	v_mfma_f32_16x16x32_bf16 v[74:77], v[138:141], v[170:173], v[74:77]
	v_mfma_f32_16x16x32_bf16 v[70:73], v[146:149], v[170:173], v[70:73]
	s_setprio 0
	s_barrier
	s_mov_b32 m0, s19
	v_lshl_add_u64 v[230:231], s[60:61], 0, v[206:207]
	s_add_u32 s42, s60, 0xc0000
	ds_read_b128 v[190:193], v249 offset:16384
	ds_read_b128 v[194:197], v249 offset:17408
	ds_read_b128 v[182:185], v249 offset:18432
	ds_read_b128 v[186:189], v249 offset:19456
	ds_read_b128 v[174:177], v249 offset:20480
	ds_read_b128 v[178:181], v249 offset:21504
	ds_read_b128 v[166:169], v249 offset:22528
	ds_read_b128 v[170:173], v249 offset:23552
	global_load_lds_dwordx4 v[230:231], off
	v_lshl_add_u64 v[232:233], s[60:61], 0, v[202:203]
	s_mov_b32 m0, s25
	s_addc_u32 s43, s61, 0
	global_load_lds_dwordx4 v[232:233], off
	v_lshl_add_u64 v[4:5], s[42:43], 0, v[206:207]
	s_mov_b32 m0, s72
	v_lshl_add_u64 v[234:235], s[64:65], 0, v[208:209]
	global_load_lds_dwordx4 v[4:5], off
	v_lshl_add_u64 v[4:5], s[42:43], 0, v[202:203]
	s_mov_b32 m0, s73
	v_lshl_add_u64 v[236:237], s[64:65], 0, v[204:205]
	global_load_lds_dwordx4 v[4:5], off
	s_mov_b32 m0, s18
	v_cndmask_b32_e64 v2, 0, 1, s[68:69]
	global_load_lds_dwordx4 v[234:235], off
	s_mov_b32 m0, s74
	v_cmp_ne_u32_e64 s[42:43], 1, v2
	global_load_lds_dwordx4 v[236:237], off
	s_andn2_b64 vcc, exec, s[68:69]
	s_cbranch_vccnz .LBB0_792
	s_waitcnt vmcnt(24)
	s_cbranch_execnz .LBB0_783

; #define PG8_STAGE(bufoff, gbase, voff) do { _Pragma("unroll") for (int _i = 0; _i < 2; ++_i) \
;         __builtin_amdgcn_global_load_lds((const unsigned*)((const char*)(gbase) + (voff)[_i]), (PG8_LAS unsigned*)(lds + (bufoff) + ldsw + _i * 8192), 16, 0, 0); } while (0)
; #define PG8_LDA(dst, b, h) do { _Pragma("unroll") for (int m = 0; m < 4; ++m) _Pragma("unroll") for (int k = 0; k < 2; ++k) dst[m][k] = *(const PG8_LAS bf16x8*)(lds + PG8_SA(b, h) + aoff + m * 2048 + k * 1024); } while (0)
; #define PG8_LDB(dst, b, h) do { _Pragma("unroll") for (int n = 0; n < 2; ++n) _Pragma("unroll") for (int k = 0; k < 2; ++k) dst[n][k] = *(const PG8_LAS bf16x8*)(lds + PG8_SB(b, h) + boff + n * 2048 + k * 1024); } while (0)
; #define PG8_MMA(ai, bj, At, Bt) do { __builtin_amdgcn_s_setprio(1); _Pragma("unroll") for (int m = 0; m < 4; ++m) _Pragma("unroll") for (int n = 0; n < 2; ++n) _Pragma("unroll") for (int k = 0; k < 2; ++k) \
;         acc[ai][bj][m][n] = mma16(Bt[n][k], At[m][k], acc[ai][bj][m][n]); __builtin_amdgcn_s_setprio(0); } while (0)
; #define PG8_WAIT_V(n) asm volatile("s_waitcnt vmcnt(" #n ")" ::: "memory")
; #define PG8_WAIT_VN(n) asm volatile("s_waitcnt vmcnt(%0)" :: "n"(n) : "memory")
; #define PG8_WAIT_L(n) asm volatile("s_waitcnt lgkmcnt(" #n ")" ::: "memory")
; #define PG8_BAR __builtin_amdgcn_s_barrier()
; #define PG8_SCHED __builtin_amdgcn_sched_barrier(0)
; template <class Epi, class Sched, bool ALIGN_EPI = false, bool SP2 = false>
; __device__ __forceinline__ void gemm_phase(PG8_LAS unsigned char* lds, const Gemm g, const Sched& S, const Epi& E, Stopwatch& sw) {
;     ...
;             if (relax) PG8_WAIT_VN(8 + Epi::NST); else PG8_WAIT_V(8); PG8_WAIT_L(0); PG8_BAR; PG8_MMA(1, 0, At, B0); PG8_MMA(1, 1, At, B1); PG8_BAR; PG8_SCHED;
;             PG8_LDB(B0, 1, 0); PG8_LDB(B1, 1, 1); PG8_SCHED; PG8_LDA(At, 1, 0); PG8_STAGE(PG8_SA(0, 1), a2 + hstep, voffA);
;             if (relax) PG8_WAIT_VN(8 + Epi::NST); else PG8_WAIT_V(8); PG8_WAIT_L(0); PG8_BAR; PG8_MMA(0, 0, At, B0); PG8_MMA(0, 1, At, B1); PG8_BAR; PG8_SCHED;
.LBB0_783:
	s_waitcnt lgkmcnt(0)
	s_barrier
	s_setprio 1
	s_waitcnt lgkmcnt(0)
	v_mfma_f32_16x16x32_bf16 v[66:69], v[150:153], v[190:193], v[66:69]
	v_mfma_f32_16x16x32_bf16 v[62:65], v[158:161], v[190:193], v[62:65]
	v_mfma_f32_16x16x32_bf16 v[50:53], v[150:153], v[182:185], v[50:53]
	v_mfma_f32_16x16x32_bf16 v[46:49], v[158:161], v[182:185], v[46:49]
	v_mfma_f32_16x16x32_bf16 v[34:37], v[150:153], v[174:177], v[34:37]
	v_mfma_f32_16x16x32_bf16 v[30:33], v[158:161], v[174:177], v[30:33]
	v_mfma_f32_16x16x32_bf16 v[18:21], v[150:153], v[166:169], v[18:21]
	v_mfma_f32_16x16x32_bf16 v[14:17], v[158:161], v[166:169], v[14:17]
	v_mfma_f32_16x16x32_bf16 v[66:69], v[154:157], v[194:197], v[66:69]
	v_mfma_f32_16x16x32_bf16 v[62:65], v[162:165], v[194:197], v[62:65]
	v_mfma_f32_16x16x32_bf16 v[50:53], v[154:157], v[186:189], v[50:53]
	v_mfma_f32_16x16x32_bf16 v[46:49], v[162:165], v[186:189], v[46:49]
	v_mfma_f32_16x16x32_bf16 v[34:37], v[154:157], v[178:181], v[34:37]
	v_mfma_f32_16x16x32_bf16 v[30:33], v[162:165], v[178:181], v[30:33]
	v_mfma_f32_16x16x32_bf16 v[18:21], v[154:157], v[170:173], v[18:21]
	v_mfma_f32_16x16x32_bf16 v[14:17], v[162:165], v[170:173], v[14:17]
	v_mfma_f32_16x16x32_bf16 v[58:61], v[134:137], v[190:193], v[58:61]
	v_mfma_f32_16x16x32_bf16 v[54:57], v[142:145], v[190:193], v[54:57]
	v_mfma_f32_16x16x32_bf16 v[42:45], v[134:137], v[182:185], v[42:45]
	v_mfma_f32_16x16x32_bf16 v[38:41], v[142:145], v[182:185], v[38:41]
	v_mfma_f32_16x16x32_bf16 v[26:29], v[134:137], v[174:177], v[26:29]
	v_mfma_f32_16x16x32_bf16 v[22:25], v[142:145], v[174:177], v[22:25]
	v_mfma_f32_16x16x32_bf16 v[10:13], v[134:137], v[166:169], v[10:13]
	v_mfma_f32_16x16x32_bf16 v[4:7], v[142:145], v[166:169], v[6:9]
	v_mfma_f32_16x16x32_bf16 v[58:61], v[138:141], v[194:197], v[58:61]
	v_mfma_f32_16x16x32_bf16 v[54:57], v[146:149], v[194:197], v[54:57]
	v_mfma_f32_16x16x32_bf16 v[42:45], v[138:141], v[186:189], v[42:45]
	v_mfma_f32_16x16x32_bf16 v[38:41], v[146:149], v[186:189], v[38:41]
	v_mfma_f32_16x16x32_bf16 v[26:29], v[138:141], v[178:181], v[26:29]
	v_mfma_f32_16x16x32_bf16 v[22:25], v[146:149], v[178:181], v[22:25]
	v_mfma_f32_16x16x32_bf16 v[10:13], v[138:141], v[170:173], v[10:13]
	v_mfma_f32_16x16x32_bf16 v[4:7], v[146:149], v[170:173], v[4:7]
	s_setprio 0
	s_barrier
	v_add_u32_e32 v2, 0x18000, v248
	ds_read_b128 v[150:153], v2
	ds_read_b128 v[154:157], v2 offset:1024
	ds_read_b128 v[158:161], v2 offset:2048
	ds_read_b128 v[162:165], v2 offset:3072
	v_add_u32_e32 v2, 0x1c000, v248
	ds_read_b128 v[134:137], v2
	ds_read_b128 v[138:141], v2 offset:1024
	ds_read_b128 v[142:145], v2 offset:2048
	ds_read_b128 v[146:149], v2 offset:3072
	s_add_u32 s64, s64, 0xc0000
	s_addc_u32 s65, s65, 0
	s_mov_b32 m0, s75
	v_lshl_add_u64 v[8:9], s[64:65], 0, v[208:209]
	ds_read_b128 v[190:193], v249 offset:32768
	ds_read_b128 v[194:197], v249 offset:33792
	ds_read_b128 v[182:185], v249 offset:34816
	ds_read_b128 v[186:189], v249 offset:35840
	ds_read_b128 v[174:177], v249 offset:36864
	ds_read_b128 v[178:181], v249 offset:37888
	ds_read_b128 v[166:169], v249 offset:38912
	ds_read_b128 v[170:173], v249 offset:39936
	global_load_lds_dwordx4 v[8:9], off
	v_lshl_add_u64 v[8:9], s[64:65], 0, v[204:205]
	s_mov_b32 m0, s78
	s_and_b64 vcc, exec, s[42:43]
	global_load_lds_dwordx4 v[8:9], off
	s_cbranch_vccnz .LBB0_793
	s_waitcnt vmcnt(24)
	s_cbranch_execnz .LBB0_786

; #define PG8_STAGE(bufoff, gbase, voff) do { _Pragma("unroll") for (int _i = 0; _i < 2; ++_i) \
;         __builtin_amdgcn_global_load_lds((const unsigned*)((const char*)(gbase) + (voff)[_i]), (PG8_LAS unsigned*)(lds + (bufoff) + ldsw + _i * 8192), 16, 0, 0); } while (0)
; #define PG8_LDA(dst, b, h) do { _Pragma("unroll") for (int m = 0; m < 4; ++m) _Pragma("unroll") for (int k = 0; k < 2; ++k) dst[m][k] = *(const PG8_LAS bf16x8*)(lds + PG8_SA(b, h) + aoff + m * 2048 + k * 1024); } while (0)
; #define PG8_MMA(ai, bj, At, Bt) do { __builtin_amdgcn_s_setprio(1); _Pragma("unroll") for (int m = 0; m < 4; ++m) _Pragma("unroll") for (int n = 0; n < 2; ++n) _Pragma("unroll") for (int k = 0; k < 2; ++k) \
;         acc[ai][bj][m][n] = mma16(Bt[n][k], At[m][k], acc[ai][bj][m][n]); __builtin_amdgcn_s_setprio(0); } while (0)
; #define PG8_WAIT_V(n) asm volatile("s_waitcnt vmcnt(" #n ")" ::: "memory")
; #define PG8_WAIT_VN(n) asm volatile("s_waitcnt vmcnt(%0)" :: "n"(n) : "memory")
; #define PG8_WAIT_L(n) asm volatile("s_waitcnt lgkmcnt(" #n ")" ::: "memory")
; #define PG8_BAR __builtin_amdgcn_s_barrier()
; #define PG8_SCHED __builtin_amdgcn_sched_barrier(0)
; template <class Epi, class Sched, bool ALIGN_EPI = false, bool SP2 = false>
; __device__ __forceinline__ void gemm_phase(PG8_LAS unsigned char* lds, const Gemm g, const Sched& S, const Epi& E, Stopwatch& sw) {
;     ...
;             if (relax) PG8_WAIT_VN(8 + Epi::NST); else PG8_WAIT_V(8); PG8_WAIT_L(0); PG8_BAR; PG8_MMA(0, 0, At, B0); PG8_MMA(0, 1, At, B1); PG8_BAR; PG8_SCHED;
;             PG8_LDA(At, 1, 1); PG8_STAGE(PG8_SB(1, 0), b3, voffB); PG8_STAGE(PG8_SB(1, 1), b3 + hstep, voffB); PG8_STAGE(PG8_SA(1, 0), a3, voffA);
;             PG8_WAIT_V(8); PG8_WAIT_L(0); PG8_BAR; PG8_MMA(1, 0, At, B0); PG8_MMA(1, 1, At, B1); PG8_BAR; PG8_SCHED;
;             if (last && has_next) PG8_STAGE(PG8_SA(1, 1), a3 + hstep, voffA);
.LBB0_786:
	s_waitcnt lgkmcnt(0)
	s_and_b64 s[42:43], s[40:41], s[62:63]
	s_barrier
	s_setprio 1
	s_waitcnt lgkmcnt(0)
	v_mfma_f32_16x16x32_bf16 v[130:133], v[150:153], v[190:193], v[130:133]
	v_mfma_f32_16x16x32_bf16 v[126:129], v[158:161], v[190:193], v[126:129]
	v_mfma_f32_16x16x32_bf16 v[114:117], v[150:153], v[182:185], v[114:117]
	v_mfma_f32_16x16x32_bf16 v[110:113], v[158:161], v[182:185], v[110:113]
	v_mfma_f32_16x16x32_bf16 v[98:101], v[150:153], v[174:177], v[98:101]
	v_mfma_f32_16x16x32_bf16 v[94:97], v[158:161], v[174:177], v[94:97]
	v_mfma_f32_16x16x32_bf16 v[82:85], v[150:153], v[166:169], v[82:85]
	v_mfma_f32_16x16x32_bf16 v[78:81], v[158:161], v[166:169], v[78:81]
	v_mfma_f32_16x16x32_bf16 v[130:133], v[154:157], v[194:197], v[130:133]
	v_mfma_f32_16x16x32_bf16 v[126:129], v[162:165], v[194:197], v[126:129]
	v_mfma_f32_16x16x32_bf16 v[114:117], v[154:157], v[186:189], v[114:117]
	v_mfma_f32_16x16x32_bf16 v[110:113], v[162:165], v[186:189], v[110:113]
	v_mfma_f32_16x16x32_bf16 v[98:101], v[154:157], v[178:181], v[98:101]
	v_mfma_f32_16x16x32_bf16 v[94:97], v[162:165], v[178:181], v[94:97]
	v_mfma_f32_16x16x32_bf16 v[82:85], v[154:157], v[170:173], v[82:85]
	v_mfma_f32_16x16x32_bf16 v[78:81], v[162:165], v[170:173], v[78:81]
	v_mfma_f32_16x16x32_bf16 v[122:125], v[134:137], v[190:193], v[122:125]
	v_mfma_f32_16x16x32_bf16 v[118:121], v[142:145], v[190:193], v[118:121]
	v_mfma_f32_16x16x32_bf16 v[106:109], v[134:137], v[182:185], v[106:109]
	v_mfma_f32_16x16x32_bf16 v[102:105], v[142:145], v[182:185], v[102:105]
	v_mfma_f32_16x16x32_bf16 v[90:93], v[134:137], v[174:177], v[90:93]
	v_mfma_f32_16x16x32_bf16 v[86:89], v[142:145], v[174:177], v[86:89]
	v_mfma_f32_16x16x32_bf16 v[74:77], v[134:137], v[166:169], v[74:77]
	v_mfma_f32_16x16x32_bf16 v[70:73], v[142:145], v[166:169], v[70:73]
	v_mfma_f32_16x16x32_bf16 v[122:125], v[138:141], v[194:197], v[122:125]
	v_mfma_f32_16x16x32_bf16 v[118:121], v[146:149], v[194:197], v[118:121]
	v_mfma_f32_16x16x32_bf16 v[106:109], v[138:141], v[186:189], v[106:109]
	v_mfma_f32_16x16x32_bf16 v[102:105], v[146:149], v[186:189], v[102:105]
	v_mfma_f32_16x16x32_bf16 v[90:93], v[138:141], v[178:181], v[90:93]
	v_mfma_f32_16x16x32_bf16 v[86:89], v[146:149], v[178:181], v[86:89]
	v_mfma_f32_16x16x32_bf16 v[74:77], v[138:141], v[170:173], v[74:77]
	v_mfma_f32_16x16x32_bf16 v[70:73], v[146:149], v[170:173], v[70:73]
	s_setprio 0
	s_barrier
	s_mov_b32 m0, s79
	v_lshl_add_u64 v[8:9], v[230:231], 0, s[20:21]
	s_add_u32 s60, s60, 0xc0080
	ds_read_b128 v[166:169], v249 offset:49152
	ds_read_b128 v[170:173], v249 offset:50176
	ds_read_b128 v[174:177], v249 offset:51200
	ds_read_b128 v[178:181], v249 offset:52224
	ds_read_b128 v[182:185], v249 offset:53248
	ds_read_b128 v[186:189], v249 offset:54272
	ds_read_b128 v[190:193], v249 offset:55296
	ds_read_b128 v[194:197], v249 offset:56320
	global_load_lds_dwordx4 v[8:9], off
	v_lshl_add_u64 v[8:9], v[232:233], 0, s[20:21]
	s_mov_b32 m0, s80
	s_addc_u32 s61, s61, 0
	global_load_lds_dwordx4 v[8:9], off
	v_lshl_add_u64 v[8:9], s[60:61], 0, v[206:207]
	s_mov_b32 m0, s94
	s_nop 0
	global_load_lds_dwordx4 v[8:9], off
	v_lshl_add_u64 v[8:9], s[60:61], 0, v[202:203]
	s_mov_b32 m0, s95
	s_nop 0
	global_load_lds_dwordx4 v[8:9], off
	v_lshl_add_u64 v[8:9], v[234:235], 0, s[20:21]
	s_mov_b32 m0, s81
	s_nop 0
	global_load_lds_dwordx4 v[8:9], off
	v_lshl_add_u64 v[8:9], v[236:237], 0, s[20:21]
	s_mov_b32 m0, s90
	s_nop 0
	global_load_lds_dwordx4 v[8:9], off
	s_waitcnt vmcnt(8)
	s_waitcnt lgkmcnt(0)
	s_barrier
	s_setprio 1
	s_waitcnt lgkmcnt(0)
	v_mfma_f32_16x16x32_bf16 v[66:69], v[150:153], v[166:169], v[66:69]
	v_mfma_f32_16x16x32_bf16 v[62:65], v[158:161], v[166:169], v[62:65]
	v_mfma_f32_16x16x32_bf16 v[50:53], v[150:153], v[174:177], v[50:53]
	v_mfma_f32_16x16x32_bf16 v[46:49], v[158:161], v[174:177], v[46:49]
	v_mfma_f32_16x16x32_bf16 v[34:37], v[150:153], v[182:185], v[34:37]
	v_mfma_f32_16x16x32_bf16 v[30:33], v[158:161], v[182:185], v[30:33]
	v_mfma_f32_16x16x32_bf16 v[18:21], v[150:153], v[190:193], v[18:21]
	v_mfma_f32_16x16x32_bf16 v[14:17], v[158:161], v[190:193], v[14:17]
	v_mfma_f32_16x16x32_bf16 v[66:69], v[154:157], v[170:173], v[66:69]
	v_mfma_f32_16x16x32_bf16 v[62:65], v[162:165], v[170:173], v[62:65]
	v_mfma_f32_16x16x32_bf16 v[50:53], v[154:157], v[178:181], v[50:53]
	v_mfma_f32_16x16x32_bf16 v[46:49], v[162:165], v[178:181], v[46:49]
	v_mfma_f32_16x16x32_bf16 v[34:37], v[154:157], v[186:189], v[34:37]
	v_mfma_f32_16x16x32_bf16 v[30:33], v[162:165], v[186:189], v[30:33]
	v_mfma_f32_16x16x32_bf16 v[18:21], v[154:157], v[194:197], v[18:21]
	v_mfma_f32_16x16x32_bf16 v[14:17], v[162:165], v[194:197], v[14:17]
	v_mfma_f32_16x16x32_bf16 v[58:61], v[134:137], v[166:169], v[58:61]
	v_mfma_f32_16x16x32_bf16 v[54:57], v[142:145], v[166:169], v[54:57]
	v_mfma_f32_16x16x32_bf16 v[42:45], v[134:137], v[174:177], v[42:45]
	v_mfma_f32_16x16x32_bf16 v[38:41], v[142:145], v[174:177], v[38:41]
	v_mfma_f32_16x16x32_bf16 v[26:29], v[134:137], v[182:185], v[26:29]
	v_mfma_f32_16x16x32_bf16 v[22:25], v[142:145], v[182:185], v[22:25]
	v_mfma_f32_16x16x32_bf16 v[8:11], v[134:137], v[190:193], v[10:13]
	v_mfma_f32_16x16x32_bf16 v[4:7], v[142:145], v[190:193], v[4:7]
	v_mfma_f32_16x16x32_bf16 v[58:61], v[138:141], v[170:173], v[58:61]
	v_mfma_f32_16x16x32_bf16 v[54:57], v[146:149], v[170:173], v[54:57]
	v_mfma_f32_16x16x32_bf16 v[42:45], v[138:141], v[178:181], v[42:45]
	v_mfma_f32_16x16x32_bf16 v[38:41], v[146:149], v[178:181], v[38:41]
	v_mfma_f32_16x16x32_bf16 v[26:29], v[138:141], v[186:189], v[26:29]
	v_mfma_f32_16x16x32_bf16 v[22:25], v[146:149], v[186:189], v[22:25]
	v_mfma_f32_16x16x32_bf16 v[10:13], v[138:141], v[194:197], v[8:11]
	v_mfma_f32_16x16x32_bf16 v[6:9], v[146:149], v[194:197], v[4:7]
	s_setprio 0
	s_barrier
	s_andn2_b64 vcc, exec, s[42:43]
	s_cbranch_vccnz .LBB0_788
	s_add_i32 m0, s18, 0xc000
	s_nop 0
	global_load_lds_dwordx4 v[220:221], off
	s_add_i32 m0, s18, 0xe000
	s_nop 0
	global_load_lds_dwordx4 v[222:223], off

; #define PG8_STAGE(bufoff, gbase, voff) do { _Pragma("unroll") for (int _i = 0; _i < 2; ++_i) \
;         __builtin_amdgcn_global_load_lds((const unsigned*)((const char*)(gbase) + (voff)[_i]), (PG8_LAS unsigned*)(lds + (bufoff) + ldsw + _i * 8192), 16, 0, 0); } while (0)
; #define PG8_LDA(dst, b, h) do { _Pragma("unroll") for (int m = 0; m < 4; ++m) _Pragma("unroll") for (int k = 0; k < 2; ++k) dst[m][k] = *(const PG8_LAS bf16x8*)(lds + PG8_SA(b, h) + aoff + m * 2048 + k * 1024); } while (0)
; #define PG8_LDB(dst, b, h) do { _Pragma("unroll") for (int n = 0; n < 2; ++n) _Pragma("unroll") for (int k = 0; k < 2; ++k) dst[n][k] = *(const PG8_LAS bf16x8*)(lds + PG8_SB(b, h) + boff + n * 2048 + k * 1024); } while (0)
; #define PG8_MMA(ai, bj, At, Bt) do { __builtin_amdgcn_s_setprio(1); _Pragma("unroll") for (int m = 0; m < 4; ++m) _Pragma("unroll") for (int n = 0; n < 2; ++n) _Pragma("unroll") for (int k = 0; k < 2; ++k) \
;         acc[ai][bj][m][n] = mma16(Bt[n][k], At[m][k], acc[ai][bj][m][n]); __builtin_amdgcn_s_setprio(0); } while (0)
; template <class Epi, class Sched, bool ALIGN_EPI = false, bool SP2 = false>
; __device__ __forceinline__ void gemm_phase(PG8_LAS unsigned char* lds, const Gemm g, const Sched& S, const Epi& E, Stopwatch& sw) {
;     ...
;             const bool last = (t == nt - 2);
;             const char* a1 = cA + (size_t)(t + 1) * kstep;
;             const char* a2 = last ? nA : cA + (size_t)(t + 2) * kstep; const char* b2 = last ? nB : cB + (size_t)(t + 2) * kstep;
;             const char* a3 = a2 + kstep; const char* b3 = b2 + kstep;
;             if (last && has_next) S.a_ready(nxt);
;             if constexpr (SP2) {
;             int relax = __builtin_amdgcn_readfirstlane((int)((ui > 0) && (t == 0))); asm volatile("" : "+s"(relax));
;             PG8_LDB(B0, 0, 0); PG8_LDB(B1, 0, 1); PG8_SCHED; PG8_LDA(At, 0, 0); if (!relax) PG8_STAGE(PG8_SA(1, 1), a1 + hstep, voffA);
;             if (relax) PG8_WAIT_VN(8 + Epi::NST); else PG8_WAIT_V(8); PG8_WAIT_L(0); PG8_BAR; PG8_MMA(0, 0, At, B0); PG8_MMA(0, 1, At, B1); PG8_BAR; PG8_SCHED;
;             PG8_LDA(At, 0, 1); PG8_STAGE(PG8_SB(0, 0), b2, voffB); PG8_STAGE(PG8_SB(0, 1), b2 + hstep, voffB); PG8_STAGE(PG8_SA(0, 0), a2, voffA);
;             if (relax) PG8_WAIT_VN(8 + Epi::NST); else PG8_WAIT_V(8); PG8_WAIT_L(0); PG8_BAR; PG8_MMA(1, 0, At, B0); PG8_MMA(1, 1, At, B1); PG8_BAR; PG8_SCHED;
.LBB0_893:
	s_add_u32 s42, s58, s62
	s_addc_u32 s43, s59, s63
	s_add_u32 s74, s42, 0x100
	s_addc_u32 s75, s43, 0
	s_add_u32 s64, s76, s62
	s_addc_u32 s65, s77, s63
	s_cmpk_eq_i32 s62, 0xf00
	s_cselect_b64 s[68:69], -1, 0
	s_waitcnt lgkmcnt(0)
	s_and_b64 s[42:43], s[68:69], exec
	s_cselect_b32 s65, s51, s65
	s_cselect_b32 s64, s91, s64
	s_cselect_b32 s75, s53, s75
	s_cselect_b32 s74, s3, s74
	s_barrier
	s_setprio 1
	s_waitcnt lgkmcnt(0)
	v_mfma_f32_16x16x32_bf16 v[128:131], v[148:151], v[188:191], v[128:131]
	v_mfma_f32_16x16x32_bf16 v[124:127], v[156:159], v[188:191], v[124:127]
	v_mfma_f32_16x16x32_bf16 v[112:115], v[148:151], v[180:183], v[112:115]
	v_mfma_f32_16x16x32_bf16 v[108:111], v[156:159], v[180:183], v[108:111]
	v_mfma_f32_16x16x32_bf16 v[96:99], v[148:151], v[172:175], v[96:99]
	v_mfma_f32_16x16x32_bf16 v[92:95], v[156:159], v[172:175], v[92:95]
	v_mfma_f32_16x16x32_bf16 v[80:83], v[148:151], v[164:167], v[80:83]
	v_mfma_f32_16x16x32_bf16 v[76:79], v[156:159], v[164:167], v[76:79]
	v_mfma_f32_16x16x32_bf16 v[128:131], v[152:155], v[192:195], v[128:131]
	v_mfma_f32_16x16x32_bf16 v[124:127], v[160:163], v[192:195], v[124:127]
	v_mfma_f32_16x16x32_bf16 v[112:115], v[152:155], v[184:187], v[112:115]
	v_mfma_f32_16x16x32_bf16 v[108:111], v[160:163], v[184:187], v[108:111]
	v_mfma_f32_16x16x32_bf16 v[96:99], v[152:155], v[176:179], v[96:99]
	v_mfma_f32_16x16x32_bf16 v[92:95], v[160:163], v[176:179], v[92:95]
	v_mfma_f32_16x16x32_bf16 v[80:83], v[152:155], v[168:171], v[80:83]
	v_mfma_f32_16x16x32_bf16 v[76:79], v[160:163], v[168:171], v[76:79]
	v_mfma_f32_16x16x32_bf16 v[120:123], v[132:135], v[188:191], v[120:123]
	v_mfma_f32_16x16x32_bf16 v[116:119], v[140:143], v[188:191], v[116:119]
	v_mfma_f32_16x16x32_bf16 v[104:107], v[132:135], v[180:183], v[104:107]
	v_mfma_f32_16x16x32_bf16 v[100:103], v[140:143], v[180:183], v[100:103]
	v_mfma_f32_16x16x32_bf16 v[88:91], v[132:135], v[172:175], v[88:91]
	v_mfma_f32_16x16x32_bf16 v[84:87], v[140:143], v[172:175], v[84:87]
	v_mfma_f32_16x16x32_bf16 v[72:75], v[132:135], v[164:167], v[72:75]
	v_mfma_f32_16x16x32_bf16 v[68:71], v[140:143], v[164:167], v[68:71]
	v_mfma_f32_16x16x32_bf16 v[120:123], v[136:139], v[192:195], v[120:123]
	v_mfma_f32_16x16x32_bf16 v[116:119], v[144:147], v[192:195], v[116:119]
	v_mfma_f32_16x16x32_bf16 v[104:107], v[136:139], v[184:187], v[104:107]
	v_mfma_f32_16x16x32_bf16 v[100:103], v[144:147], v[184:187], v[100:103]
	v_mfma_f32_16x16x32_bf16 v[88:91], v[136:139], v[176:179], v[88:91]
	v_mfma_f32_16x16x32_bf16 v[84:87], v[144:147], v[176:179], v[84:87]
	v_mfma_f32_16x16x32_bf16 v[72:75], v[136:139], v[168:171], v[72:75]
	v_mfma_f32_16x16x32_bf16 v[68:71], v[144:147], v[168:171], v[68:71]
	s_setprio 0
	s_barrier
	s_mov_b32 m0, s18
	v_lshl_add_u64 v[218:219], s[64:65], 0, v[2:3]
	s_add_u32 s42, s64, 0x80000
	ds_read_b128 v[188:191], v228 offset:16384
	ds_read_b128 v[192:195], v228 offset:17408
	ds_read_b128 v[180:183], v228 offset:18432
	ds_read_b128 v[184:187], v228 offset:19456
	ds_read_b128 v[172:175], v228 offset:20480
	ds_read_b128 v[176:179], v228 offset:21504
	ds_read_b128 v[164:167], v228 offset:22528
	ds_read_b128 v[168:171], v228 offset:23552
	global_load_lds_dwordx4 v[218:219], off
	v_lshl_add_u64 v[220:221], s[64:65], 0, v[196:197]
	s_mov_b32 m0, s19
	s_addc_u32 s43, s65, 0
	global_load_lds_dwordx4 v[220:221], off
	v_lshl_add_u64 v[222:223], s[42:43], 0, v[2:3]
	s_mov_b32 m0, s24
	v_lshl_add_u64 v[224:225], s[74:75], 0, v[202:203]
	global_load_lds_dwordx4 v[222:223], off
	v_lshl_add_u64 v[222:223], s[42:43], 0, v[196:197]
	s_mov_b32 m0, s25
	v_cndmask_b32_e64 v229, 0, 1, s[78:79]
	global_load_lds_dwordx4 v[222:223], off
	v_lshl_add_u64 v[222:223], s[74:75], 0, v[204:205]
	s_mov_b32 m0, s16
	v_cmp_ne_u32_e64 s[42:43], 1, v229
	global_load_lds_dwordx4 v[222:223], off
	s_mov_b32 m0, s31
	s_andn2_b64 vcc, exec, s[78:79]
	global_load_lds_dwordx4 v[224:225], off
	s_cbranch_vccnz .LBB0_902
	s_waitcnt vmcnt(32)
	s_cbranch_execnz .LBB0_896

; #define PG8_STAGE(bufoff, gbase, voff) do { _Pragma("unroll") for (int _i = 0; _i < 2; ++_i) \
;         __builtin_amdgcn_global_load_lds((const unsigned*)((const char*)(gbase) + (voff)[_i]), (PG8_LAS unsigned*)(lds + (bufoff) + ldsw + _i * 8192), 16, 0, 0); } while (0)
; #define PG8_LDA(dst, b, h) do { _Pragma("unroll") for (int m = 0; m < 4; ++m) _Pragma("unroll") for (int k = 0; k < 2; ++k) dst[m][k] = *(const PG8_LAS bf16x8*)(lds + PG8_SA(b, h) + aoff + m * 2048 + k * 1024); } while (0)
; #define PG8_LDB(dst, b, h) do { _Pragma("unroll") for (int n = 0; n < 2; ++n) _Pragma("unroll") for (int k = 0; k < 2; ++k) dst[n][k] = *(const PG8_LAS bf16x8*)(lds + PG8_SB(b, h) + boff + n * 2048 + k * 1024); } while (0)
; #define PG8_MMA(ai, bj, At, Bt) do { __builtin_amdgcn_s_setprio(1); _Pragma("unroll") for (int m = 0; m < 4; ++m) _Pragma("unroll") for (int n = 0; n < 2; ++n) _Pragma("unroll") for (int k = 0; k < 2; ++k) \
;         acc[ai][bj][m][n] = mma16(Bt[n][k], At[m][k], acc[ai][bj][m][n]); __builtin_amdgcn_s_setprio(0); } while (0)
; #define PG8_WAIT_V(n) asm volatile("s_waitcnt vmcnt(" #n ")" ::: "memory")
; #define PG8_WAIT_VN(n) asm volatile("s_waitcnt vmcnt(%0)" :: "n"(n) : "memory")
; #define PG8_WAIT_L(n) asm volatile("s_waitcnt lgkmcnt(" #n ")" ::: "memory")
; #define PG8_BAR __builtin_amdgcn_s_barrier()
; #define PG8_SCHED __builtin_amdgcn_sched_barrier(0)
; template <class Epi, class Sched, bool ALIGN_EPI = false, bool SP2 = false>
; __device__ __forceinline__ void gemm_phase(PG8_LAS unsigned char* lds, const Gemm g, const Sched& S, const Epi& E, Stopwatch& sw) {
;     ...
;             if (relax) PG8_WAIT_VN(8 + Epi::NST); else PG8_WAIT_V(8); PG8_WAIT_L(0); PG8_BAR; PG8_MMA(1, 0, At, B0); PG8_MMA(1, 1, At, B1); PG8_BAR; PG8_SCHED;
;             PG8_LDB(B0, 1, 0); PG8_LDB(B1, 1, 1); PG8_SCHED; PG8_LDA(At, 1, 0); PG8_STAGE(PG8_SA(0, 1), a2 + hstep, voffA);
;             if (relax) PG8_WAIT_VN(8 + Epi::NST); else PG8_WAIT_V(8); PG8_WAIT_L(0); PG8_BAR; PG8_MMA(0, 0, At, B0); PG8_MMA(0, 1, At, B1); PG8_BAR; PG8_SCHED;
.LBB0_896:
	s_waitcnt lgkmcnt(0)
	s_barrier
	s_setprio 1
	s_waitcnt lgkmcnt(0)
	v_mfma_f32_16x16x32_bf16 v[64:67], v[148:151], v[188:191], v[64:67]
	v_mfma_f32_16x16x32_bf16 v[60:63], v[156:159], v[188:191], v[60:63]
	v_mfma_f32_16x16x32_bf16 v[48:51], v[148:151], v[180:183], v[48:51]
	v_mfma_f32_16x16x32_bf16 v[44:47], v[156:159], v[180:183], v[44:47]
	v_mfma_f32_16x16x32_bf16 v[32:35], v[148:151], v[172:175], v[32:35]
	v_mfma_f32_16x16x32_bf16 v[28:31], v[156:159], v[172:175], v[28:31]
	v_mfma_f32_16x16x32_bf16 v[16:19], v[148:151], v[164:167], v[16:19]
	v_mfma_f32_16x16x32_bf16 v[12:15], v[156:159], v[164:167], v[12:15]
	v_mfma_f32_16x16x32_bf16 v[64:67], v[152:155], v[192:195], v[64:67]
	v_mfma_f32_16x16x32_bf16 v[60:63], v[160:163], v[192:195], v[60:63]
	v_mfma_f32_16x16x32_bf16 v[48:51], v[152:155], v[184:187], v[48:51]
	v_mfma_f32_16x16x32_bf16 v[44:47], v[160:163], v[184:187], v[44:47]
	v_mfma_f32_16x16x32_bf16 v[32:35], v[152:155], v[176:179], v[32:35]
	v_mfma_f32_16x16x32_bf16 v[28:31], v[160:163], v[176:179], v[28:31]
	v_mfma_f32_16x16x32_bf16 v[16:19], v[152:155], v[168:171], v[16:19]
	v_mfma_f32_16x16x32_bf16 v[12:15], v[160:163], v[168:171], v[12:15]
	v_mfma_f32_16x16x32_bf16 v[56:59], v[132:135], v[188:191], v[56:59]
	v_mfma_f32_16x16x32_bf16 v[52:55], v[140:143], v[188:191], v[52:55]
	v_mfma_f32_16x16x32_bf16 v[40:43], v[132:135], v[180:183], v[40:43]
	v_mfma_f32_16x16x32_bf16 v[36:39], v[140:143], v[180:183], v[36:39]
	v_mfma_f32_16x16x32_bf16 v[24:27], v[132:135], v[172:175], v[24:27]
	v_mfma_f32_16x16x32_bf16 v[20:23], v[140:143], v[172:175], v[20:23]
	v_mfma_f32_16x16x32_bf16 v[8:11], v[132:135], v[164:167], v[8:11]
	v_mfma_f32_16x16x32_bf16 v[4:7], v[140:143], v[164:167], v[4:7]
	v_mfma_f32_16x16x32_bf16 v[56:59], v[136:139], v[192:195], v[56:59]
	v_mfma_f32_16x16x32_bf16 v[52:55], v[144:147], v[192:195], v[52:55]
	v_mfma_f32_16x16x32_bf16 v[40:43], v[136:139], v[184:187], v[40:43]
	v_mfma_f32_16x16x32_bf16 v[36:39], v[144:147], v[184:187], v[36:39]
	v_mfma_f32_16x16x32_bf16 v[24:27], v[136:139], v[176:179], v[24:27]
	v_mfma_f32_16x16x32_bf16 v[20:23], v[144:147], v[176:179], v[20:23]
	v_mfma_f32_16x16x32_bf16 v[8:11], v[136:139], v[168:171], v[8:11]
	v_mfma_f32_16x16x32_bf16 v[4:7], v[144:147], v[168:171], v[4:7]
	s_setprio 0
	s_barrier
	v_add_u32_e32 v132, 0x18000, v227
	v_add_u32_e32 v144, 0x1c000, v227
	ds_read_b128 v[148:151], v132
	ds_read_b128 v[152:155], v132 offset:1024
	ds_read_b128 v[156:159], v132 offset:2048
	ds_read_b128 v[160:163], v132 offset:3072
	ds_read_b128 v[132:135], v144
	ds_read_b128 v[136:139], v144 offset:1024
	ds_read_b128 v[140:143], v144 offset:2048
	ds_read_b128 v[144:147], v144 offset:3072
	s_add_u32 s74, s74, 0x80000
	s_addc_u32 s75, s75, 0
	s_mov_b32 m0, s36
	v_lshl_add_u64 v[230:231], s[74:75], 0, v[204:205]
	ds_read_b128 v[188:191], v228 offset:32768
	ds_read_b128 v[192:195], v228 offset:33792
	ds_read_b128 v[180:183], v228 offset:34816
	ds_read_b128 v[184:187], v228 offset:35840
	ds_read_b128 v[172:175], v228 offset:36864
	ds_read_b128 v[176:179], v228 offset:37888
	ds_read_b128 v[164:167], v228 offset:38912
	ds_read_b128 v[168:171], v228 offset:39936
	global_load_lds_dwordx4 v[230:231], off
	v_lshl_add_u64 v[230:231], s[74:75], 0, v[202:203]
	s_mov_b32 m0, s37
	s_and_b64 vcc, exec, s[42:43]
	global_load_lds_dwordx4 v[230:231], off
	s_cbranch_vccnz .LBB0_903
	s_waitcnt vmcnt(32)
	s_mov_b64 s[74:75], s[10:11]
	s_cbranch_execnz .LBB0_899

; #define PG8_STAGE(bufoff, gbase, voff) do { _Pragma("unroll") for (int _i = 0; _i < 2; ++_i) \
;         __builtin_amdgcn_global_load_lds((const unsigned*)((const char*)(gbase) + (voff)[_i]), (PG8_LAS unsigned*)(lds + (bufoff) + ldsw + _i * 8192), 16, 0, 0); } while (0)
; #define PG8_LDA(dst, b, h) do { _Pragma("unroll") for (int m = 0; m < 4; ++m) _Pragma("unroll") for (int k = 0; k < 2; ++k) dst[m][k] = *(const PG8_LAS bf16x8*)(lds + PG8_SA(b, h) + aoff + m * 2048 + k * 1024); } while (0)
; #define PG8_MMA(ai, bj, At, Bt) do { __builtin_amdgcn_s_setprio(1); _Pragma("unroll") for (int m = 0; m < 4; ++m) _Pragma("unroll") for (int n = 0; n < 2; ++n) _Pragma("unroll") for (int k = 0; k < 2; ++k) \
;         acc[ai][bj][m][n] = mma16(Bt[n][k], At[m][k], acc[ai][bj][m][n]); __builtin_amdgcn_s_setprio(0); } while (0)
; #define PG8_WAIT_V(n) asm volatile("s_waitcnt vmcnt(" #n ")" ::: "memory")
; #define PG8_WAIT_VN(n) asm volatile("s_waitcnt vmcnt(%0)" :: "n"(n) : "memory")
; #define PG8_WAIT_L(n) asm volatile("s_waitcnt lgkmcnt(" #n ")" ::: "memory")
; #define PG8_BAR __builtin_amdgcn_s_barrier()
; #define PG8_SCHED __builtin_amdgcn_sched_barrier(0)
; template <class Epi, class Sched, bool ALIGN_EPI = false, bool SP2 = false>
; __device__ __forceinline__ void gemm_phase(PG8_LAS unsigned char* lds, const Gemm g, const Sched& S, const Epi& E, Stopwatch& sw) {
;     ...
;             if (relax) PG8_WAIT_VN(8 + Epi::NST); else PG8_WAIT_V(8); PG8_WAIT_L(0); PG8_BAR; PG8_MMA(0, 0, At, B0); PG8_MMA(0, 1, At, B1); PG8_BAR; PG8_SCHED;
;             PG8_LDA(At, 1, 1); PG8_STAGE(PG8_SB(1, 0), b3, voffB); PG8_STAGE(PG8_SB(1, 1), b3 + hstep, voffB); PG8_STAGE(PG8_SA(1, 0), a3, voffA);
;             PG8_WAIT_V(8); PG8_WAIT_L(0); PG8_BAR; PG8_MMA(1, 0, At, B0); PG8_MMA(1, 1, At, B1); PG8_BAR; PG8_SCHED;
;             if (last && has_next) PG8_STAGE(PG8_SA(1, 1), a3 + hstep, voffA);
.LBB0_899:
	s_waitcnt lgkmcnt(0)
	s_and_b64 s[42:43], s[40:41], s[68:69]
	s_barrier
	s_setprio 1
	s_waitcnt lgkmcnt(0)
	v_mfma_f32_16x16x32_bf16 v[128:131], v[148:151], v[188:191], v[128:131]
	v_mfma_f32_16x16x32_bf16 v[124:127], v[156:159], v[188:191], v[124:127]
	v_mfma_f32_16x16x32_bf16 v[112:115], v[148:151], v[180:183], v[112:115]
	v_mfma_f32_16x16x32_bf16 v[108:111], v[156:159], v[180:183], v[108:111]
	v_mfma_f32_16x16x32_bf16 v[96:99], v[148:151], v[172:175], v[96:99]
	v_mfma_f32_16x16x32_bf16 v[92:95], v[156:159], v[172:175], v[92:95]
	v_mfma_f32_16x16x32_bf16 v[80:83], v[148:151], v[164:167], v[80:83]
	v_mfma_f32_16x16x32_bf16 v[76:79], v[156:159], v[164:167], v[76:79]
	v_mfma_f32_16x16x32_bf16 v[128:131], v[152:155], v[192:195], v[128:131]
	v_mfma_f32_16x16x32_bf16 v[124:127], v[160:163], v[192:195], v[124:127]
	v_mfma_f32_16x16x32_bf16 v[112:115], v[152:155], v[184:187], v[112:115]
	v_mfma_f32_16x16x32_bf16 v[108:111], v[160:163], v[184:187], v[108:111]
	v_mfma_f32_16x16x32_bf16 v[96:99], v[152:155], v[176:179], v[96:99]
	v_mfma_f32_16x16x32_bf16 v[92:95], v[160:163], v[176:179], v[92:95]
	v_mfma_f32_16x16x32_bf16 v[80:83], v[152:155], v[168:171], v[80:83]
	v_mfma_f32_16x16x32_bf16 v[76:79], v[160:163], v[168:171], v[76:79]
	v_mfma_f32_16x16x32_bf16 v[120:123], v[132:135], v[188:191], v[120:123]
	v_mfma_f32_16x16x32_bf16 v[116:119], v[140:143], v[188:191], v[116:119]
	v_mfma_f32_16x16x32_bf16 v[104:107], v[132:135], v[180:183], v[104:107]
	v_mfma_f32_16x16x32_bf16 v[100:103], v[140:143], v[180:183], v[100:103]
	v_mfma_f32_16x16x32_bf16 v[88:91], v[132:135], v[172:175], v[88:91]
	v_mfma_f32_16x16x32_bf16 v[84:87], v[140:143], v[172:175], v[84:87]
	v_mfma_f32_16x16x32_bf16 v[72:75], v[132:135], v[164:167], v[72:75]
	v_mfma_f32_16x16x32_bf16 v[68:71], v[140:143], v[164:167], v[68:71]
	v_mfma_f32_16x16x32_bf16 v[120:123], v[136:139], v[192:195], v[120:123]
	v_mfma_f32_16x16x32_bf16 v[116:119], v[144:147], v[192:195], v[116:119]
	v_mfma_f32_16x16x32_bf16 v[104:107], v[136:139], v[184:187], v[104:107]
	v_mfma_f32_16x16x32_bf16 v[100:103], v[144:147], v[184:187], v[100:103]
	v_mfma_f32_16x16x32_bf16 v[88:91], v[136:139], v[176:179], v[88:91]
	v_mfma_f32_16x16x32_bf16 v[84:87], v[144:147], v[176:179], v[84:87]
	v_mfma_f32_16x16x32_bf16 v[72:75], v[136:139], v[168:171], v[72:75]
	v_mfma_f32_16x16x32_bf16 v[68:71], v[144:147], v[168:171], v[68:71]
	s_setprio 0
	s_barrier
	s_mov_b32 m0, s73
	v_lshl_add_u64 v[218:219], v[218:219], 0, s[20:21]
	s_add_u32 s64, s64, 0x80080
	ds_read_b128 v[164:167], v228 offset:49152
	ds_read_b128 v[168:171], v228 offset:50176
	ds_read_b128 v[172:175], v228 offset:51200
	ds_read_b128 v[176:179], v228 offset:52224
	ds_read_b128 v[180:183], v228 offset:53248
	ds_read_b128 v[184:187], v228 offset:54272
	ds_read_b128 v[188:191], v228 offset:55296
	ds_read_b128 v[192:195], v228 offset:56320
	global_load_lds_dwordx4 v[218:219], off
	v_lshl_add_u64 v[218:219], v[220:221], 0, s[20:21]
	s_mov_b32 m0, s80
	s_addc_u32 s65, s65, 0
	global_load_lds_dwordx4 v[218:219], off
	v_lshl_add_u64 v[218:219], s[64:65], 0, v[2:3]
	s_mov_b32 m0, s83
	s_nop 0
	global_load_lds_dwordx4 v[218:219], off
	v_lshl_add_u64 v[218:219], s[64:65], 0, v[196:197]
	s_mov_b32 m0, s90
	s_nop 0
	global_load_lds_dwordx4 v[218:219], off
	v_lshl_add_u64 v[218:219], v[222:223], 0, s[20:21]
	s_mov_b32 m0, s81
	s_nop 0
	global_load_lds_dwordx4 v[218:219], off
	v_lshl_add_u64 v[218:219], v[224:225], 0, s[20:21]
	s_mov_b32 m0, s82
	s_nop 0
	global_load_lds_dwordx4 v[218:219], off
	s_waitcnt vmcnt(8)
	s_waitcnt lgkmcnt(0)
	s_barrier
	s_setprio 1
	s_waitcnt lgkmcnt(0)
	v_mfma_f32_16x16x32_bf16 v[64:67], v[148:151], v[164:167], v[64:67]
	v_mfma_f32_16x16x32_bf16 v[60:63], v[156:159], v[164:167], v[60:63]
	v_mfma_f32_16x16x32_bf16 v[48:51], v[148:151], v[172:175], v[48:51]
	v_mfma_f32_16x16x32_bf16 v[44:47], v[156:159], v[172:175], v[44:47]
	v_mfma_f32_16x16x32_bf16 v[32:35], v[148:151], v[180:183], v[32:35]
	v_mfma_f32_16x16x32_bf16 v[28:31], v[156:159], v[180:183], v[28:31]
	v_mfma_f32_16x16x32_bf16 v[16:19], v[148:151], v[188:191], v[16:19]
	v_mfma_f32_16x16x32_bf16 v[12:15], v[156:159], v[188:191], v[12:15]
	v_mfma_f32_16x16x32_bf16 v[64:67], v[152:155], v[168:171], v[64:67]
	v_mfma_f32_16x16x32_bf16 v[60:63], v[160:163], v[168:171], v[60:63]
	v_mfma_f32_16x16x32_bf16 v[48:51], v[152:155], v[176:179], v[48:51]
	v_mfma_f32_16x16x32_bf16 v[44:47], v[160:163], v[176:179], v[44:47]
	v_mfma_f32_16x16x32_bf16 v[32:35], v[152:155], v[184:187], v[32:35]
	v_mfma_f32_16x16x32_bf16 v[28:31], v[160:163], v[184:187], v[28:31]
	v_mfma_f32_16x16x32_bf16 v[16:19], v[152:155], v[192:195], v[16:19]
	v_mfma_f32_16x16x32_bf16 v[12:15], v[160:163], v[192:195], v[12:15]
	v_mfma_f32_16x16x32_bf16 v[56:59], v[132:135], v[164:167], v[56:59]
	v_mfma_f32_16x16x32_bf16 v[52:55], v[140:143], v[164:167], v[52:55]
	v_mfma_f32_16x16x32_bf16 v[40:43], v[132:135], v[172:175], v[40:43]
	v_mfma_f32_16x16x32_bf16 v[36:39], v[140:143], v[172:175], v[36:39]
	v_mfma_f32_16x16x32_bf16 v[24:27], v[132:135], v[180:183], v[24:27]
	v_mfma_f32_16x16x32_bf16 v[20:23], v[140:143], v[180:183], v[20:23]
	v_mfma_f32_16x16x32_bf16 v[8:11], v[132:135], v[188:191], v[8:11]
	v_mfma_f32_16x16x32_bf16 v[4:7], v[140:143], v[188:191], v[4:7]
	v_mfma_f32_16x16x32_bf16 v[56:59], v[136:139], v[168:171], v[56:59]
	v_mfma_f32_16x16x32_bf16 v[52:55], v[144:147], v[168:171], v[52:55]
	v_mfma_f32_16x16x32_bf16 v[40:43], v[136:139], v[176:179], v[40:43]
	v_mfma_f32_16x16x32_bf16 v[36:39], v[144:147], v[176:179], v[36:39]
	v_mfma_f32_16x16x32_bf16 v[24:27], v[136:139], v[184:187], v[24:27]
	v_mfma_f32_16x16x32_bf16 v[20:23], v[144:147], v[184:187], v[20:23]
	v_mfma_f32_16x16x32_bf16 v[8:11], v[136:139], v[192:195], v[8:11]
	v_mfma_f32_16x16x32_bf16 v[4:7], v[144:147], v[192:195], v[4:7]
	s_setprio 0
	s_barrier
	s_andn2_b64 vcc, exec, s[42:43]
	s_cbranch_vccnz .LBB0_889
	s_add_i32 m0, s16, 0xc000
	s_nop 0
	global_load_lds_dwordx4 v[212:213], off
	s_add_i32 m0, s16, 0xe000
	s_nop 0
	global_load_lds_dwordx4 v[210:211], off
	s_branch .LBB0_889

; #define PG8_STAGE(bufoff, gbase, voff) do { _Pragma("unroll") for (int _i = 0; _i < 2; ++_i) \
;         __builtin_amdgcn_global_load_lds((const unsigned*)((const char*)(gbase) + (voff)[_i]), (PG8_LAS unsigned*)(lds + (bufoff) + ldsw + _i * 8192), 16, 0, 0); } while (0)
; #define PG8_WAIT_V(n) asm volatile("s_waitcnt vmcnt(" #n ")" ::: "memory")
; #define PG8_BAR __builtin_amdgcn_s_barrier()
; template <class Epi, class Sched, bool ALIGN_EPI = false, bool SP2 = false>
; __device__ __forceinline__ void gemm_phase(PG8_LAS unsigned char* lds, const Gemm g, const Sched& S, const Epi& E, Stopwatch& sw) {
;     ...
;     for (int i = 0; i < 2; ++i) { int R, C; stage_rc(tid * 16 + i * 8192, R, C); const int Rb = Epi::PERM ? ((R & ~31) + perm32(R & 31)) : R;
;         voffA[i] = (unsigned)(R * K + C) * 2u; voffB[i] = (unsigned)(Rb * K + C) * 2u; }
;     const size_t kstep = (size_t)(BK * 2);
;     const size_t hstep = (size_t)HALF * K * 2;
;     const size_t tstep = 2 * hstep;
;     const unsigned ldsw = (unsigned)wid * 1024u;
;     const int aoff = lds_byte(wr * 64 + fr, fq * 8), boff = lds_byte(wc * 32 + fr, fq * 8);
;     ...
;         PG8_STAGE(PG8_SB(0, 0), cB, voffB); PG8_STAGE(PG8_SB(0, 1), cB + hstep, voffB); PG8_STAGE(PG8_SA(0, 0), cA, voffA); PG8_STAGE(PG8_SA(0, 1), cA + hstep, voffA);
;         if (wr == 1) PG8_BAR;
;         PG8_WAIT_V(2); PG8_BAR;
;         PG8_STAGE(PG8_SB(1, 0), cB + kstep, voffB); PG8_STAGE(PG8_SA(1, 0), cA + kstep, voffA); PG8_STAGE(PG8_SB(1, 1), cB + hstep + kstep, voffB);
;         PG8_WAIT_V(6); PG8_BAR;
.LBB0_1107:
	v_lshrrev_b32_e32 v20, 1, v14
	v_and_b32_e32 v20, 24, v20
	v_and_b32_e32 v15, 15, v14
	v_lshlrev_b32_e32 v21, 1, v20
	v_lshlrev_b32_e32 v14, 2, v14
	s_lshl_b32 s3, s3, 5
	v_lshl_or_b32 v1, s4, 6, v15
	v_lshl_or_b32 v15, v15, 6, v21
	s_lshl_b32 s4, s4, 13
	v_and_b32_e32 v14, 32, v14
	s_and_b32 s3, s3, 0x60
	v_bitop3_b32 v21, v15, s4, v14 bitop3:0xde
	s_lshl_b32 s4, s3, 8
	v_bitop3_b32 v14, v15, s4, v14 bitop3:0xde
	v_readlane_b32 s4, v255, 26
	s_lshl_b32 s34, s4, 13
	s_lshl_b64 s[38:39], s[34:35], 2
	v_readlane_b32 s4, v250, 32
	s_add_u32 s46, s4, s38
	v_readlane_b32 s4, v250, 33
	v_readlane_b32 s58, v254, 15
	s_addc_u32 s47, s4, s39
	s_add_i32 s34, s19, 0x18000
	v_mov_b32_e32 v205, v3
	v_readlane_b32 s59, v254, 16
	v_lshl_add_u64 v[4:5], v[4:5], 0, s[20:21]
	s_mov_b32 m0, s34
	s_add_i32 s82, s19, 0x1a000
	v_lshl_add_u64 v[16:17], s[58:59], 0, v[204:205]
	v_mov_b32_e32 v203, v3
	s_waitcnt vmcnt(2)
	s_barrier
	global_load_lds_dwordx4 v[4:5], off
	v_lshl_add_u64 v[4:5], v[6:7], 0, s[20:21]
	s_mov_b32 m0, s82
	s_add_i32 s83, s19, 0x8000
	s_add_i32 s90, s19, 0xa000
	v_lshl_add_u64 v[18:19], s[58:59], 0, v[202:203]
	global_load_lds_dwordx4 v[4:5], off
	v_lshl_add_u64 v[4:5], v[16:17], 0, s[20:21]
	s_mov_b32 m0, s83
	s_add_u32 s38, s40, 0x40080
	global_load_lds_dwordx4 v[4:5], off
	v_lshl_add_u64 v[4:5], v[18:19], 0, s[20:21]
	s_mov_b32 m0, s90
	s_addc_u32 s39, s41, 0
	s_add_i32 s94, s19, 0x1c000
	global_load_lds_dwordx4 v[4:5], off
	v_lshl_add_u64 v[4:5], s[38:39], 0, v[2:3]
	s_mov_b32 m0, s94
	s_add_i32 s95, s19, 0x1e000
	global_load_lds_dwordx4 v[4:5], off
	v_lshl_add_u64 v[4:5], s[38:39], 0, v[196:197]
	s_mov_b32 m0, s95
	s_cmpk_lt_u32 s0, 0x100
	global_load_lds_dwordx4 v[4:5], off
	v_lshlrev_b32_e32 v4, 14, v12
	v_and_b32_e32 v4, 0xffff8000, v4
	v_lshl_add_u32 v4, v11, 11, v4
	v_and_b32_e32 v5, 1, v12
	v_lshl_or_b32 v4, v5, 6, v4
	v_lshl_add_u32 v206, v13, 1, v4
	v_lshlrev_b32_e32 v4, 14, v8
	v_and_b32_e32 v4, 0xffff8000, v4
	s_waitcnt vmcnt(6)
	v_lshl_add_u32 v4, v9, 11, v4
	v_and_b32_e32 v5, 1, v8
	v_lshl_or_b32 v4, v5, 6, v4
	v_readlane_b32 s38, v254, 11
	s_cselect_b64 s[48:49], -1, 0
	v_or_b32_e32 v226, s3, v20
	v_add_u32_e32 v226, s3, v226
	v_mov_b32_e32 v207, v3
	v_lshl_add_u32 v208, v10, 1, v4
	v_mov_b32_e32 v209, v3
	s_mov_b32 s0, 0
	v_add_u32_e32 v227, 0, v14
	v_add_u32_e32 v228, 0, v21
	v_readlane_b32 s31, v253, 54
	s_mov_b32 s4, s38
	s_barrier
	v_readlane_b32 s39, v254, 12
	s_branch .LBB0_1110

; #define PG8_STAGE(bufoff, gbase, voff) do { _Pragma("unroll") for (int _i = 0; _i < 2; ++_i) \
;         __builtin_amdgcn_global_load_lds((const unsigned*)((const char*)(gbase) + (voff)[_i]), (PG8_LAS unsigned*)(lds + (bufoff) + ldsw + _i * 8192), 16, 0, 0); } while (0)
; #define PG8_LDA(dst, b, h) do { _Pragma("unroll") for (int m = 0; m < 4; ++m) _Pragma("unroll") for (int k = 0; k < 2; ++k) dst[m][k] = *(const PG8_LAS bf16x8*)(lds + PG8_SA(b, h) + aoff + m * 2048 + k * 1024); } while (0)
; #define PG8_LDB(dst, b, h) do { _Pragma("unroll") for (int n = 0; n < 2; ++n) _Pragma("unroll") for (int k = 0; k < 2; ++k) dst[n][k] = *(const PG8_LAS bf16x8*)(lds + PG8_SB(b, h) + boff + n * 2048 + k * 1024); } while (0)
; #define PG8_MMA(ai, bj, At, Bt) do { __builtin_amdgcn_s_setprio(1); _Pragma("unroll") for (int m = 0; m < 4; ++m) _Pragma("unroll") for (int n = 0; n < 2; ++n) _Pragma("unroll") for (int k = 0; k < 2; ++k) \
;         acc[ai][bj][m][n] = mma16(Bt[n][k], At[m][k], acc[ai][bj][m][n]); __builtin_amdgcn_s_setprio(0); } while (0)
; #define PG8_WAIT_V(n) asm volatile("s_waitcnt vmcnt(" #n ")" ::: "memory")
; #define PG8_WAIT_VN(n) asm volatile("s_waitcnt vmcnt(%0)" :: "n"(n) : "memory")
; #define PG8_WAIT_L(n) asm volatile("s_waitcnt lgkmcnt(" #n ")" ::: "memory")
; #define PG8_BAR __builtin_amdgcn_s_barrier()
; #define PG8_SCHED __builtin_amdgcn_sched_barrier(0)
; template <class Epi, class Sched, bool ALIGN_EPI = false, bool SP2 = false>
; __device__ __forceinline__ void gemm_phase(PG8_LAS unsigned char* lds, const Gemm g, const Sched& S, const Epi& E, Stopwatch& sw) {
;     ...
;             int relax = __builtin_amdgcn_readfirstlane((int)((ui > 0) && (t == 0))); asm volatile("" : "+s"(relax));
;             PG8_LDB(B0, 0, 0); PG8_LDB(B1, 0, 1); PG8_SCHED; PG8_LDA(At, 0, 0); if (!relax) PG8_STAGE(PG8_SA(1, 1), a1 + hstep, voffA);
;             if (relax) PG8_WAIT_VN(8 + Epi::NST); else PG8_WAIT_V(8); PG8_WAIT_L(0); PG8_BAR; PG8_MMA(0, 0, At, B0); PG8_MMA(0, 1, At, B1); PG8_BAR; PG8_SCHED;
.LBB0_1118:
	s_cmp_eq_u32 s62, 0
	s_cselect_b64 s[40:41], -1, 0
	s_and_b64 s[40:41], s[60:61], s[40:41]
	v_cndmask_b32_e64 v132, 0, 1, s[40:41]
	v_add_u32_e32 v144, 0x11000, v227
	v_readfirstlane_b32 s40, v132
	s_and_b32 s40, s40, 1
	v_add_u32_e32 v132, 0x10000, v227
	ds_read_b128 v[148:151], v132
	ds_read_b128 v[152:155], v132 offset:1024
	ds_read_b128 v[156:159], v132 offset:2048
	ds_read_b128 v[160:163], v132 offset:3072
	ds_read_b128 v[132:135], v144
	ds_read_b128 v[136:139], v144 offset:1024
	ds_read_b128 v[140:143], v144 offset:2048
	ds_read_b128 v[144:147], v144 offset:3072
	ds_read_b128 v[188:191], v228
	ds_read_b128 v[192:195], v228 offset:1024
	ds_read_b128 v[180:183], v228 offset:2048
	ds_read_b128 v[184:187], v228 offset:3072
	ds_read_b128 v[172:175], v228 offset:4096
	ds_read_b128 v[176:179], v228 offset:5120
	ds_read_b128 v[164:167], v228 offset:6144
	ds_read_b128 v[168:171], v228 offset:7168
	s_cmp_lg_u32 s40, 0
	s_cselect_b64 s[78:79], -1, 0
	s_and_b64 vcc, exec, s[78:79]
	s_cbranch_vccz .LBB0_1129
	s_waitcnt vmcnt(24)
	s_cbranch_execnz .LBB0_1121

; #define PG8_STAGE(bufoff, gbase, voff) do { _Pragma("unroll") for (int _i = 0; _i < 2; ++_i) \
;         __builtin_amdgcn_global_load_lds((const unsigned*)((const char*)(gbase) + (voff)[_i]), (PG8_LAS unsigned*)(lds + (bufoff) + ldsw + _i * 8192), 16, 0, 0); } while (0)
; #define PG8_LDA(dst, b, h) do { _Pragma("unroll") for (int m = 0; m < 4; ++m) _Pragma("unroll") for (int k = 0; k < 2; ++k) dst[m][k] = *(const PG8_LAS bf16x8*)(lds + PG8_SA(b, h) + aoff + m * 2048 + k * 1024); } while (0)
; #define PG8_LDB(dst, b, h) do { _Pragma("unroll") for (int n = 0; n < 2; ++n) _Pragma("unroll") for (int k = 0; k < 2; ++k) dst[n][k] = *(const PG8_LAS bf16x8*)(lds + PG8_SB(b, h) + boff + n * 2048 + k * 1024); } while (0)
; #define PG8_MMA(ai, bj, At, Bt) do { __builtin_amdgcn_s_setprio(1); _Pragma("unroll") for (int m = 0; m < 4; ++m) _Pragma("unroll") for (int n = 0; n < 2; ++n) _Pragma("unroll") for (int k = 0; k < 2; ++k) \
;         acc[ai][bj][m][n] = mma16(Bt[n][k], At[m][k], acc[ai][bj][m][n]); __builtin_amdgcn_s_setprio(0); } while (0)
; template <class Epi, class Sched, bool ALIGN_EPI = false, bool SP2 = false>
; __device__ __forceinline__ void gemm_phase(PG8_LAS unsigned char* lds, const Gemm g, const Sched& S, const Epi& E, Stopwatch& sw) {
;     ...
;             const bool last = (t == nt - 2);
;             const char* a1 = cA + (size_t)(t + 1) * kstep;
;             const char* a2 = last ? nA : cA + (size_t)(t + 2) * kstep; const char* b2 = last ? nB : cB + (size_t)(t + 2) * kstep;
;             const char* a3 = a2 + kstep; const char* b3 = b2 + kstep;
;             if (last && has_next) S.a_ready(nxt);
;             if constexpr (SP2) {
;             int relax = __builtin_amdgcn_readfirstlane((int)((ui > 0) && (t == 0))); asm volatile("" : "+s"(relax));
;             PG8_LDB(B0, 0, 0); PG8_LDB(B1, 0, 1); PG8_SCHED; PG8_LDA(At, 0, 0); if (!relax) PG8_STAGE(PG8_SA(1, 1), a1 + hstep, voffA);
;             if (relax) PG8_WAIT_VN(8 + Epi::NST); else PG8_WAIT_V(8); PG8_WAIT_L(0); PG8_BAR; PG8_MMA(0, 0, At, B0); PG8_MMA(0, 1, At, B1); PG8_BAR; PG8_SCHED;
;             PG8_LDA(At, 0, 1); PG8_STAGE(PG8_SB(0, 0), b2, voffB); PG8_STAGE(PG8_SB(0, 1), b2 + hstep, voffB); PG8_STAGE(PG8_SA(0, 0), a2, voffA);
;             if (relax) PG8_WAIT_VN(8 + Epi::NST); else PG8_WAIT_V(8); PG8_WAIT_L(0); PG8_BAR; PG8_MMA(1, 0, At, B0); PG8_MMA(1, 1, At, B1); PG8_BAR; PG8_SCHED;
.LBB0_1121:
	s_add_u32 s40, s58, s62
	s_addc_u32 s41, s59, s63
	s_add_u32 s74, s40, 0x100
	s_addc_u32 s75, s41, 0
	s_add_u32 s64, s76, s62
	s_addc_u32 s65, s77, s63
	s_cmpk_eq_i32 s62, 0x700
	s_cselect_b64 s[68:69], -1, 0
	s_waitcnt lgkmcnt(0)
	s_and_b64 s[40:41], s[68:69], exec
	s_cselect_b32 s65, s51, s65
	s_cselect_b32 s64, s91, s64
	s_cselect_b32 s75, s53, s75
	s_cselect_b32 s74, s3, s74
	s_barrier
	s_setprio 1
	s_waitcnt lgkmcnt(0)
	v_mfma_i32_16x16x64_i8 v[128:131], v[148:151], v[188:191], v[128:131]
	v_mfma_i32_16x16x64_i8 v[124:127], v[156:159], v[188:191], v[124:127]
	v_mfma_i32_16x16x64_i8 v[120:123], v[148:151], v[180:183], v[120:123]
	v_mfma_i32_16x16x64_i8 v[116:119], v[156:159], v[180:183], v[116:119]
	v_mfma_i32_16x16x64_i8 v[112:115], v[148:151], v[172:175], v[112:115]
	v_mfma_i32_16x16x64_i8 v[108:111], v[156:159], v[172:175], v[108:111]
	v_mfma_i32_16x16x64_i8 v[104:107], v[148:151], v[164:167], v[104:107]
	v_mfma_i32_16x16x64_i8 v[100:103], v[156:159], v[164:167], v[100:103]
	v_mfma_i32_16x16x64_i8 v[128:131], v[152:155], v[192:195], v[128:131]
	v_mfma_i32_16x16x64_i8 v[124:127], v[160:163], v[192:195], v[124:127]
	v_mfma_i32_16x16x64_i8 v[120:123], v[152:155], v[184:187], v[120:123]
	v_mfma_i32_16x16x64_i8 v[116:119], v[160:163], v[184:187], v[116:119]
	v_mfma_i32_16x16x64_i8 v[112:115], v[152:155], v[176:179], v[112:115]
	v_mfma_i32_16x16x64_i8 v[108:111], v[160:163], v[176:179], v[108:111]
	v_mfma_i32_16x16x64_i8 v[104:107], v[152:155], v[168:171], v[104:107]
	v_mfma_i32_16x16x64_i8 v[100:103], v[160:163], v[168:171], v[100:103]
	v_mfma_i32_16x16x64_i8 v[76:79], v[132:135], v[188:191], v[76:79]
	v_mfma_i32_16x16x64_i8 v[68:71], v[140:143], v[188:191], v[68:71]
	v_mfma_i32_16x16x64_i8 v[60:63], v[132:135], v[180:183], v[60:63]
	v_mfma_i32_16x16x64_i8 v[52:55], v[140:143], v[180:183], v[52:55]
	v_mfma_i32_16x16x64_i8 v[48:51], v[132:135], v[172:175], v[48:51]
	v_mfma_i32_16x16x64_i8 v[44:47], v[140:143], v[172:175], v[44:47]
	v_mfma_i32_16x16x64_i8 v[40:43], v[132:135], v[164:167], v[40:43]
	v_mfma_i32_16x16x64_i8 v[36:39], v[140:143], v[164:167], v[36:39]
	v_mfma_i32_16x16x64_i8 v[76:79], v[136:139], v[192:195], v[76:79]
	v_mfma_i32_16x16x64_i8 v[68:71], v[144:147], v[192:195], v[68:71]
	v_mfma_i32_16x16x64_i8 v[60:63], v[136:139], v[184:187], v[60:63]
	v_mfma_i32_16x16x64_i8 v[52:55], v[144:147], v[184:187], v[52:55]
	v_mfma_i32_16x16x64_i8 v[48:51], v[136:139], v[176:179], v[48:51]
	v_mfma_i32_16x16x64_i8 v[44:47], v[144:147], v[176:179], v[44:47]
	v_mfma_i32_16x16x64_i8 v[40:43], v[136:139], v[168:171], v[40:43]
	v_mfma_i32_16x16x64_i8 v[36:39], v[144:147], v[168:171], v[36:39]
	s_setprio 0
	s_barrier
	s_mov_b32 m0, s25
	v_lshl_add_u64 v[218:219], s[64:65], 0, v[2:3]
	s_add_u32 s40, s64, 0x40000
	ds_read_b128 v[188:191], v228 offset:16384
	ds_read_b128 v[192:195], v228 offset:17408
	ds_read_b128 v[180:183], v228 offset:18432
	ds_read_b128 v[184:187], v228 offset:19456
	ds_read_b128 v[172:175], v228 offset:20480
	ds_read_b128 v[176:179], v228 offset:21504
	ds_read_b128 v[164:167], v228 offset:22528
	ds_read_b128 v[168:171], v228 offset:23552
	global_load_lds_dwordx4 v[218:219], off
	v_lshl_add_u64 v[220:221], s[64:65], 0, v[196:197]
	s_mov_b32 m0, s36
	s_addc_u32 s41, s65, 0
	global_load_lds_dwordx4 v[220:221], off
	v_lshl_add_u64 v[222:223], s[40:41], 0, v[2:3]
	s_mov_b32 m0, s37
	v_lshl_add_u64 v[224:225], s[74:75], 0, v[202:203]
	global_load_lds_dwordx4 v[222:223], off
	v_lshl_add_u64 v[222:223], s[40:41], 0, v[196:197]
	s_mov_b32 m0, s72
	v_cndmask_b32_e64 v229, 0, 1, s[78:79]
	global_load_lds_dwordx4 v[222:223], off
	v_lshl_add_u64 v[222:223], s[74:75], 0, v[204:205]
	s_mov_b32 m0, s19
	v_cmp_ne_u32_e64 s[40:41], 1, v229
	global_load_lds_dwordx4 v[222:223], off
	s_mov_b32 m0, s73
	s_andn2_b64 vcc, exec, s[78:79]
	global_load_lds_dwordx4 v[224:225], off
	s_cbranch_vccnz .LBB0_1130
	s_waitcnt vmcnt(24)
	s_cbranch_execnz .LBB0_1124

; #define PG8_STAGE(bufoff, gbase, voff) do { _Pragma("unroll") for (int _i = 0; _i < 2; ++_i) \
;         __builtin_amdgcn_global_load_lds((const unsigned*)((const char*)(gbase) + (voff)[_i]), (PG8_LAS unsigned*)(lds + (bufoff) + ldsw + _i * 8192), 16, 0, 0); } while (0)
; #define PG8_LDA(dst, b, h) do { _Pragma("unroll") for (int m = 0; m < 4; ++m) _Pragma("unroll") for (int k = 0; k < 2; ++k) dst[m][k] = *(const PG8_LAS bf16x8*)(lds + PG8_SA(b, h) + aoff + m * 2048 + k * 1024); } while (0)
; #define PG8_LDB(dst, b, h) do { _Pragma("unroll") for (int n = 0; n < 2; ++n) _Pragma("unroll") for (int k = 0; k < 2; ++k) dst[n][k] = *(const PG8_LAS bf16x8*)(lds + PG8_SB(b, h) + boff + n * 2048 + k * 1024); } while (0)
; #define PG8_MMA(ai, bj, At, Bt) do { __builtin_amdgcn_s_setprio(1); _Pragma("unroll") for (int m = 0; m < 4; ++m) _Pragma("unroll") for (int n = 0; n < 2; ++n) _Pragma("unroll") for (int k = 0; k < 2; ++k) \
;         acc[ai][bj][m][n] = mma16(Bt[n][k], At[m][k], acc[ai][bj][m][n]); __builtin_amdgcn_s_setprio(0); } while (0)
; #define PG8_WAIT_V(n) asm volatile("s_waitcnt vmcnt(" #n ")" ::: "memory")
; #define PG8_WAIT_VN(n) asm volatile("s_waitcnt vmcnt(%0)" :: "n"(n) : "memory")
; #define PG8_WAIT_L(n) asm volatile("s_waitcnt lgkmcnt(" #n ")" ::: "memory")
; #define PG8_BAR __builtin_amdgcn_s_barrier()
; #define PG8_SCHED __builtin_amdgcn_sched_barrier(0)
; template <class Epi, class Sched, bool ALIGN_EPI = false, bool SP2 = false>
; __device__ __forceinline__ void gemm_phase(PG8_LAS unsigned char* lds, const Gemm g, const Sched& S, const Epi& E, Stopwatch& sw) {
;     ...
;             if (relax) PG8_WAIT_VN(8 + Epi::NST); else PG8_WAIT_V(8); PG8_WAIT_L(0); PG8_BAR; PG8_MMA(1, 0, At, B0); PG8_MMA(1, 1, At, B1); PG8_BAR; PG8_SCHED;
;             PG8_LDB(B0, 1, 0); PG8_LDB(B1, 1, 1); PG8_SCHED; PG8_LDA(At, 1, 0); PG8_STAGE(PG8_SA(0, 1), a2 + hstep, voffA);
;             if (relax) PG8_WAIT_VN(8 + Epi::NST); else PG8_WAIT_V(8); PG8_WAIT_L(0); PG8_BAR; PG8_MMA(0, 0, At, B0); PG8_MMA(0, 1, At, B1); PG8_BAR; PG8_SCHED;
.LBB0_1124:
	s_waitcnt lgkmcnt(0)
	s_barrier
	s_setprio 1
	s_waitcnt lgkmcnt(0)
	v_mfma_i32_16x16x64_i8 v[96:99], v[148:151], v[188:191], v[96:99]
	v_mfma_i32_16x16x64_i8 v[92:95], v[156:159], v[188:191], v[92:95]
	v_mfma_i32_16x16x64_i8 v[88:91], v[148:151], v[180:183], v[88:91]
	v_mfma_i32_16x16x64_i8 v[84:87], v[156:159], v[180:183], v[84:87]
	v_mfma_i32_16x16x64_i8 v[80:83], v[148:151], v[172:175], v[80:83]
	v_mfma_i32_16x16x64_i8 v[72:75], v[156:159], v[172:175], v[72:75]
	v_mfma_i32_16x16x64_i8 v[64:67], v[148:151], v[164:167], v[64:67]
	v_mfma_i32_16x16x64_i8 v[56:59], v[156:159], v[164:167], v[56:59]
	v_mfma_i32_16x16x64_i8 v[96:99], v[152:155], v[192:195], v[96:99]
	v_mfma_i32_16x16x64_i8 v[92:95], v[160:163], v[192:195], v[92:95]
	v_mfma_i32_16x16x64_i8 v[88:91], v[152:155], v[184:187], v[88:91]
	v_mfma_i32_16x16x64_i8 v[84:87], v[160:163], v[184:187], v[84:87]
	v_mfma_i32_16x16x64_i8 v[80:83], v[152:155], v[176:179], v[80:83]
	v_mfma_i32_16x16x64_i8 v[72:75], v[160:163], v[176:179], v[72:75]
	v_mfma_i32_16x16x64_i8 v[64:67], v[152:155], v[168:171], v[64:67]
	v_mfma_i32_16x16x64_i8 v[56:59], v[160:163], v[168:171], v[56:59]
	v_mfma_i32_16x16x64_i8 v[32:35], v[132:135], v[188:191], v[32:35]
	v_mfma_i32_16x16x64_i8 v[28:31], v[140:143], v[188:191], v[28:31]
	v_mfma_i32_16x16x64_i8 v[24:27], v[132:135], v[180:183], v[24:27]
	v_mfma_i32_16x16x64_i8 v[20:23], v[140:143], v[180:183], v[20:23]
	v_mfma_i32_16x16x64_i8 v[16:19], v[132:135], v[172:175], v[16:19]
	v_mfma_i32_16x16x64_i8 v[12:15], v[140:143], v[172:175], v[12:15]
	v_mfma_i32_16x16x64_i8 v[8:11], v[132:135], v[164:167], v[8:11]
	v_mfma_i32_16x16x64_i8 v[4:7], v[140:143], v[164:167], v[4:7]
	v_mfma_i32_16x16x64_i8 v[32:35], v[136:139], v[192:195], v[32:35]
	v_mfma_i32_16x16x64_i8 v[28:31], v[144:147], v[192:195], v[28:31]
	v_mfma_i32_16x16x64_i8 v[24:27], v[136:139], v[184:187], v[24:27]
	v_mfma_i32_16x16x64_i8 v[20:23], v[144:147], v[184:187], v[20:23]
	v_mfma_i32_16x16x64_i8 v[16:19], v[136:139], v[176:179], v[16:19]
	v_mfma_i32_16x16x64_i8 v[12:15], v[144:147], v[176:179], v[12:15]
	v_mfma_i32_16x16x64_i8 v[8:11], v[136:139], v[168:171], v[8:11]
	v_mfma_i32_16x16x64_i8 v[4:7], v[144:147], v[168:171], v[4:7]
	s_setprio 0
	s_barrier
	v_add_u32_e32 v132, 0x18000, v227
	v_add_u32_e32 v144, 0x19000, v227
	ds_read_b128 v[148:151], v132
	ds_read_b128 v[152:155], v132 offset:1024
	ds_read_b128 v[156:159], v132 offset:2048
	ds_read_b128 v[160:163], v132 offset:3072
	ds_read_b128 v[132:135], v144
	ds_read_b128 v[136:139], v144 offset:1024
	ds_read_b128 v[140:143], v144 offset:2048
	ds_read_b128 v[144:147], v144 offset:3072
	s_add_u32 s74, s74, 0x40000
	s_addc_u32 s75, s75, 0
	s_mov_b32 m0, s80
	v_lshl_add_u64 v[230:231], s[74:75], 0, v[204:205]
	ds_read_b128 v[188:191], v228 offset:32768
	ds_read_b128 v[192:195], v228 offset:33792
	ds_read_b128 v[180:183], v228 offset:34816
	ds_read_b128 v[184:187], v228 offset:35840
	ds_read_b128 v[172:175], v228 offset:36864
	ds_read_b128 v[176:179], v228 offset:37888
	ds_read_b128 v[164:167], v228 offset:38912
	ds_read_b128 v[168:171], v228 offset:39936
	global_load_lds_dwordx4 v[230:231], off
	v_lshl_add_u64 v[230:231], s[74:75], 0, v[202:203]
	s_mov_b32 m0, s81
	s_and_b64 vcc, exec, s[40:41]
	global_load_lds_dwordx4 v[230:231], off
	s_cbranch_vccnz .LBB0_1131
	s_waitcnt vmcnt(24)
	s_mov_b64 s[74:75], s[10:11]
	s_cbranch_execnz .LBB0_1127

; #define PG8_STAGE(bufoff, gbase, voff) do { _Pragma("unroll") for (int _i = 0; _i < 2; ++_i) \
;         __builtin_amdgcn_global_load_lds((const unsigned*)((const char*)(gbase) + (voff)[_i]), (PG8_LAS unsigned*)(lds + (bufoff) + ldsw + _i * 8192), 16, 0, 0); } while (0)
; #define PG8_LDA(dst, b, h) do { _Pragma("unroll") for (int m = 0; m < 4; ++m) _Pragma("unroll") for (int k = 0; k < 2; ++k) dst[m][k] = *(const PG8_LAS bf16x8*)(lds + PG8_SA(b, h) + aoff + m * 2048 + k * 1024); } while (0)
; #define PG8_MMA(ai, bj, At, Bt) do { __builtin_amdgcn_s_setprio(1); _Pragma("unroll") for (int m = 0; m < 4; ++m) _Pragma("unroll") for (int n = 0; n < 2; ++n) _Pragma("unroll") for (int k = 0; k < 2; ++k) \
;         acc[ai][bj][m][n] = mma16(Bt[n][k], At[m][k], acc[ai][bj][m][n]); __builtin_amdgcn_s_setprio(0); } while (0)
; #define PG8_WAIT_V(n) asm volatile("s_waitcnt vmcnt(" #n ")" ::: "memory")
; #define PG8_WAIT_VN(n) asm volatile("s_waitcnt vmcnt(%0)" :: "n"(n) : "memory")
; #define PG8_WAIT_L(n) asm volatile("s_waitcnt lgkmcnt(" #n ")" ::: "memory")
; #define PG8_BAR __builtin_amdgcn_s_barrier()
; #define PG8_SCHED __builtin_amdgcn_sched_barrier(0)
; template <class Epi, class Sched, bool ALIGN_EPI = false, bool SP2 = false>
; __device__ __forceinline__ void gemm_phase(PG8_LAS unsigned char* lds, const Gemm g, const Sched& S, const Epi& E, Stopwatch& sw) {
;     ...
;             if (relax) PG8_WAIT_VN(8 + Epi::NST); else PG8_WAIT_V(8); PG8_WAIT_L(0); PG8_BAR; PG8_MMA(0, 0, At, B0); PG8_MMA(0, 1, At, B1); PG8_BAR; PG8_SCHED;
;             PG8_LDA(At, 1, 1); PG8_STAGE(PG8_SB(1, 0), b3, voffB); PG8_STAGE(PG8_SB(1, 1), b3 + hstep, voffB); PG8_STAGE(PG8_SA(1, 0), a3, voffA);
;             PG8_WAIT_V(8); PG8_WAIT_L(0); PG8_BAR; PG8_MMA(1, 0, At, B0); PG8_MMA(1, 1, At, B1); PG8_BAR; PG8_SCHED;
;             if (last && has_next) PG8_STAGE(PG8_SA(1, 1), a3 + hstep, voffA);
.LBB0_1127:
	s_waitcnt lgkmcnt(0)
	s_and_b64 s[40:41], s[38:39], s[68:69]
	s_barrier
	s_setprio 1
	s_waitcnt lgkmcnt(0)
	v_mfma_i32_16x16x64_i8 v[128:131], v[148:151], v[188:191], v[128:131]
	v_mfma_i32_16x16x64_i8 v[124:127], v[156:159], v[188:191], v[124:127]
	v_mfma_i32_16x16x64_i8 v[120:123], v[148:151], v[180:183], v[120:123]
	v_mfma_i32_16x16x64_i8 v[116:119], v[156:159], v[180:183], v[116:119]
	v_mfma_i32_16x16x64_i8 v[112:115], v[148:151], v[172:175], v[112:115]
	v_mfma_i32_16x16x64_i8 v[108:111], v[156:159], v[172:175], v[108:111]
	v_mfma_i32_16x16x64_i8 v[104:107], v[148:151], v[164:167], v[104:107]
	v_mfma_i32_16x16x64_i8 v[100:103], v[156:159], v[164:167], v[100:103]
	v_mfma_i32_16x16x64_i8 v[128:131], v[152:155], v[192:195], v[128:131]
	v_mfma_i32_16x16x64_i8 v[124:127], v[160:163], v[192:195], v[124:127]
	v_mfma_i32_16x16x64_i8 v[120:123], v[152:155], v[184:187], v[120:123]
	v_mfma_i32_16x16x64_i8 v[116:119], v[160:163], v[184:187], v[116:119]
	v_mfma_i32_16x16x64_i8 v[112:115], v[152:155], v[176:179], v[112:115]
	v_mfma_i32_16x16x64_i8 v[108:111], v[160:163], v[176:179], v[108:111]
	v_mfma_i32_16x16x64_i8 v[104:107], v[152:155], v[168:171], v[104:107]
	v_mfma_i32_16x16x64_i8 v[100:103], v[160:163], v[168:171], v[100:103]
	v_mfma_i32_16x16x64_i8 v[76:79], v[132:135], v[188:191], v[76:79]
	v_mfma_i32_16x16x64_i8 v[68:71], v[140:143], v[188:191], v[68:71]
	v_mfma_i32_16x16x64_i8 v[60:63], v[132:135], v[180:183], v[60:63]
	v_mfma_i32_16x16x64_i8 v[52:55], v[140:143], v[180:183], v[52:55]
	v_mfma_i32_16x16x64_i8 v[48:51], v[132:135], v[172:175], v[48:51]
	v_mfma_i32_16x16x64_i8 v[44:47], v[140:143], v[172:175], v[44:47]
	v_mfma_i32_16x16x64_i8 v[40:43], v[132:135], v[164:167], v[40:43]
	v_mfma_i32_16x16x64_i8 v[36:39], v[140:143], v[164:167], v[36:39]
	v_mfma_i32_16x16x64_i8 v[76:79], v[136:139], v[192:195], v[76:79]
	v_mfma_i32_16x16x64_i8 v[68:71], v[144:147], v[192:195], v[68:71]
	v_mfma_i32_16x16x64_i8 v[60:63], v[136:139], v[184:187], v[60:63]
	v_mfma_i32_16x16x64_i8 v[52:55], v[144:147], v[184:187], v[52:55]
	v_mfma_i32_16x16x64_i8 v[48:51], v[136:139], v[176:179], v[48:51]
	v_mfma_i32_16x16x64_i8 v[44:47], v[144:147], v[176:179], v[44:47]
	v_mfma_i32_16x16x64_i8 v[40:43], v[136:139], v[168:171], v[40:43]
	v_mfma_i32_16x16x64_i8 v[36:39], v[144:147], v[168:171], v[36:39]
	s_setprio 0
	s_barrier
	s_mov_b32 m0, s34
	v_lshl_add_u64 v[218:219], v[218:219], 0, s[20:21]
	s_add_u32 s64, s64, 0x40080
	ds_read_b128 v[164:167], v228 offset:49152
	ds_read_b128 v[168:171], v228 offset:50176
	ds_read_b128 v[172:175], v228 offset:51200
	ds_read_b128 v[176:179], v228 offset:52224
	ds_read_b128 v[180:183], v228 offset:53248
	ds_read_b128 v[184:187], v228 offset:54272
	ds_read_b128 v[188:191], v228 offset:55296
	ds_read_b128 v[192:195], v228 offset:56320
	global_load_lds_dwordx4 v[218:219], off
	v_lshl_add_u64 v[218:219], v[220:221], 0, s[20:21]
	s_mov_b32 m0, s82
	s_addc_u32 s65, s65, 0
	global_load_lds_dwordx4 v[218:219], off
	v_lshl_add_u64 v[218:219], s[64:65], 0, v[2:3]
	s_mov_b32 m0, s94
	s_nop 0
	global_load_lds_dwordx4 v[218:219], off
	v_lshl_add_u64 v[218:219], s[64:65], 0, v[196:197]
	s_mov_b32 m0, s95
	s_nop 0
	global_load_lds_dwordx4 v[218:219], off
	v_lshl_add_u64 v[218:219], v[222:223], 0, s[20:21]
	s_mov_b32 m0, s83
	s_nop 0
	global_load_lds_dwordx4 v[218:219], off
	v_lshl_add_u64 v[218:219], v[224:225], 0, s[20:21]
	s_mov_b32 m0, s90
	s_nop 0
	global_load_lds_dwordx4 v[218:219], off
	s_waitcnt vmcnt(8)
	s_waitcnt lgkmcnt(0)
	s_barrier
	s_setprio 1
	s_waitcnt lgkmcnt(0)
	v_mfma_i32_16x16x64_i8 v[96:99], v[148:151], v[164:167], v[96:99]
	v_mfma_i32_16x16x64_i8 v[92:95], v[156:159], v[164:167], v[92:95]
	v_mfma_i32_16x16x64_i8 v[88:91], v[148:151], v[172:175], v[88:91]
	v_mfma_i32_16x16x64_i8 v[84:87], v[156:159], v[172:175], v[84:87]
	v_mfma_i32_16x16x64_i8 v[80:83], v[148:151], v[180:183], v[80:83]
	v_mfma_i32_16x16x64_i8 v[72:75], v[156:159], v[180:183], v[72:75]
	v_mfma_i32_16x16x64_i8 v[64:67], v[148:151], v[188:191], v[64:67]
	v_mfma_i32_16x16x64_i8 v[56:59], v[156:159], v[188:191], v[56:59]
	v_mfma_i32_16x16x64_i8 v[96:99], v[152:155], v[168:171], v[96:99]
	v_mfma_i32_16x16x64_i8 v[92:95], v[160:163], v[168:171], v[92:95]
	v_mfma_i32_16x16x64_i8 v[88:91], v[152:155], v[176:179], v[88:91]
	v_mfma_i32_16x16x64_i8 v[84:87], v[160:163], v[176:179], v[84:87]
	v_mfma_i32_16x16x64_i8 v[80:83], v[152:155], v[184:187], v[80:83]
	v_mfma_i32_16x16x64_i8 v[72:75], v[160:163], v[184:187], v[72:75]
	v_mfma_i32_16x16x64_i8 v[64:67], v[152:155], v[192:195], v[64:67]
	v_mfma_i32_16x16x64_i8 v[56:59], v[160:163], v[192:195], v[56:59]
	v_mfma_i32_16x16x64_i8 v[32:35], v[132:135], v[164:167], v[32:35]
	v_mfma_i32_16x16x64_i8 v[28:31], v[140:143], v[164:167], v[28:31]
	v_mfma_i32_16x16x64_i8 v[24:27], v[132:135], v[172:175], v[24:27]
	v_mfma_i32_16x16x64_i8 v[20:23], v[140:143], v[172:175], v[20:23]
	v_mfma_i32_16x16x64_i8 v[16:19], v[132:135], v[180:183], v[16:19]
	v_mfma_i32_16x16x64_i8 v[12:15], v[140:143], v[180:183], v[12:15]
	v_mfma_i32_16x16x64_i8 v[8:11], v[132:135], v[188:191], v[8:11]
	v_mfma_i32_16x16x64_i8 v[4:7], v[140:143], v[188:191], v[4:7]
	v_mfma_i32_16x16x64_i8 v[32:35], v[136:139], v[168:171], v[32:35]
	v_mfma_i32_16x16x64_i8 v[28:31], v[144:147], v[168:171], v[28:31]
	v_mfma_i32_16x16x64_i8 v[24:27], v[136:139], v[176:179], v[24:27]
	v_mfma_i32_16x16x64_i8 v[20:23], v[144:147], v[176:179], v[20:23]
	v_mfma_i32_16x16x64_i8 v[16:19], v[136:139], v[184:187], v[16:19]
	v_mfma_i32_16x16x64_i8 v[12:15], v[144:147], v[184:187], v[12:15]
	v_mfma_i32_16x16x64_i8 v[8:11], v[136:139], v[192:195], v[8:11]
	v_mfma_i32_16x16x64_i8 v[4:7], v[144:147], v[192:195], v[4:7]
	s_setprio 0
	s_barrier
	s_andn2_b64 vcc, exec, s[40:41]
	s_cbranch_vccnz .LBB0_1117
	s_add_i32 m0, s19, 0xc000
	s_nop 0
	global_load_lds_dwordx4 v[210:211], off
	s_add_i32 m0, s19, 0xe000
	s_nop 0
	global_load_lds_dwordx4 v[212:213], off
	s_branch .LBB0_1117

;     __device__ __forceinline__ void operator()(const i32x4 (&acc)[2][2][4][2], const Unit& u, int wr, int wc, int fr, int fq) const {
;         const int row0 = u.pm * BM + wr * 64 + fr, col0 = u.pn * BM + wc * 32 + 8 * fq;
;         float rr[2][4]; f32x4 cc[2][2];
; #pragma unroll
;         for (int ai = 0; ai < 2; ++ai)
; #pragma unroll
;             for (int m = 0; m < 4; ++m) rr[ai][m] = rq[row0 + ai * HALF + m * 16];
; #pragma unroll
;         for (int bj = 0; bj < 2; ++bj) { cc[bj][0] = *(const f32x4*)(cmax + col0 + bj * HALF) * (1.0f / 127.0f); cc[bj][1] = *(const f32x4*)(cmax + col0 + bj * HALF + 4) * (1.0f / 127.0f); }
;     ...
;                     f32x4 v0 = __builtin_convertvector(acc[ai][bj][m][0], f32x4) * (cc[bj][0] * rr[ai][m]), v1 = __builtin_convertvector(acc[ai][bj][m][1], f32x4) * (cc[bj][1] * rr[ai][m]);
.LBB0_1134:
	v_lshl_add_u32 v170, s4, 8, v1
	v_or_b32_e32 v168, 16, v170
	v_ashrrev_i32_e32 v171, 31, v170
	v_ashrrev_i32_e32 v169, 31, v168
	v_or_b32_e32 v166, 32, v170
	s_mov_b32 s100, 0x20000
	s_mov_b32 s101, 0
	v_bfe_i32 v233, v234, 3, 1
	v_and_b32_e32 v232, 0xfffe0040, v233
	v_lshl_add_u64 v[132:133], v[170:171], 2, s[22:23]
	v_lshl_add_u64 v[134:135], v[168:169], 2, s[22:23]
	v_ashrrev_i32_e32 v167, 31, v166
	v_or_b32_e32 v164, 48, v170
	v_lshl_or_b32 v176, s31, 8, v226
	global_load_dword v154, v[132:133], off
	global_load_dword v152, v[134:135], off
	v_lshl_add_u64 v[134:135], v[166:167], 2, s[22:23]
	v_ashrrev_i32_e32 v165, 31, v164
	v_ashrrev_i32_e32 v177, 31, v176
	global_load_dword v150, v[134:135], off
	v_lshl_add_u64 v[134:135], v[164:165], 2, s[22:23]
	v_lshl_add_u64 v[136:137], v[176:177], 2, s[46:47]
	global_load_dword v148, v[134:135], off
	global_load_dword v146, v[132:133], off offset:512
	global_load_dword v138, v[132:133], off offset:576
	s_nop 0
	global_load_dword v134, v[132:133], off offset:640
	s_nop 0
	global_load_dword v132, v[132:133], off offset:704
	s_nop 0
	global_load_dwordx4 v[140:143], v[136:137], off offset:16
	global_load_dwordx4 v[156:159], v[136:137], off
	v_cvt_f32_i32_e32 v129, v129
	v_cvt_f32_i32_e32 v128, v128
	v_cvt_f32_i32_e32 v131, v131
	v_cvt_f32_i32_e32 v130, v130
	v_cvt_f32_i32_e32 v125, v125
	v_cvt_f32_i32_e32 v124, v124
	v_cvt_f32_i32_e32 v127, v127
	v_cvt_f32_i32_e32 v126, v126
	v_cvt_f32_i32_e32 v117, v117
	v_cvt_f32_i32_e32 v116, v116
	v_cvt_f32_i32_e32 v119, v119
	v_cvt_f32_i32_e32 v118, v118
	v_cvt_f32_i32_e32 v113, v113
	v_cvt_f32_i32_e32 v112, v112
	v_cvt_f32_i32_e32 v115, v115
	v_cvt_f32_i32_e32 v114, v114
	v_cvt_f32_i32_e32 v109, v109
	v_cvt_f32_i32_e32 v108, v108
	v_cvt_f32_i32_e32 v111, v111
	v_cvt_f32_i32_e32 v110, v110
	v_cvt_f32_i32_e32 v105, v105
	v_cvt_f32_i32_e32 v104, v104
	v_cvt_f32_i32_e32 v107, v107
	v_cvt_f32_i32_e32 v106, v106
	v_cvt_f32_i32_e32 v101, v101
	v_cvt_f32_i32_e32 v100, v100
	v_cvt_f32_i32_e32 v103, v103
	v_cvt_f32_i32_e32 v102, v102
	v_cvt_f32_i32_e32 v97, v97
	v_cvt_f32_i32_e32 v96, v96
	v_cvt_f32_i32_e32 v99, v99
	v_cvt_f32_i32_e32 v98, v98
	v_cvt_f32_i32_e32 v93, v93
	v_cvt_f32_i32_e32 v92, v92
	v_cvt_f32_i32_e32 v95, v95
	v_cvt_f32_i32_e32 v94, v94
	s_mov_b32 s0, 0x200000
	v_cvt_f32_i32_e32 v89, v89
	v_cvt_f32_i32_e32 v88, v88
	v_cvt_f32_i32_e32 v91, v91
	v_cvt_f32_i32_e32 v90, v90
	v_cvt_f32_i32_e32 v85, v85
	v_cvt_f32_i32_e32 v84, v84
	v_cvt_f32_i32_e32 v87, v87
	v_cvt_f32_i32_e32 v86, v86
	v_cvt_f32_i32_e32 v83, v83
	v_cvt_f32_i32_e32 v82, v82
	v_cvt_f32_i32_e32 v81, v81
	v_cvt_f32_i32_e32 v80, v80
	v_cvt_f32_i32_e32 v75, v75
	v_cvt_f32_i32_e32 v74, v74
	v_cvt_f32_i32_e32 v73, v73
	v_cvt_f32_i32_e32 v72, v72
	v_cvt_f32_i32_e32 v67, v67
	v_cvt_f32_i32_e32 v66, v66
	v_cvt_f32_i32_e32 v65, v65
	v_cvt_f32_i32_e32 v64, v64
	v_cvt_f32_i32_e32 v59, v59
	v_cvt_f32_i32_e32 v58, v58
	v_cvt_f32_i32_e32 v57, v57
	v_cvt_f32_i32_e32 v56, v56
	v_cvt_f32_i32_e32 v53, v53
	v_cvt_f32_i32_e32 v52, v52
	v_cvt_f32_i32_e32 v55, v55
	v_cvt_f32_i32_e32 v54, v54
	v_cvt_f32_i32_e32 v49, v49
	v_cvt_f32_i32_e32 v48, v48
	v_cvt_f32_i32_e32 v51, v51
	v_cvt_f32_i32_e32 v50, v50
	v_cvt_f32_i32_e32 v45, v45
	v_cvt_f32_i32_e32 v44, v44
	v_cvt_f32_i32_e32 v47, v47
	v_cvt_f32_i32_e32 v46, v46
	v_cvt_f32_i32_e32 v41, v41
	v_cvt_f32_i32_e32 v40, v40
	v_cvt_f32_i32_e32 v43, v43
	v_cvt_f32_i32_e32 v42, v42
	v_cvt_f32_i32_e32 v37, v37
	v_cvt_f32_i32_e32 v36, v36
	s_waitcnt vmcnt(0)
	v_pk_mul_f32 v[160:161], v[158:159], s[30:31] op_sel_hi:[1,0]
	v_pk_mul_f32 v[162:163], v[156:157], s[30:31] op_sel_hi:[1,0]
	v_pk_mul_f32 v[156:157], v[142:143], s[30:31] op_sel_hi:[1,0]
	v_pk_mul_f32 v[158:159], v[140:141], s[30:31] op_sel_hi:[1,0]
	global_load_dwordx4 v[172:175], v[136:137], off offset:144
	global_load_dwordx4 v[140:143], v[136:137], off offset:128
	v_cvt_f32_i32_e32 v39, v39
	v_cvt_f32_i32_e32 v38, v38
	v_cvt_f32_i32_e32 v33, v33
	v_cvt_f32_i32_e32 v32, v32
	v_cvt_f32_i32_e32 v35, v35
	v_cvt_f32_i32_e32 v34, v34
	v_cvt_f32_i32_e32 v29, v29
	v_cvt_f32_i32_e32 v28, v28
	v_cvt_f32_i32_e32 v31, v31
	v_cvt_f32_i32_e32 v30, v30
	v_cvt_f32_i32_e32 v25, v25
	v_cvt_f32_i32_e32 v24, v24
	s_mov_b64 s[40:41], 0x200000
	v_cvt_f32_i32_e32 v27, v27
	v_cvt_f32_i32_e32 v26, v26
	v_cvt_f32_i32_e32 v21, v21
	v_cvt_f32_i32_e32 v20, v20
	v_cvt_f32_i32_e32 v23, v23
	v_cvt_f32_i32_e32 v22, v22
	v_cvt_f32_i32_e32 v17, v17
	v_cvt_f32_i32_e32 v16, v16
	v_cvt_f32_i32_e32 v19, v19
	v_cvt_f32_i32_e32 v18, v18
	v_cvt_f32_i32_e32 v13, v13
	v_cvt_f32_i32_e32 v12, v12
	v_cvt_f32_i32_e32 v15, v15
	v_cvt_f32_i32_e32 v14, v14
	v_cvt_f32_i32_e32 v9, v9
	v_cvt_f32_i32_e32 v8, v8
	v_cvt_f32_i32_e32 v11, v11
	v_cvt_f32_i32_e32 v10, v10
	v_cvt_f32_i32_e32 v5, v5
	v_cvt_f32_i32_e32 v4, v4
	v_cvt_f32_i32_e32 v7, v7
	v_cvt_f32_i32_e32 v6, v6
	s_waitcnt vmcnt(0)
; __device__ __forceinline__ unsigned cvt_pk_bf16(float lo, float hi) { f32x2c v = {lo, hi}; bf16x2c b = __builtin_convertvector(v, bf16x2c); return __builtin_bit_cast(unsigned, b); }
;     __device__ __forceinline__ void operator()(const i32x4 (&acc)[2][2][4][2], const Unit& u, int wr, int wc, int fr, int fq) const {
;     ...
; #pragma unroll
;         for (int bj = 0; bj < 2; ++bj)
; #pragma unroll
;             for (int ai = 0; ai < 2; ++ai)
; #pragma unroll
;                 for (int m = 0; m < 4; ++m) { const int row = row0 + ai * HALF + m * 16;
;                     f32x4 v0 = __builtin_convertvector(acc[ai][bj][m][0], f32x4) * (cc[bj][0] * rr[ai][m]), v1 = __builtin_convertvector(acc[ai][bj][m][1], f32x4) * (cc[bj][1] * rr[ai][m]);
; #pragma unroll
;                     for (int j = 0; j < 4; ++j) { const float a = __builtin_fmaxf(v0[j], 0.f), b = __builtin_fmaxf(v1[j], 0.f); v0[j] = a * a; v1[j] = b * b; }
;                     u32x4 w; w.x = cvt_pk_bf16(v0[0], v0[1]); w.y = cvt_pk_bf16(v0[2], v0[3]); w.z = cvt_pk_bf16(v1[0], v1[1]); w.w = cvt_pk_bf16(v1[2], v1[3]);
;                     *(u32x4*)(O + (size_t)row * ldc + col0 + bj * HALF) = w; }
	v_pk_mul_f32 v[136:137], v[174:175], s[30:31] op_sel_hi:[1,0]
	v_pk_mul_f32 v[144:145], v[140:141], s[30:31] op_sel_hi:[1,0]
	v_pk_mul_f32 v[140:141], v[172:173], s[30:31] op_sel_hi:[1,0]
	v_pk_mul_f32 v[172:173], v[154:155], v[162:163] op_sel_hi:[0,1]
	v_pk_mul_f32 v[174:175], v[154:155], v[160:161] op_sel_hi:[0,1]
	v_pk_mul_f32 v[128:129], v[172:173], v[128:129]
	v_pk_mul_f32 v[172:173], v[154:155], v[158:159] op_sel_hi:[0,1]
	v_pk_mul_f32 v[130:131], v[174:175], v[130:131]
	v_pk_mul_f32 v[174:175], v[154:155], v[156:157] op_sel_hi:[0,1]
	v_pk_mul_f32 v[124:125], v[172:173], v[124:125]
	v_pk_mul_f32 v[126:127], v[174:175], v[126:127]
	v_max_f32_e32 v128, 0, v128
	v_max_f32_e32 v124, 0, v124
	v_max_f32_e32 v129, 0, v129
	v_max_f32_e32 v125, 0, v125
	v_max_f32_e32 v130, 0, v130
	v_max_f32_e32 v131, 0, v131
	v_pk_mul_f32 v[128:129], v[128:129], v[128:129]
	v_pk_mul_f32 v[124:125], v[124:125], v[124:125]
	v_max_f32_e32 v126, 0, v126
	v_max_f32_e32 v127, 0, v127
	v_pk_mul_f32 v[130:131], v[130:131], v[130:131]
	v_pk_mul_f32 v[126:127], v[126:127], v[126:127]
	v_cvt_pk_bf16_f32 v128, v128, v129
	v_cvt_pk_bf16_f32 v129, v130, v131
	v_cvt_pk_bf16_f32 v130, v124, v125
	v_lshlrev_b64 v[124:125], 14, v[170:171]
	v_cvt_pk_bf16_f32 v131, v126, v127
	v_lshl_add_u64 v[124:125], s[14:15], 0, v[124:125]
	v_lshlrev_b64 v[126:127], 1, v[176:177]
	v_lshl_add_u64 v[124:125], v[124:125], 0, v[126:127]
	v_mov_b64_e32 v[178:179], v[128:129]
	v_mov_b64_e32 v[180:181], v[130:131]
	v_pk_mul_f32 v[142:143], v[142:143], s[30:31] op_sel_hi:[1,0]
	s_nop 0
	v_cvt_f32_i32_e32 v129, v121
	v_cvt_f32_i32_e32 v128, v120
	v_cvt_f32_i32_e32 v121, v123
	v_cvt_f32_i32_e32 v120, v122
	v_pk_mul_f32 v[122:123], v[152:153], v[162:163] op_sel_hi:[0,1]
	v_pk_mul_f32 v[130:131], v[152:153], v[160:161] op_sel_hi:[0,1]
	v_pk_mul_f32 v[122:123], v[122:123], v[128:129]
	v_pk_mul_f32 v[128:129], v[152:153], v[158:159] op_sel_hi:[0,1]
	v_pk_mul_f32 v[120:121], v[130:131], v[120:121]
	v_pk_mul_f32 v[130:131], v[152:153], v[156:157] op_sel_hi:[0,1]
	v_pk_mul_f32 v[116:117], v[128:129], v[116:117]
	v_pk_mul_f32 v[118:119], v[130:131], v[118:119]
	v_max_f32_e32 v116, 0, v116
	v_max_f32_e32 v117, 0, v117
	v_max_f32_e32 v120, 0, v120
	v_max_f32_e32 v121, 0, v121
	v_pk_mul_f32 v[116:117], v[116:117], v[116:117]
	v_max_f32_e32 v118, 0, v118
	v_max_f32_e32 v119, 0, v119
	v_pk_mul_f32 v[120:121], v[120:121], v[120:121]
	v_max_f32_e32 v122, 0, v122
	v_max_f32_e32 v123, 0, v123
	v_pk_mul_f32 v[128:129], v[118:119], v[118:119]
	v_cvt_pk_bf16_f32 v119, v120, v121
	v_cvt_pk_bf16_f32 v120, v116, v117
	v_lshlrev_b64 v[116:117], 14, v[168:169]
	v_pk_mul_f32 v[122:123], v[122:123], v[122:123]
	v_lshl_add_u64 v[116:117], s[14:15], 0, v[116:117]
	v_cvt_pk_bf16_f32 v118, v122, v123
	v_cvt_pk_bf16_f32 v121, v128, v129
	v_lshl_add_u64 v[116:117], v[116:117], 0, v[126:127]
	v_mov_b64_e32 v[182:183], v[118:119]
	v_mov_b64_e32 v[184:185], v[120:121]
	s_nop 1
	v_pk_mul_f32 v[118:119], v[150:151], v[162:163] op_sel_hi:[0,1]
	v_pk_mul_f32 v[120:121], v[150:151], v[160:161] op_sel_hi:[0,1]
	v_pk_mul_f32 v[112:113], v[118:119], v[112:113]
	v_pk_mul_f32 v[118:119], v[150:151], v[158:159] op_sel_hi:[0,1]
	v_pk_mul_f32 v[114:115], v[120:121], v[114:115]
	v_pk_mul_f32 v[120:121], v[150:151], v[156:157] op_sel_hi:[0,1]
	v_pk_mul_f32 v[108:109], v[118:119], v[108:109]
	v_pk_mul_f32 v[110:111], v[120:121], v[110:111]
	v_max_f32_e32 v112, 0, v112
	v_max_f32_e32 v108, 0, v108
	v_max_f32_e32 v113, 0, v113
	v_max_f32_e32 v109, 0, v109
	v_pk_mul_f32 v[112:113], v[112:113], v[112:113]
	v_pk_mul_f32 v[108:109], v[108:109], v[108:109]
	v_max_f32_e32 v110, 0, v110
	v_max_f32_e32 v111, 0, v111
	v_max_f32_e32 v114, 0, v114
	v_max_f32_e32 v115, 0, v115
	v_pk_mul_f32 v[118:119], v[110:111], v[110:111]
	v_cvt_pk_bf16_f32 v110, v112, v113
	v_cvt_pk_bf16_f32 v112, v108, v109
	v_lshlrev_b64 v[108:109], 14, v[166:167]
	v_pk_mul_f32 v[114:115], v[114:115], v[114:115]
	v_lshl_add_u64 v[108:109], s[14:15], 0, v[108:109]
	v_cvt_pk_bf16_f32 v111, v114, v115
	v_cvt_pk_bf16_f32 v113, v118, v119
	v_lshl_add_u64 v[108:109], v[108:109], 0, v[126:127]
	v_mov_b64_e32 v[186:187], v[110:111]
	v_mov_b64_e32 v[188:189], v[112:113]
	s_nop 1
	v_pk_mul_f32 v[110:111], v[148:149], v[162:163] op_sel_hi:[0,1]
	v_pk_mul_f32 v[112:113], v[148:149], v[160:161] op_sel_hi:[0,1]
	v_pk_mul_f32 v[104:105], v[110:111], v[104:105]
	v_pk_mul_f32 v[110:111], v[148:149], v[158:159] op_sel_hi:[0,1]
	v_pk_mul_f32 v[106:107], v[112:113], v[106:107]
	v_pk_mul_f32 v[112:113], v[148:149], v[156:157] op_sel_hi:[0,1]
	v_pk_mul_f32 v[100:101], v[110:111], v[100:101]
	v_pk_mul_f32 v[102:103], v[112:113], v[102:103]
	v_max_f32_e32 v104, 0, v104
	v_max_f32_e32 v100, 0, v100
	v_max_f32_e32 v105, 0, v105
	v_max_f32_e32 v101, 0, v101
	v_pk_mul_f32 v[104:105], v[104:105], v[104:105]
	v_pk_mul_f32 v[100:101], v[100:101], v[100:101]
	v_max_f32_e32 v102, 0, v102
	v_max_f32_e32 v103, 0, v103
	v_max_f32_e32 v106, 0, v106
	v_max_f32_e32 v107, 0, v107
	v_pk_mul_f32 v[110:111], v[102:103], v[102:103]
	v_cvt_pk_bf16_f32 v102, v104, v105
	v_cvt_pk_bf16_f32 v104, v100, v101
	v_lshlrev_b64 v[100:101], 14, v[164:165]
	v_pk_mul_f32 v[106:107], v[106:107], v[106:107]
	v_lshl_add_u64 v[100:101], s[14:15], 0, v[100:101]
	v_cvt_pk_bf16_f32 v103, v106, v107
	v_cvt_pk_bf16_f32 v105, v110, v111
	v_lshl_add_u64 v[100:101], v[100:101], 0, v[126:127]
	v_mov_b64_e32 v[190:191], v[102:103]
	v_mov_b64_e32 v[192:193], v[104:105]
	s_nop 1
	v_pk_mul_f32 v[102:103], v[146:147], v[162:163] op_sel_hi:[0,1]
	v_pk_mul_f32 v[104:105], v[146:147], v[160:161] op_sel_hi:[0,1]
	v_pk_mul_f32 v[98:99], v[104:105], v[98:99]
; __device__ __forceinline__ unsigned cvt_pk_bf16(float lo, float hi) { f32x2c v = {lo, hi}; bf16x2c b = __builtin_convertvector(v, bf16x2c); return __builtin_bit_cast(unsigned, b); }
;     __device__ __forceinline__ void operator()(const i32x4 (&acc)[2][2][4][2], const Unit& u, int wr, int wc, int fr, int fq) const {
;     ...
; #pragma unroll
;         for (int bj = 0; bj < 2; ++bj)
; #pragma unroll
;             for (int ai = 0; ai < 2; ++ai)
; #pragma unroll
;                 for (int m = 0; m < 4; ++m) { const int row = row0 + ai * HALF + m * 16;
;                     f32x4 v0 = __builtin_convertvector(acc[ai][bj][m][0], f32x4) * (cc[bj][0] * rr[ai][m]), v1 = __builtin_convertvector(acc[ai][bj][m][1], f32x4) * (cc[bj][1] * rr[ai][m]);
; #pragma unroll
;                     for (int j = 0; j < 4; ++j) { const float a = __builtin_fmaxf(v0[j], 0.f), b = __builtin_fmaxf(v1[j], 0.f); v0[j] = a * a; v1[j] = b * b; }
;                     u32x4 w; w.x = cvt_pk_bf16(v0[0], v0[1]); w.y = cvt_pk_bf16(v0[2], v0[3]); w.z = cvt_pk_bf16(v1[0], v1[1]); w.w = cvt_pk_bf16(v1[2], v1[3]);
;                     *(u32x4*)(O + (size_t)row * ldc + col0 + bj * HALF) = w; }
	v_pk_mul_f32 v[96:97], v[102:103], v[96:97]
	v_pk_mul_f32 v[102:103], v[146:147], v[158:159] op_sel_hi:[0,1]
	v_pk_mul_f32 v[104:105], v[146:147], v[156:157] op_sel_hi:[0,1]
	v_pk_mul_f32 v[94:95], v[104:105], v[94:95]
	v_pk_mul_f32 v[92:93], v[102:103], v[92:93]
	v_max_f32_e32 v98, 0, v98
	v_max_f32_e32 v99, 0, v99
	v_max_f32_e32 v96, 0, v96
	v_max_f32_e32 v92, 0, v92
	v_max_f32_e32 v97, 0, v97
	v_max_f32_e32 v93, 0, v93
	v_max_f32_e32 v94, 0, v94
	v_max_f32_e32 v95, 0, v95
	v_pk_mul_f32 v[98:99], v[98:99], v[98:99]
	v_pk_mul_f32 v[96:97], v[96:97], v[96:97]
	v_pk_mul_f32 v[92:93], v[92:93], v[92:93]
	v_pk_mul_f32 v[102:103], v[94:95], v[94:95]
	v_cvt_pk_bf16_f32 v95, v98, v99
	v_add_co_u32_e32 v98, vcc, s0, v124
	v_cvt_pk_bf16_f32 v94, v96, v97
	v_cvt_pk_bf16_f32 v96, v92, v93
	v_cvt_pk_bf16_f32 v97, v102, v103
	v_addc_co_u32_e32 v99, vcc, 0, v125, vcc
	v_mov_b64_e32 v[210:211], v[94:95]
	v_mov_b64_e32 v[212:213], v[96:97]
	s_mov_b32 s0, 0x240000
	v_lshl_add_u64 v[92:93], v[124:125], 0, s[40:41]
	v_pk_mul_f32 v[94:95], v[138:139], v[162:163] op_sel_hi:[0,1]
	v_pk_mul_f32 v[96:97], v[138:139], v[160:161] op_sel_hi:[0,1]
	v_pk_mul_f32 v[90:91], v[96:97], v[90:91]
	v_pk_mul_f32 v[88:89], v[94:95], v[88:89]
	v_pk_mul_f32 v[94:95], v[138:139], v[158:159] op_sel_hi:[0,1]
	v_pk_mul_f32 v[96:97], v[138:139], v[156:157] op_sel_hi:[0,1]
	v_pk_mul_f32 v[86:87], v[96:97], v[86:87]
	v_pk_mul_f32 v[84:85], v[94:95], v[84:85]
	v_max_f32_e32 v90, 0, v90
	v_max_f32_e32 v91, 0, v91
	v_max_f32_e32 v88, 0, v88
	v_max_f32_e32 v84, 0, v84
	v_max_f32_e32 v89, 0, v89
	v_max_f32_e32 v85, 0, v85
	v_max_f32_e32 v86, 0, v86
	v_max_f32_e32 v87, 0, v87
	v_pk_mul_f32 v[90:91], v[90:91], v[90:91]
	v_pk_mul_f32 v[88:89], v[88:89], v[88:89]
	v_pk_mul_f32 v[84:85], v[84:85], v[84:85]
	v_pk_mul_f32 v[94:95], v[86:87], v[86:87]
	v_cvt_pk_bf16_f32 v87, v90, v91
	v_add_co_u32_e32 v90, vcc, s0, v124
	v_cvt_pk_bf16_f32 v86, v88, v89
	v_cvt_pk_bf16_f32 v88, v84, v85
	v_cvt_pk_bf16_f32 v89, v94, v95
	v_addc_co_u32_e32 v91, vcc, 0, v125, vcc
	v_mov_b64_e32 v[214:215], v[86:87]
	v_mov_b64_e32 v[216:217], v[88:89]
	s_mov_b32 s0, 0x280000
	s_mov_b64 s[40:41], 0x240000
	v_pk_mul_f32 v[88:89], v[134:135], v[160:161] op_sel_hi:[0,1]
	v_pk_mul_f32 v[86:87], v[134:135], v[162:163] op_sel_hi:[0,1]
	v_pk_mul_f32 v[82:83], v[88:89], v[82:83]
	v_pk_mul_f32 v[88:89], v[134:135], v[156:157] op_sel_hi:[0,1]
	v_pk_mul_f32 v[80:81], v[86:87], v[80:81]
	v_pk_mul_f32 v[86:87], v[134:135], v[158:159] op_sel_hi:[0,1]
	v_pk_mul_f32 v[74:75], v[88:89], v[74:75]
	v_pk_mul_f32 v[72:73], v[86:87], v[72:73]
	v_max_f32_e32 v80, 0, v80
	v_max_f32_e32 v81, 0, v81
	v_max_f32_e32 v82, 0, v82
	v_max_f32_e32 v74, 0, v74
	v_max_f32_e32 v83, 0, v83
	v_max_f32_e32 v75, 0, v75
	v_max_f32_e32 v72, 0, v72
	v_max_f32_e32 v73, 0, v73
	v_pk_mul_f32 v[80:81], v[80:81], v[80:81]
	v_pk_mul_f32 v[82:83], v[82:83], v[82:83]
	v_pk_mul_f32 v[74:75], v[74:75], v[74:75]
	v_pk_mul_f32 v[72:73], v[72:73], v[72:73]
	v_cvt_pk_bf16_f32 v80, v80, v81
	v_cvt_pk_bf16_f32 v81, v82, v83
	v_cvt_pk_bf16_f32 v83, v74, v75
	v_add_co_u32_e32 v74, vcc, s0, v124
	v_cvt_pk_bf16_f32 v82, v72, v73
	s_nop 0
	v_addc_co_u32_e32 v75, vcc, 0, v125, vcc
	v_mov_b64_e32 v[218:219], v[80:81]
	v_mov_b64_e32 v[220:221], v[82:83]
	v_pk_mul_f32 v[74:75], v[132:133], v[162:163] op_sel_hi:[0,1]
	v_pk_mul_f32 v[64:65], v[74:75], v[64:65]
	v_pk_mul_f32 v[80:81], v[132:133], v[160:161] op_sel_hi:[0,1]
	v_pk_mul_f32 v[66:67], v[80:81], v[66:67]
	v_pk_mul_f32 v[80:81], v[132:133], v[156:157] op_sel_hi:[0,1]
	v_pk_mul_f32 v[74:75], v[132:133], v[158:159] op_sel_hi:[0,1]
	v_pk_mul_f32 v[58:59], v[80:81], v[58:59]
	v_pk_mul_f32 v[56:57], v[74:75], v[56:57]
	v_max_f32_e32 v64, 0, v64
	v_max_f32_e32 v65, 0, v65
	v_max_f32_e32 v66, 0, v66
	v_max_f32_e32 v58, 0, v58
	v_max_f32_e32 v67, 0, v67
	v_max_f32_e32 v59, 0, v59
	v_max_f32_e32 v56, 0, v56
	v_max_f32_e32 v57, 0, v57
	v_pk_mul_f32 v[64:65], v[64:65], v[64:65]
	v_pk_mul_f32 v[66:67], v[66:67], v[66:67]
	v_pk_mul_f32 v[58:59], v[58:59], v[58:59]
	s_mov_b32 s0, 0x2c0000
	v_pk_mul_f32 v[56:57], v[56:57], v[56:57]
	v_cvt_pk_bf16_f32 v64, v64, v65
	v_cvt_pk_bf16_f32 v65, v66, v67
	v_cvt_pk_bf16_f32 v67, v58, v59
	v_add_co_u32_e32 v58, vcc, s0, v124
	v_cvt_pk_bf16_f32 v66, v56, v57
	s_nop 0
	v_addc_co_u32_e32 v59, vcc, 0, v125, vcc
	v_mov_b64_e32 v[222:223], v[64:65]
	v_mov_b64_e32 v[224:225], v[66:67]
	v_cvt_f32_i32_e32 v59, v77
	v_cvt_f32_i32_e32 v58, v76
	v_cvt_f32_i32_e32 v65, v79
	v_cvt_f32_i32_e32 v64, v78
	v_pk_mul_f32 v[66:67], v[154:155], v[144:145] op_sel_hi:[0,1]
	v_pk_mul_f32 v[58:59], v[66:67], v[58:59]
	v_cvt_f32_i32_e32 v67, v69
	v_cvt_f32_i32_e32 v66, v68
	v_cvt_f32_i32_e32 v69, v71
	v_cvt_f32_i32_e32 v68, v70
	v_pk_mul_f32 v[74:75], v[154:155], v[142:143] op_sel_hi:[0,1]
	v_pk_mul_f32 v[64:65], v[74:75], v[64:65]
	v_max_f32_e32 v58, 0, v58
	v_max_f32_e32 v59, 0, v59
	v_pk_mul_f32 v[70:71], v[154:155], v[140:141] op_sel_hi:[0,1]
	v_pk_mul_f32 v[74:75], v[154:155], v[136:137] op_sel_hi:[0,1]
	v_pk_mul_f32 v[58:59], v[58:59], v[58:59]
	v_max_f32_e32 v64, 0, v64
	v_max_f32_e32 v65, 0, v65
	v_pk_mul_f32 v[68:69], v[74:75], v[68:69]
	v_pk_mul_f32 v[66:67], v[70:71], v[66:67]
	v_pk_mul_f32 v[70:71], v[64:65], v[64:65]
	v_cvt_pk_bf16_f32 v64, v58, v59
	v_cvt_f32_i32_e32 v59, v61
	v_cvt_f32_i32_e32 v58, v60
	v_max_f32_e32 v66, 0, v66
	v_max_f32_e32 v67, 0, v67
	v_max_f32_e32 v68, 0, v68
	v_max_f32_e32 v69, 0, v69
	v_cvt_f32_i32_e32 v61, v63
	v_cvt_f32_i32_e32 v60, v62
	v_pk_mul_f32 v[66:67], v[66:67], v[66:67]
	v_pk_mul_f32 v[68:69], v[68:69], v[68:69]
	v_cvt_pk_bf16_f32 v65, v70, v71
	v_cvt_pk_bf16_f32 v66, v66, v67
; __device__ __forceinline__ unsigned cvt_pk_bf16(float lo, float hi) { f32x2c v = {lo, hi}; bf16x2c b = __builtin_convertvector(v, bf16x2c); return __builtin_bit_cast(unsigned, b); }
;     __device__ __forceinline__ void operator()(const i32x4 (&acc)[2][2][4][2], const Unit& u, int wr, int wc, int fr, int fq) const {
;     ...
; #pragma unroll
;         for (int bj = 0; bj < 2; ++bj)
; #pragma unroll
;             for (int ai = 0; ai < 2; ++ai)
; #pragma unroll
;                 for (int m = 0; m < 4; ++m) { const int row = row0 + ai * HALF + m * 16;
;                     f32x4 v0 = __builtin_convertvector(acc[ai][bj][m][0], f32x4) * (cc[bj][0] * rr[ai][m]), v1 = __builtin_convertvector(acc[ai][bj][m][1], f32x4) * (cc[bj][1] * rr[ai][m]);
; #pragma unroll
;                     for (int j = 0; j < 4; ++j) { const float a = __builtin_fmaxf(v0[j], 0.f), b = __builtin_fmaxf(v1[j], 0.f); v0[j] = a * a; v1[j] = b * b; }
;                     u32x4 w; w.x = cvt_pk_bf16(v0[0], v0[1]); w.y = cvt_pk_bf16(v0[2], v0[3]); w.z = cvt_pk_bf16(v1[0], v1[1]); w.w = cvt_pk_bf16(v1[2], v1[3]);
;                     *(u32x4*)(O + (size_t)row * ldc + col0 + bj * HALF) = w; }
	v_cvt_pk_bf16_f32 v67, v68, v69
	v_pk_mul_f32 v[62:63], v[152:153], v[144:145] op_sel_hi:[0,1]
	s_nop 1
	v_mov_b32_dpp v194, v64 row_ror:8 row_mask:0xf bank_mask:0xf
	v_mov_b32_dpp v195, v65 row_ror:8 row_mask:0xf bank_mask:0xf
	s_nop 0
	v_mov_b32_dpp v64, v178 row_ror:8 row_mask:0xf bank_mask:0x3
	v_mov_b32_dpp v65, v179 row_ror:8 row_mask:0xf bank_mask:0x3
	v_mov_b32_dpp v178, v194 quad_perm:[0,1,2,3] row_mask:0xf bank_mask:0xc
	v_mov_b32_dpp v179, v195 quad_perm:[0,1,2,3] row_mask:0xf bank_mask:0xc
	v_mov_b32_dpp v194, v66 row_ror:8 row_mask:0xf bank_mask:0xf
	v_mov_b32_dpp v195, v67 row_ror:8 row_mask:0xf bank_mask:0xf
	s_nop 0
	v_mov_b32_dpp v66, v180 row_ror:8 row_mask:0xf bank_mask:0x3
	v_mov_b32_dpp v67, v181 row_ror:8 row_mask:0xf bank_mask:0x3
	v_mov_b32_dpp v180, v194 quad_perm:[0,1,2,3] row_mask:0xf bank_mask:0xc
	v_mov_b32_dpp v181, v195 quad_perm:[0,1,2,3] row_mask:0xf bank_mask:0xc
	v_lshl_add_u64 v[230:231], v[124:125], 0, v[232:233]
	global_store_dwordx4 v[230:231], v[178:181], off
	v_lshl_add_u64 v[230:231], v[230:231], 0, s[100:101]
	global_store_dwordx4 v[230:231], v[64:67], off
	v_pk_mul_f32 v[58:59], v[62:63], v[58:59]
	v_pk_mul_f32 v[62:63], v[152:153], v[140:141] op_sel_hi:[0,1]
	v_pk_mul_f32 v[64:65], v[152:153], v[142:143] op_sel_hi:[0,1]
	v_pk_mul_f32 v[60:61], v[64:65], v[60:61]
	v_pk_mul_f32 v[64:65], v[152:153], v[136:137] op_sel_hi:[0,1]
	v_pk_mul_f32 v[52:53], v[62:63], v[52:53]
	v_pk_mul_f32 v[54:55], v[64:65], v[54:55]
	v_max_f32_e32 v52, 0, v52
	v_max_f32_e32 v53, 0, v53
	v_max_f32_e32 v58, 0, v58
	v_max_f32_e32 v59, 0, v59
	v_pk_mul_f32 v[62:63], v[52:53], v[52:53]
	v_max_f32_e32 v52, 0, v60
	v_max_f32_e32 v54, 0, v54
	v_max_f32_e32 v53, 0, v61
	v_max_f32_e32 v55, 0, v55
	v_pk_mul_f32 v[58:59], v[58:59], v[58:59]
	v_pk_mul_f32 v[60:61], v[52:53], v[52:53]
	v_pk_mul_f32 v[64:65], v[54:55], v[54:55]
	v_cvt_pk_bf16_f32 v52, v58, v59
	v_cvt_pk_bf16_f32 v53, v60, v61
	v_cvt_pk_bf16_f32 v54, v62, v63
	v_cvt_pk_bf16_f32 v55, v64, v65
	s_nop 1
	v_mov_b32_dpp v194, v52 row_ror:8 row_mask:0xf bank_mask:0xf
	v_mov_b32_dpp v195, v53 row_ror:8 row_mask:0xf bank_mask:0xf
	s_nop 0
	v_mov_b32_dpp v52, v182 row_ror:8 row_mask:0xf bank_mask:0x3
	v_mov_b32_dpp v53, v183 row_ror:8 row_mask:0xf bank_mask:0x3
	v_mov_b32_dpp v182, v194 quad_perm:[0,1,2,3] row_mask:0xf bank_mask:0xc
	v_mov_b32_dpp v183, v195 quad_perm:[0,1,2,3] row_mask:0xf bank_mask:0xc
	v_mov_b32_dpp v194, v54 row_ror:8 row_mask:0xf bank_mask:0xf
	v_mov_b32_dpp v195, v55 row_ror:8 row_mask:0xf bank_mask:0xf
	s_nop 0
	v_mov_b32_dpp v54, v184 row_ror:8 row_mask:0xf bank_mask:0x3
	v_mov_b32_dpp v55, v185 row_ror:8 row_mask:0xf bank_mask:0x3
	v_mov_b32_dpp v184, v194 quad_perm:[0,1,2,3] row_mask:0xf bank_mask:0xc
	v_mov_b32_dpp v185, v195 quad_perm:[0,1,2,3] row_mask:0xf bank_mask:0xc
	v_lshl_add_u64 v[230:231], v[116:117], 0, v[232:233]
	global_store_dwordx4 v[230:231], v[182:185], off
	v_lshl_add_u64 v[230:231], v[230:231], 0, s[100:101]
	global_store_dwordx4 v[230:231], v[52:55], off
	v_lshl_add_u64 v[84:85], v[124:125], 0, s[40:41]
	s_mov_b64 s[40:41], 0x280000
	v_pk_mul_f32 v[52:53], v[150:151], v[144:145] op_sel_hi:[0,1]
	v_pk_mul_f32 v[54:55], v[150:151], v[142:143] op_sel_hi:[0,1]
	v_pk_mul_f32 v[48:49], v[52:53], v[48:49]
	v_pk_mul_f32 v[52:53], v[150:151], v[140:141] op_sel_hi:[0,1]
	v_pk_mul_f32 v[50:51], v[54:55], v[50:51]
	v_pk_mul_f32 v[54:55], v[150:151], v[136:137] op_sel_hi:[0,1]
	v_pk_mul_f32 v[44:45], v[52:53], v[44:45]
	v_pk_mul_f32 v[46:47], v[54:55], v[46:47]
	v_max_f32_e32 v44, 0, v44
	v_max_f32_e32 v45, 0, v45
	v_max_f32_e32 v48, 0, v48
	v_max_f32_e32 v49, 0, v49
	v_pk_mul_f32 v[52:53], v[44:45], v[44:45]
	v_max_f32_e32 v44, 0, v50
	v_max_f32_e32 v46, 0, v46
	v_max_f32_e32 v45, 0, v51
	v_max_f32_e32 v47, 0, v47
	v_pk_mul_f32 v[48:49], v[48:49], v[48:49]
	v_pk_mul_f32 v[50:51], v[44:45], v[44:45]
	v_pk_mul_f32 v[54:55], v[46:47], v[46:47]
	v_cvt_pk_bf16_f32 v44, v48, v49
	v_cvt_pk_bf16_f32 v45, v50, v51
	v_cvt_pk_bf16_f32 v46, v52, v53
	v_cvt_pk_bf16_f32 v47, v54, v55
	s_nop 1
	v_mov_b32_dpp v194, v44 row_ror:8 row_mask:0xf bank_mask:0xf
	v_mov_b32_dpp v195, v45 row_ror:8 row_mask:0xf bank_mask:0xf
	s_nop 0
	v_mov_b32_dpp v44, v186 row_ror:8 row_mask:0xf bank_mask:0x3
	v_mov_b32_dpp v45, v187 row_ror:8 row_mask:0xf bank_mask:0x3
	v_mov_b32_dpp v186, v194 quad_perm:[0,1,2,3] row_mask:0xf bank_mask:0xc
	v_mov_b32_dpp v187, v195 quad_perm:[0,1,2,3] row_mask:0xf bank_mask:0xc
	v_mov_b32_dpp v194, v46 row_ror:8 row_mask:0xf bank_mask:0xf
	v_mov_b32_dpp v195, v47 row_ror:8 row_mask:0xf bank_mask:0xf
	s_nop 0
	v_mov_b32_dpp v46, v188 row_ror:8 row_mask:0xf bank_mask:0x3
	v_mov_b32_dpp v47, v189 row_ror:8 row_mask:0xf bank_mask:0x3
	v_mov_b32_dpp v188, v194 quad_perm:[0,1,2,3] row_mask:0xf bank_mask:0xc
	v_mov_b32_dpp v189, v195 quad_perm:[0,1,2,3] row_mask:0xf bank_mask:0xc
	v_lshl_add_u64 v[230:231], v[108:109], 0, v[232:233]
	global_store_dwordx4 v[230:231], v[186:189], off
	v_lshl_add_u64 v[230:231], v[230:231], 0, s[100:101]
	global_store_dwordx4 v[230:231], v[44:47], off
	v_lshl_add_u64 v[72:73], v[124:125], 0, s[40:41]
	s_mov_b64 s[40:41], 0x2c0000
	v_pk_mul_f32 v[44:45], v[148:149], v[144:145] op_sel_hi:[0,1]
	v_pk_mul_f32 v[46:47], v[148:149], v[142:143] op_sel_hi:[0,1]
	v_pk_mul_f32 v[40:41], v[44:45], v[40:41]
	v_pk_mul_f32 v[44:45], v[148:149], v[140:141] op_sel_hi:[0,1]
	v_pk_mul_f32 v[42:43], v[46:47], v[42:43]
	v_pk_mul_f32 v[46:47], v[148:149], v[136:137] op_sel_hi:[0,1]
	v_pk_mul_f32 v[36:37], v[44:45], v[36:37]
	v_pk_mul_f32 v[38:39], v[46:47], v[38:39]
	v_max_f32_e32 v36, 0, v36
	v_max_f32_e32 v37, 0, v37
	v_max_f32_e32 v40, 0, v40
; __device__ __forceinline__ unsigned cvt_pk_bf16(float lo, float hi) { f32x2c v = {lo, hi}; bf16x2c b = __builtin_convertvector(v, bf16x2c); return __builtin_bit_cast(unsigned, b); }
;     __device__ __forceinline__ void operator()(const i32x4 (&acc)[2][2][4][2], const Unit& u, int wr, int wc, int fr, int fq) const {
;     ...
; #pragma unroll
;         for (int bj = 0; bj < 2; ++bj)
; #pragma unroll
;             for (int ai = 0; ai < 2; ++ai)
; #pragma unroll
;                 for (int m = 0; m < 4; ++m) { const int row = row0 + ai * HALF + m * 16;
;                     f32x4 v0 = __builtin_convertvector(acc[ai][bj][m][0], f32x4) * (cc[bj][0] * rr[ai][m]), v1 = __builtin_convertvector(acc[ai][bj][m][1], f32x4) * (cc[bj][1] * rr[ai][m]);
; #pragma unroll
;                     for (int j = 0; j < 4; ++j) { const float a = __builtin_fmaxf(v0[j], 0.f), b = __builtin_fmaxf(v1[j], 0.f); v0[j] = a * a; v1[j] = b * b; }
;                     u32x4 w; w.x = cvt_pk_bf16(v0[0], v0[1]); w.y = cvt_pk_bf16(v0[2], v0[3]); w.z = cvt_pk_bf16(v1[0], v1[1]); w.w = cvt_pk_bf16(v1[2], v1[3]);
;                     *(u32x4*)(O + (size_t)row * ldc + col0 + bj * HALF) = w; }
	v_max_f32_e32 v41, 0, v41
	v_pk_mul_f32 v[44:45], v[36:37], v[36:37]
	v_max_f32_e32 v36, 0, v42
	v_max_f32_e32 v38, 0, v38
	v_max_f32_e32 v37, 0, v43
	v_max_f32_e32 v39, 0, v39
	v_pk_mul_f32 v[40:41], v[40:41], v[40:41]
	v_pk_mul_f32 v[42:43], v[36:37], v[36:37]
	v_pk_mul_f32 v[46:47], v[38:39], v[38:39]
	v_cvt_pk_bf16_f32 v36, v40, v41
	v_cvt_pk_bf16_f32 v37, v42, v43
	v_cvt_pk_bf16_f32 v38, v44, v45
	v_cvt_pk_bf16_f32 v39, v46, v47
	s_nop 1
	v_mov_b32_dpp v194, v36 row_ror:8 row_mask:0xf bank_mask:0xf
	v_mov_b32_dpp v195, v37 row_ror:8 row_mask:0xf bank_mask:0xf
	s_nop 0
	v_mov_b32_dpp v36, v190 row_ror:8 row_mask:0xf bank_mask:0x3
	v_mov_b32_dpp v37, v191 row_ror:8 row_mask:0xf bank_mask:0x3
	v_mov_b32_dpp v190, v194 quad_perm:[0,1,2,3] row_mask:0xf bank_mask:0xc
	v_mov_b32_dpp v191, v195 quad_perm:[0,1,2,3] row_mask:0xf bank_mask:0xc
	v_mov_b32_dpp v194, v38 row_ror:8 row_mask:0xf bank_mask:0xf
	v_mov_b32_dpp v195, v39 row_ror:8 row_mask:0xf bank_mask:0xf
	s_nop 0
	v_mov_b32_dpp v38, v192 row_ror:8 row_mask:0xf bank_mask:0x3
	v_mov_b32_dpp v39, v193 row_ror:8 row_mask:0xf bank_mask:0x3
	v_mov_b32_dpp v192, v194 quad_perm:[0,1,2,3] row_mask:0xf bank_mask:0xc
	v_mov_b32_dpp v193, v195 quad_perm:[0,1,2,3] row_mask:0xf bank_mask:0xc
	v_lshl_add_u64 v[230:231], v[100:101], 0, v[232:233]
	global_store_dwordx4 v[230:231], v[190:193], off
	v_lshl_add_u64 v[230:231], v[230:231], 0, s[100:101]
	global_store_dwordx4 v[230:231], v[36:39], off
	v_lshl_add_u64 v[56:57], v[124:125], 0, s[40:41]
	s_mov_b64 s[40:41], -1
	v_pk_mul_f32 v[36:37], v[146:147], v[144:145] op_sel_hi:[0,1]
	v_pk_mul_f32 v[38:39], v[146:147], v[142:143] op_sel_hi:[0,1]
	v_pk_mul_f32 v[32:33], v[36:37], v[32:33]
	v_pk_mul_f32 v[36:37], v[146:147], v[140:141] op_sel_hi:[0,1]
	v_pk_mul_f32 v[34:35], v[38:39], v[34:35]
	v_pk_mul_f32 v[38:39], v[146:147], v[136:137] op_sel_hi:[0,1]
	v_pk_mul_f32 v[28:29], v[36:37], v[28:29]
	v_pk_mul_f32 v[30:31], v[38:39], v[30:31]
	v_max_f32_e32 v28, 0, v28
	v_max_f32_e32 v29, 0, v29
	v_max_f32_e32 v32, 0, v32
	v_max_f32_e32 v33, 0, v33
	v_pk_mul_f32 v[36:37], v[28:29], v[28:29]
	v_max_f32_e32 v28, 0, v34
	v_max_f32_e32 v30, 0, v30
	v_max_f32_e32 v29, 0, v35
	v_max_f32_e32 v31, 0, v31
	v_pk_mul_f32 v[32:33], v[32:33], v[32:33]
	v_pk_mul_f32 v[34:35], v[28:29], v[28:29]
	v_pk_mul_f32 v[38:39], v[30:31], v[30:31]
	v_cvt_pk_bf16_f32 v28, v32, v33
	v_cvt_pk_bf16_f32 v29, v34, v35
	v_cvt_pk_bf16_f32 v30, v36, v37
	v_cvt_pk_bf16_f32 v31, v38, v39
	s_nop 1
	v_mov_b32_dpp v194, v28 row_ror:8 row_mask:0xf bank_mask:0xf
	v_mov_b32_dpp v195, v29 row_ror:8 row_mask:0xf bank_mask:0xf
	s_nop 0
	v_mov_b32_dpp v28, v210 row_ror:8 row_mask:0xf bank_mask:0x3
	v_mov_b32_dpp v29, v211 row_ror:8 row_mask:0xf bank_mask:0x3
	v_mov_b32_dpp v210, v194 quad_perm:[0,1,2,3] row_mask:0xf bank_mask:0xc
	v_mov_b32_dpp v211, v195 quad_perm:[0,1,2,3] row_mask:0xf bank_mask:0xc
	v_mov_b32_dpp v194, v30 row_ror:8 row_mask:0xf bank_mask:0xf
	v_mov_b32_dpp v195, v31 row_ror:8 row_mask:0xf bank_mask:0xf
	s_nop 0
	v_mov_b32_dpp v30, v212 row_ror:8 row_mask:0xf bank_mask:0x3
	v_mov_b32_dpp v31, v213 row_ror:8 row_mask:0xf bank_mask:0x3
	v_mov_b32_dpp v212, v194 quad_perm:[0,1,2,3] row_mask:0xf bank_mask:0xc
	v_mov_b32_dpp v213, v195 quad_perm:[0,1,2,3] row_mask:0xf bank_mask:0xc
	v_lshl_add_u64 v[230:231], v[92:93], 0, v[232:233]
	global_store_dwordx4 v[230:231], v[210:213], off
	v_lshl_add_u64 v[230:231], v[230:231], 0, s[100:101]
	global_store_dwordx4 v[230:231], v[28:31], off
	s_andn2_b64 vcc, exec, s[38:39]
	s_nop 0
	v_pk_mul_f32 v[28:29], v[138:139], v[144:145] op_sel_hi:[0,1]
	v_pk_mul_f32 v[30:31], v[138:139], v[142:143] op_sel_hi:[0,1]
	v_pk_mul_f32 v[24:25], v[28:29], v[24:25]
	v_pk_mul_f32 v[28:29], v[138:139], v[140:141] op_sel_hi:[0,1]
	v_pk_mul_f32 v[26:27], v[30:31], v[26:27]
	v_pk_mul_f32 v[30:31], v[138:139], v[136:137] op_sel_hi:[0,1]
	v_pk_mul_f32 v[20:21], v[28:29], v[20:21]
	v_pk_mul_f32 v[22:23], v[30:31], v[22:23]
	v_max_f32_e32 v20, 0, v20
	v_max_f32_e32 v21, 0, v21
	v_max_f32_e32 v24, 0, v24
	v_max_f32_e32 v25, 0, v25
	v_pk_mul_f32 v[28:29], v[20:21], v[20:21]
	v_max_f32_e32 v20, 0, v26
	v_max_f32_e32 v22, 0, v22
	v_max_f32_e32 v21, 0, v27
	v_max_f32_e32 v23, 0, v23
	v_pk_mul_f32 v[24:25], v[24:25], v[24:25]
	v_pk_mul_f32 v[26:27], v[20:21], v[20:21]
	v_pk_mul_f32 v[30:31], v[22:23], v[22:23]
	v_cvt_pk_bf16_f32 v20, v24, v25
	v_cvt_pk_bf16_f32 v21, v26, v27
	v_cvt_pk_bf16_f32 v22, v28, v29
	v_cvt_pk_bf16_f32 v23, v30, v31
	s_nop 1
	v_mov_b32_dpp v194, v20 row_ror:8 row_mask:0xf bank_mask:0xf
	v_mov_b32_dpp v195, v21 row_ror:8 row_mask:0xf bank_mask:0xf
	s_nop 0
	v_mov_b32_dpp v20, v214 row_ror:8 row_mask:0xf bank_mask:0x3
	v_mov_b32_dpp v21, v215 row_ror:8 row_mask:0xf bank_mask:0x3
; __device__ __forceinline__ unsigned cvt_pk_bf16(float lo, float hi) { f32x2c v = {lo, hi}; bf16x2c b = __builtin_convertvector(v, bf16x2c); return __builtin_bit_cast(unsigned, b); }
;     __device__ __forceinline__ void operator()(const i32x4 (&acc)[2][2][4][2], const Unit& u, int wr, int wc, int fr, int fq) const {
;     ...
; #pragma unroll
;         for (int bj = 0; bj < 2; ++bj)
; #pragma unroll
;             for (int ai = 0; ai < 2; ++ai)
; #pragma unroll
;                 for (int m = 0; m < 4; ++m) { const int row = row0 + ai * HALF + m * 16;
;                     f32x4 v0 = __builtin_convertvector(acc[ai][bj][m][0], f32x4) * (cc[bj][0] * rr[ai][m]), v1 = __builtin_convertvector(acc[ai][bj][m][1], f32x4) * (cc[bj][1] * rr[ai][m]);
; #pragma unroll
;                     for (int j = 0; j < 4; ++j) { const float a = __builtin_fmaxf(v0[j], 0.f), b = __builtin_fmaxf(v1[j], 0.f); v0[j] = a * a; v1[j] = b * b; }
;                     u32x4 w; w.x = cvt_pk_bf16(v0[0], v0[1]); w.y = cvt_pk_bf16(v0[2], v0[3]); w.z = cvt_pk_bf16(v1[0], v1[1]); w.w = cvt_pk_bf16(v1[2], v1[3]);
;                     *(u32x4*)(O + (size_t)row * ldc + col0 + bj * HALF) = w; }
	v_mov_b32_dpp v214, v194 quad_perm:[0,1,2,3] row_mask:0xf bank_mask:0xc
	v_mov_b32_dpp v215, v195 quad_perm:[0,1,2,3] row_mask:0xf bank_mask:0xc
	v_mov_b32_dpp v194, v22 row_ror:8 row_mask:0xf bank_mask:0xf
	v_mov_b32_dpp v195, v23 row_ror:8 row_mask:0xf bank_mask:0xf
	s_nop 0
	v_mov_b32_dpp v22, v216 row_ror:8 row_mask:0xf bank_mask:0x3
	v_mov_b32_dpp v23, v217 row_ror:8 row_mask:0xf bank_mask:0x3
	v_mov_b32_dpp v216, v194 quad_perm:[0,1,2,3] row_mask:0xf bank_mask:0xc
	v_mov_b32_dpp v217, v195 quad_perm:[0,1,2,3] row_mask:0xf bank_mask:0xc
	v_lshl_add_u64 v[230:231], v[84:85], 0, v[232:233]
	global_store_dwordx4 v[230:231], v[214:217], off
	v_lshl_add_u64 v[230:231], v[230:231], 0, s[100:101]
	global_store_dwordx4 v[230:231], v[20:23], off
	s_nop 1
	v_pk_mul_f32 v[20:21], v[134:135], v[144:145] op_sel_hi:[0,1]
	v_pk_mul_f32 v[22:23], v[134:135], v[142:143] op_sel_hi:[0,1]
	v_pk_mul_f32 v[16:17], v[20:21], v[16:17]
	v_pk_mul_f32 v[20:21], v[134:135], v[140:141] op_sel_hi:[0,1]
	v_pk_mul_f32 v[18:19], v[22:23], v[18:19]
	v_pk_mul_f32 v[22:23], v[134:135], v[136:137] op_sel_hi:[0,1]
	v_pk_mul_f32 v[12:13], v[20:21], v[12:13]
	v_pk_mul_f32 v[14:15], v[22:23], v[14:15]
	v_max_f32_e32 v12, 0, v12
	v_max_f32_e32 v13, 0, v13
	v_max_f32_e32 v16, 0, v16
	v_max_f32_e32 v17, 0, v17
	v_pk_mul_f32 v[20:21], v[12:13], v[12:13]
	v_max_f32_e32 v12, 0, v18
	v_max_f32_e32 v14, 0, v14
	v_max_f32_e32 v13, 0, v19
	v_max_f32_e32 v15, 0, v15
	v_pk_mul_f32 v[16:17], v[16:17], v[16:17]
	v_pk_mul_f32 v[18:19], v[12:13], v[12:13]
	v_pk_mul_f32 v[22:23], v[14:15], v[14:15]
	v_cvt_pk_bf16_f32 v12, v16, v17
	v_cvt_pk_bf16_f32 v13, v18, v19
	v_cvt_pk_bf16_f32 v14, v20, v21
	v_cvt_pk_bf16_f32 v15, v22, v23
	s_nop 1
	v_mov_b32_dpp v194, v12 row_ror:8 row_mask:0xf bank_mask:0xf
	v_mov_b32_dpp v195, v13 row_ror:8 row_mask:0xf bank_mask:0xf
	s_nop 0
	v_mov_b32_dpp v12, v218 row_ror:8 row_mask:0xf bank_mask:0x3
	v_mov_b32_dpp v13, v219 row_ror:8 row_mask:0xf bank_mask:0x3
	v_mov_b32_dpp v218, v194 quad_perm:[0,1,2,3] row_mask:0xf bank_mask:0xc
	v_mov_b32_dpp v219, v195 quad_perm:[0,1,2,3] row_mask:0xf bank_mask:0xc
	v_mov_b32_dpp v194, v14 row_ror:8 row_mask:0xf bank_mask:0xf
	v_mov_b32_dpp v195, v15 row_ror:8 row_mask:0xf bank_mask:0xf
	s_nop 0
	v_mov_b32_dpp v14, v220 row_ror:8 row_mask:0xf bank_mask:0x3
	v_mov_b32_dpp v15, v221 row_ror:8 row_mask:0xf bank_mask:0x3
	v_mov_b32_dpp v220, v194 quad_perm:[0,1,2,3] row_mask:0xf bank_mask:0xc
	v_mov_b32_dpp v221, v195 quad_perm:[0,1,2,3] row_mask:0xf bank_mask:0xc
	v_lshl_add_u64 v[230:231], v[72:73], 0, v[232:233]
	global_store_dwordx4 v[230:231], v[218:221], off
	v_lshl_add_u64 v[230:231], v[230:231], 0, s[100:101]
	global_store_dwordx4 v[230:231], v[12:15], off
	s_nop 1
	v_pk_mul_f32 v[12:13], v[132:133], v[144:145] op_sel_hi:[0,1]
	v_pk_mul_f32 v[14:15], v[132:133], v[142:143] op_sel_hi:[0,1]
	v_pk_mul_f32 v[8:9], v[12:13], v[8:9]
	v_pk_mul_f32 v[12:13], v[132:133], v[140:141] op_sel_hi:[0,1]
	v_pk_mul_f32 v[10:11], v[14:15], v[10:11]
	v_pk_mul_f32 v[14:15], v[132:133], v[136:137] op_sel_hi:[0,1]
	v_pk_mul_f32 v[4:5], v[12:13], v[4:5]
	v_pk_mul_f32 v[6:7], v[14:15], v[6:7]
	v_max_f32_e32 v4, 0, v4
	v_max_f32_e32 v5, 0, v5
	v_max_f32_e32 v8, 0, v8
	v_max_f32_e32 v9, 0, v9
	v_pk_mul_f32 v[12:13], v[4:5], v[4:5]
	v_max_f32_e32 v4, 0, v10
	v_max_f32_e32 v6, 0, v6
	v_max_f32_e32 v5, 0, v11
	v_max_f32_e32 v7, 0, v7
	v_pk_mul_f32 v[8:9], v[8:9], v[8:9]
	v_pk_mul_f32 v[10:11], v[4:5], v[4:5]
	v_pk_mul_f32 v[14:15], v[6:7], v[6:7]
	v_cvt_pk_bf16_f32 v4, v8, v9
	v_cvt_pk_bf16_f32 v5, v10, v11
	v_cvt_pk_bf16_f32 v6, v12, v13
	v_cvt_pk_bf16_f32 v7, v14, v15
	s_nop 1
	v_mov_b32_dpp v194, v4 row_ror:8 row_mask:0xf bank_mask:0xf
	v_mov_b32_dpp v195, v5 row_ror:8 row_mask:0xf bank_mask:0xf
	s_nop 0
	v_mov_b32_dpp v4, v222 row_ror:8 row_mask:0xf bank_mask:0x3
	v_mov_b32_dpp v5, v223 row_ror:8 row_mask:0xf bank_mask:0x3
	v_mov_b32_dpp v222, v194 quad_perm:[0,1,2,3] row_mask:0xf bank_mask:0xc
	v_mov_b32_dpp v223, v195 quad_perm:[0,1,2,3] row_mask:0xf bank_mask:0xc
	v_mov_b32_dpp v194, v6 row_ror:8 row_mask:0xf bank_mask:0xf
	v_mov_b32_dpp v195, v7 row_ror:8 row_mask:0xf bank_mask:0xf
	s_nop 0
	v_mov_b32_dpp v6, v224 row_ror:8 row_mask:0xf bank_mask:0x3
	v_mov_b32_dpp v7, v225 row_ror:8 row_mask:0xf bank_mask:0x3
	v_mov_b32_dpp v224, v194 quad_perm:[0,1,2,3] row_mask:0xf bank_mask:0xc
	v_mov_b32_dpp v225, v195 quad_perm:[0,1,2,3] row_mask:0xf bank_mask:0xc
	v_lshl_add_u64 v[230:231], v[56:57], 0, v[232:233]
	global_store_dwordx4 v[230:231], v[222:225], off
	v_lshl_add_u64 v[230:231], v[230:231], 0, s[100:101]
	global_store_dwordx4 v[230:231], v[4:7], off
	s_cbranch_vccnz .LBB0_1109
	s_andn2_b64 vcc, exec, s[44:45]
	s_cbranch_vccnz .LBB0_1108
	s_barrier
	s_branch .LBB0_1108

; #define PG8_STAGE(bufoff, gbase, voff) do { _Pragma("unroll") for (int _i = 0; _i < 2; ++_i) \
;         __builtin_amdgcn_global_load_lds((const unsigned*)((const char*)(gbase) + (voff)[_i]), (PG8_LAS unsigned*)(lds + (bufoff) + ldsw + _i * 8192), 16, 0, 0); } while (0)
; #define PG8_WAIT_V(n) asm volatile("s_waitcnt vmcnt(" #n ")" ::: "memory")
; #define PG8_BAR __builtin_amdgcn_s_barrier()
;     __host__ __device__ bool next(int i, Unit& u) const {
;     ...
;         int wgid = (int)L; { const int q = nwg / NXCD, r = nwg % NXCD, xcd = wgid % NXCD, off = wgid / NXCD; wgid = (xcd < r ? xcd * (q + 1) : r * (q + 1) + (xcd - r) * q) + off; }
;         const int nig = WGM * nN, gid = wgid / nig, fm = gid * WGM, gsz = (nM - fm) < WGM ? (nM - fm) : WGM;
;         u.pm = fm + ((wgid % nig) % gsz); u.pn = (wgid % nig) / gsz; return true;
; template <class Epi, class Sched, bool ALIGN_EPI = false, bool SP2 = false>
; __device__ __forceinline__ void gemm_phase(PG8_LAS unsigned char* lds, const Gemm g, const Sched& S, const Epi& E, Stopwatch& sw) {
;     ...
;     const char* cA = (const char*)g.A + (size_t)cur.pm * tstep; const char* cB = (const char*)g.Bt + (size_t)cur.pn * tstep;
;     S.a_ready(cur);
;     if constexpr (SP2) {
;         PG8_STAGE(PG8_SB(0, 0), cB, voffB); PG8_STAGE(PG8_SB(0, 1), cB + hstep, voffB); PG8_STAGE(PG8_SA(0, 0), cA, voffA); PG8_STAGE(PG8_SA(0, 1), cA + hstep, voffA);
;         if (wr == 1) PG8_BAR;
;         PG8_WAIT_V(2); PG8_BAR;
;         PG8_STAGE(PG8_SB(1, 0), cB + kstep, voffB); PG8_STAGE(PG8_SA(1, 0), cA + kstep, voffA); PG8_STAGE(PG8_SB(1, 1), cB + hstep + kstep, voffB);
;         PG8_WAIT_V(6); PG8_BAR;
.LBB0_1213:
	s_cmp_le_i32 s86, s5
	s_cselect_b64 s[4:5], -1, 0
	s_and_b64 s[42:43], s[4:5], s[42:43]
	s_andn2_b64 vcc, exec, s[42:43]
	s_cbranch_vccnz .LBB0_1264
	s_waitcnt vmcnt(0) lgkmcnt(0)
	v_mov_b32_e32 v4, v234
	s_and_b64 vcc, exec, s[56:57]
	v_readfirstlane_b32 s0, v4
	s_cbranch_vccnz .LBB0_1264
	v_lshlrev_b32_e32 v1, 4, v4
	v_add_u32_e32 v2, 0x2000, v1
	v_ashrrev_i32_e32 v5, 31, v2
	v_lshrrev_b32_e32 v5, 22, v5
	v_add_u32_e32 v5, v2, v5
	v_ashrrev_i32_e32 v5, 10, v5
	v_mul_i32_i24_e32 v6, 0x400, v5
	v_sub_u32_e32 v2, v2, v6
	v_lshrrev_b32_e32 v6, 4, v2
	v_bitop3_b32 v2, v6, v2, 32 bitop3:0x6c
	v_ashrrev_i32_e32 v6, 31, v2
	v_lshrrev_b32_e32 v6, 26, v6
	v_add_u32_e32 v7, v2, v6
	v_lshlrev_b32_e32 v8, 3, v5
	v_ashrrev_i32_e32 v6, 6, v7
	v_and_b32_e32 v8, -16, v8
	v_add_u32_e32 v8, v6, v8
	v_and_b32_e32 v9, 3, v6
	s_mov_b32 s18, 0x3ffe0
	v_lshrrev_b32_e32 v10, 2, v8
	v_lshlrev_b32_e32 v11, 1, v8
	v_and_b32_e32 v7, 0xc0, v7
	v_and_or_b32 v9, v8, s18, v9
	v_and_b32_e32 v10, 4, v10
	v_and_b32_e32 v11, 24, v11
	v_sub_u32_e32 v2, v2, v7
	v_or3_b32 v9, v9, v10, v11
	v_lshlrev_b32_e32 v10, 5, v5
	v_ashrrev_i16_sdwa v2, v235, sext(v2) dst_sel:DWORD dst_unused:UNUSED_PAD src0_sel:DWORD src1_sel:BYTE_0
	v_and_b32_e32 v10, 32, v10
	v_bfe_i32 v7, v2, 0, 16
	v_add_lshl_u32 v2, v10, v7, 1
	v_lshl_add_u32 v196, v9, 14, v2
	v_lshl_add_u32 v202, v8, 14, v2
	v_bfe_i32 v2, v4, 27, 1
	v_lshrrev_b32_e32 v2, 22, v2
	v_add_u32_e32 v2, v1, v2
	v_and_b32_e32 v2, 0xfffffc00, v2
	v_sub_u32_e32 v1, v1, v2
	v_lshrrev_b32_e32 v2, 4, v1
	v_ashrrev_i32_e32 v9, 31, v4
	v_bitop3_b32 v1, v2, v1, 32 bitop3:0x6c
	v_lshrrev_b32_e32 v9, 26, v9
	v_ashrrev_i32_e32 v2, 31, v1
	v_add_u32_e32 v9, v4, v9
	v_lshrrev_b32_e32 v2, 26, v2
	v_ashrrev_i32_e32 v9, 6, v9
	v_add_u32_e32 v2, v1, v2
	v_lshlrev_b32_e32 v10, 3, v9
	s_ashr_i32 s34, s0, 6
	v_ashrrev_i32_e32 v8, 6, v2
	v_and_b32_e32 v10, -16, v10
	s_ashr_i32 s3, s0, 8
	s_lshl_b32 s16, s34, 10
	s_lshl_b32 s4, s36, 1
	v_readlane_b32 s5, v250, 22
	v_add_u32_e32 v11, v8, v10
	s_add_u32 s4, s5, s4
	v_readlane_b32 s5, v250, 23
	v_and_b32_e32 v10, 3, v8
	v_lshrrev_b32_e32 v12, 2, v11
	v_lshlrev_b32_e32 v13, 1, v11
	v_and_b32_e32 v2, 0xc0, v2
	s_addc_u32 s5, s5, 0
	v_and_or_b32 v10, v11, s18, v10
	v_and_b32_e32 v12, 4, v12
	v_and_b32_e32 v13, 24, v13
	v_sub_u32_e32 v1, v1, v2
	v_readlane_b32 s18, v254, 19
	v_or3_b32 v12, v10, v12, v13
	v_lshlrev_b32_e32 v10, 5, v9
	v_ashrrev_i16_sdwa v1, v235, sext(v1) dst_sel:DWORD dst_unused:UNUSED_PAD src0_sel:DWORD src1_sel:BYTE_0
	v_readlane_b32 s19, v254, 20
	s_add_u32 s40, s4, s18
	v_and_b32_e32 v13, 32, v10
	v_bfe_i32 v10, v1, 0, 16
	s_addc_u32 s41, s5, s19
	v_readlane_b32 s100, v254, 21
	v_readlane_b32 s101, v253, 53
	s_nop 0
	s_and_b32 s18, s100, 7
	s_andn2_b32 s100, s100, 7
	s_add_i32 s100, s100, s101
	s_mov_b32 s101, s18
	s_lshl_b32 s19, s18, 22
	s_add_u32 s40, s4, s19
	s_addc_u32 s41, s5, 0
	s_add_i32 s16, s16, 0
	v_add_lshl_u32 v1, v13, v10, 1
	s_add_i32 s18, s16, 0x10000
	s_add_i32 s19, s16, 0x12000
	v_lshl_add_u32 v2, v12, 14, v1
	s_mov_b32 m0, s18
	s_add_u32 s36, s40, 0x200000
	global_load_lds_dwordx4 v2, s[40:41]
	s_mov_b32 m0, s19
	s_addc_u32 s37, s41, 0
	s_add_i32 s24, s16, 0x14000
	global_load_lds_dwordx4 v196, s[40:41]
	s_mov_b32 m0, s24
	s_add_i32 s25, s16, 0x16000
	global_load_lds_dwordx4 v2, s[36:37]
	s_mov_b32 m0, s25
	v_lshl_add_u32 v204, v11, 14, v1
	global_load_lds_dwordx4 v196, s[36:37]
	s_lshl_b32 s36, s100, 22
	s_add_u32 s36, s14, s36
	s_mov_b32 m0, s16
	s_addc_u32 s37, s15, 0
	s_add_u32 s98, s36, 0x200000
	s_addc_u32 s99, s37, 0
	s_add_i32 s31, s16, 0x2000
	s_add_i32 s72, s16, 0x4000
	s_add_i32 s73, s16, 0x6000
	s_cmp_eq_u32 s3, 1
	s_cselect_b64 s[44:45], -1, 0
	global_load_lds_dwordx4 v204, s[36:37]
	s_mov_b32 m0, s31
	s_cmp_lg_u32 s3, 1
	global_load_lds_dwordx4 v202, s[36:37]
	s_mov_b32 s36, s98
	s_mov_b32 m0, s72
	s_mov_b32 s37, s99
	s_nop 4
	global_load_lds_dwordx4 v204, s[36:37]
	s_mov_b32 m0, s73
	s_nop 0
	global_load_lds_dwordx4 v202, s[36:37]
	s_cbranch_scc1 .LBB0_1217
	s_barrier
.LBB0_1217:
	v_lshl_add_u64 v[12:13], s[40:41], 0, v[2:3]
	v_mov_b32_e32 v197, v3
	s_lshl_b32 s56, s100, 22
	s_add_u32 s56, s14, s56
	s_addc_u32 s57, s15, 0
	s_add_i32 s79, s16, 0x18000
	v_lshl_add_u64 v[14:15], s[40:41], 0, v[196:197]
	v_mov_b32_e32 v205, v3
	s_and_b32 s78, s34, 3
	v_lshl_add_u64 v[12:13], v[12:13], 0, s[20:21]
	s_mov_b32 m0, s79
	s_add_i32 s80, s16, 0x1a000
	v_lshl_add_u64 v[16:17], s[56:57], 0, v[204:205]
	v_mov_b32_e32 v203, v3
	s_lshl_b32 s34, s3, 13
	s_lshl_b32 s38, s78, 12
	s_waitcnt vmcnt(2)
	s_barrier
	global_load_lds_dwordx4 v[12:13], off
	v_lshl_add_u64 v[12:13], v[14:15], 0, s[20:21]
	s_mov_b32 m0, s80
	s_add_i32 s81, s16, 0x8000
	s_add_i32 s82, s16, 0xa000
	v_lshl_add_u64 v[18:19], s[56:57], 0, v[202:203]
	global_load_lds_dwordx4 v[12:13], off
	v_lshl_add_u64 v[12:13], v[16:17], 0, s[20:21]
	s_mov_b32 m0, s81
	s_add_u32 s36, s40, 0x200080
	global_load_lds_dwordx4 v[12:13], off
	v_lshl_add_u64 v[12:13], v[18:19], 0, s[20:21]
	s_mov_b32 m0, s82
	s_addc_u32 s37, s41, 0
	s_add_i32 s83, s16, 0x1c000
	global_load_lds_dwordx4 v[12:13], off
	v_lshl_add_u64 v[12:13], s[36:37], 0, v[2:3]
	s_mov_b32 m0, s83
	s_add_i32 s90, s16, 0x1e000
	global_load_lds_dwordx4 v[12:13], off
	v_lshl_add_u64 v[12:13], s[36:37], 0, v[196:197]
	s_mov_b32 m0, s90
	v_bfe_u32 v11, v4, 4, 2
	global_load_lds_dwordx4 v[12:13], off
	v_lshlrev_b32_e32 v13, 3, v11
	v_lshlrev_b32_e32 v14, 4, v11
	v_cmp_eq_u32_e64 s[36:37], 0, v11
	v_lshlrev_b32_e32 v11, 17, v9
	v_and_b32_e32 v11, 0xfffc0000, v11
	v_lshl_add_u32 v8, v8, 14, v11
	v_and_b32_e32 v9, 1, v9
	v_lshl_or_b32 v8, v9, 6, v8
	v_lshl_add_u32 v206, v10, 1, v8
	v_lshlrev_b32_e32 v8, 17, v5
	v_and_b32_e32 v12, 15, v4
	v_lshlrev_b32_e32 v4, 2, v4
	v_and_b32_e32 v8, 0xfffc0000, v8
	v_lshl_or_b32 v1, s3, 6, v12
	v_lshl_or_b32 v12, v12, 6, v14
	v_and_b32_e32 v4, 32, v4
	s_waitcnt vmcnt(6)
	v_lshl_add_u32 v6, v6, 14, v8
	v_and_b32_e32 v5, 1, v5
	v_bitop3_b32 v14, v12, s34, v4 bitop3:0xde
	v_bitop3_b32 v4, v12, s38, v4 bitop3:0xde
	s_cmpk_lt_u32 s0, 0x100
	v_lshl_or_b32 v5, v5, 6, v6
	v_readlane_b32 s38, v254, 21
	v_lshl_or_b32 v226, s78, 5, v13
	s_cselect_b64 s[46:47], -1, 0
	s_mov_b32 s0, 0
	v_mov_b32_e32 v207, v3
	v_lshl_add_u32 v208, v7, 1, v5
	v_mov_b32_e32 v209, v3
	v_add_u32_e32 v227, 0, v4
	v_add_u32_e32 v228, 0, v14
	s_mov_b32 s34, s101
	s_mov_b32 s95, s100
	s_barrier
	v_readlane_b32 s39, v254, 22
	s_branch .LBB0_1220

; #define TS_BEG(sw, id) do { if ((id) == TSSEL && (sw).on) (sw).t0 = __builtin_amdgcn_s_memrealtime(); } while (0)
; #define TS_BEG(sw, id) do { } while (0)
; template <class Epi, class Sched, bool ALIGN_EPI = false, bool SP2 = false>
; __device__ __forceinline__ void gemm_phase(PG8_LAS unsigned char* lds, const Gemm g, const Sched& S, const Epi& E, Stopwatch& sw) {
;     ...
;         const bool has_next = S.next(ui + 1, nxt);
;         const char* nA = has_next ? (const char*)g.A + (size_t)nxt.pm * tstep : cA; const char* nB = has_next ? (const char*)g.Bt + (size_t)nxt.pn * tstep : cB;
;         TS_BEG(sw, 23); TS_BEG(sw, 20);
;         for (int t = 0; t < nt; t += 2) {
;             if constexpr (Epi::MID) { if (t == Epi::MID_T0 || t == Epi::MID_T1) E.mid(acc, cur, t, wr, wc, fr, fq); }
;             const bool last = (t == nt - 2);
;             const char* a1 = cA + (size_t)(t + 1) * kstep;
;             const char* a2 = last ? nA : cA + (size_t)(t + 2) * kstep; const char* b2 = last ? nB : cB + (size_t)(t + 2) * kstep;
;             const char* a3 = a2 + kstep; const char* b3 = b2 + kstep;
;             if (last && has_next) S.a_ready(nxt);
;     ...
; #pragma unroll
;         for (int a = 0; a < 2; ++a)
; #pragma unroll
;             for (int b = 0; b < 2; ++b)
; #pragma unroll
;                 for (int m = 0; m < 4; ++m)
; #pragma unroll
;                     for (int n = 0; n < 2; ++n) acc[a][b][m][n] = typename Epi::acc_t{};
;         cur = nxt; cA = nA; cB = nB; ++ui;
.LBB0_1226:
	s_and_b32 s100, s50, 7
	s_andn2_b32 s50, s50, 7
	s_add_i32 s50, s50, s48
	s_mov_b32 s48, s100
	s_ashr_i32 s51, s50, 31
	s_lshl_b64 s[52:53], s[50:51], 22
	s_add_u32 s52, s14, s52
	s_addc_u32 s53, s15, s53
	s_and_b64 s[54:55], s[38:39], exec
	s_cselect_b32 s51, s53, s57
	s_cselect_b32 s3, s52, s56
	s_ashr_i32 s49, s48, 31
	s_lshl_b64 s[54:55], s[48:49], 22
	s_add_u32 s54, s4, s54
	s_addc_u32 s55, s5, s55
	s_and_b64 s[58:59], s[38:39], exec
	s_cselect_b32 s49, s55, s41
	s_cselect_b32 s91, s54, s40
	s_cmp_lg_u32 s0, 0
	s_cselect_b64 s[58:59], -1, 0
	s_add_u32 s60, s3, 0x200080
	s_addc_u32 s61, s51, 0
	v_lshl_add_u64 v[210:211], s[60:61], 0, v[202:203]
	v_lshl_add_u64 v[212:213], s[60:61], 0, v[204:205]
	s_add_u32 s60, s56, 0x200080
	s_addc_u32 s61, s57, 0
	s_add_u32 s76, s40, 0x100
	v_mov_b32_e32 v4, 0
	v_lshl_add_u64 v[214:215], s[60:61], 0, v[206:207]
	v_lshl_add_u64 v[216:217], s[60:61], 0, v[208:209]
	s_addc_u32 s77, s41, 0
	s_mov_b32 s0, -2
	s_mov_b64 s[60:61], 0
	v_mov_b32_e32 v5, v4
	v_mov_b32_e32 v6, v4
	v_mov_b32_e32 v7, v4
	v_mov_b32_e32 v8, v4
	s_waitcnt lgkmcnt(0)
	v_mov_b32_e32 v9, v4
	v_mov_b32_e32 v10, v4
	v_mov_b32_e32 v11, v4
	v_mov_b32_e32 v20, v4
	v_mov_b32_e32 v21, v4
	v_mov_b32_e32 v22, v4
	v_mov_b32_e32 v23, v4
	v_mov_b32_e32 v24, v4
	v_mov_b32_e32 v25, v4
	v_mov_b32_e32 v26, v4
	v_mov_b32_e32 v27, v4
	v_mov_b32_e32 v36, v4
	v_mov_b32_e32 v37, v4
	v_mov_b32_e32 v38, v4
	v_mov_b32_e32 v39, v4
	v_mov_b32_e32 v40, v4
	v_mov_b32_e32 v41, v4
	v_mov_b32_e32 v42, v4
	v_mov_b32_e32 v43, v4
	v_mov_b32_e32 v52, v4
	v_mov_b32_e32 v53, v4
	v_mov_b32_e32 v54, v4
	v_mov_b32_e32 v55, v4
	v_mov_b32_e32 v56, v4
	v_mov_b32_e32 v57, v4
	v_mov_b32_e32 v58, v4
	v_mov_b32_e32 v59, v4
	v_mov_b32_e32 v12, v4
	v_mov_b32_e32 v13, v4
	v_mov_b32_e32 v14, v4
	v_mov_b32_e32 v15, v4
	v_mov_b32_e32 v16, v4
	v_mov_b32_e32 v17, v4
	v_mov_b32_e32 v18, v4
	v_mov_b32_e32 v19, v4
	v_mov_b32_e32 v28, v4
	v_mov_b32_e32 v29, v4
	v_mov_b32_e32 v30, v4
	v_mov_b32_e32 v31, v4
	v_mov_b32_e32 v32, v4
	v_mov_b32_e32 v33, v4
	v_mov_b32_e32 v34, v4
	v_mov_b32_e32 v35, v4
	v_mov_b32_e32 v44, v4
	v_mov_b32_e32 v45, v4
	v_mov_b32_e32 v46, v4
	v_mov_b32_e32 v47, v4
	v_mov_b32_e32 v48, v4
	v_mov_b32_e32 v49, v4
	v_mov_b32_e32 v50, v4
	v_mov_b32_e32 v51, v4
	v_mov_b32_e32 v60, v4
	v_mov_b32_e32 v61, v4
	v_mov_b32_e32 v62, v4
	v_mov_b32_e32 v63, v4
	v_mov_b32_e32 v64, v4
	v_mov_b32_e32 v65, v4
	v_mov_b32_e32 v66, v4
	v_mov_b32_e32 v67, v4
	v_mov_b32_e32 v68, v4
	v_mov_b32_e32 v69, v4
	v_mov_b32_e32 v70, v4
	v_mov_b32_e32 v71, v4
	v_mov_b32_e32 v72, v4
	v_mov_b32_e32 v73, v4
	v_mov_b32_e32 v74, v4
	v_mov_b32_e32 v75, v4
	v_mov_b32_e32 v84, v4
	v_mov_b32_e32 v85, v4
	v_mov_b32_e32 v86, v4
	v_mov_b32_e32 v87, v4
	v_mov_b32_e32 v88, v4
	v_mov_b32_e32 v89, v4
	v_mov_b32_e32 v90, v4
	v_mov_b32_e32 v91, v4
	v_mov_b32_e32 v100, v4
	v_mov_b32_e32 v101, v4
	v_mov_b32_e32 v102, v4
	v_mov_b32_e32 v103, v4
	v_mov_b32_e32 v104, v4
	v_mov_b32_e32 v105, v4
	v_mov_b32_e32 v106, v4
	v_mov_b32_e32 v107, v4
	v_mov_b32_e32 v116, v4
	v_mov_b32_e32 v117, v4
	v_mov_b32_e32 v118, v4
	v_mov_b32_e32 v119, v4
	v_mov_b32_e32 v120, v4
	v_mov_b32_e32 v121, v4
	v_mov_b32_e32 v122, v4
	v_mov_b32_e32 v123, v4
	v_mov_b32_e32 v76, v4
	v_mov_b32_e32 v77, v4
	v_mov_b32_e32 v78, v4
	v_mov_b32_e32 v79, v4
	v_mov_b32_e32 v80, v4
	v_mov_b32_e32 v81, v4
	v_mov_b32_e32 v82, v4
	v_mov_b32_e32 v83, v4
	v_mov_b32_e32 v92, v4
	v_mov_b32_e32 v93, v4
	v_mov_b32_e32 v94, v4
	v_mov_b32_e32 v95, v4
	v_mov_b32_e32 v96, v4
	v_mov_b32_e32 v97, v4
	v_mov_b32_e32 v98, v4
	v_mov_b32_e32 v99, v4
	v_mov_b32_e32 v108, v4
	v_mov_b32_e32 v109, v4
	v_mov_b32_e32 v110, v4
	v_mov_b32_e32 v111, v4
	v_mov_b32_e32 v112, v4
	v_mov_b32_e32 v113, v4
	v_mov_b32_e32 v114, v4
	v_mov_b32_e32 v115, v4
	v_mov_b32_e32 v124, v4
	v_mov_b32_e32 v125, v4
	v_mov_b32_e32 v126, v4
	v_mov_b32_e32 v127, v4
	v_mov_b32_e32 v128, v4
	v_mov_b32_e32 v129, v4
	v_mov_b32_e32 v130, v4
	v_mov_b32_e32 v131, v4
	s_branch .LBB0_1228

; #define PG8_STAGE(bufoff, gbase, voff) do { _Pragma("unroll") for (int _i = 0; _i < 2; ++_i) \
;         __builtin_amdgcn_global_load_lds((const unsigned*)((const char*)(gbase) + (voff)[_i]), (PG8_LAS unsigned*)(lds + (bufoff) + ldsw + _i * 8192), 16, 0, 0); } while (0)
; #define PG8_LDA(dst, b, h) do { _Pragma("unroll") for (int m = 0; m < 4; ++m) _Pragma("unroll") for (int k = 0; k < 2; ++k) dst[m][k] = *(const PG8_LAS bf16x8*)(lds + PG8_SA(b, h) + aoff + m * 2048 + k * 1024); } while (0)
; #define PG8_LDB(dst, b, h) do { _Pragma("unroll") for (int n = 0; n < 2; ++n) _Pragma("unroll") for (int k = 0; k < 2; ++k) dst[n][k] = *(const PG8_LAS bf16x8*)(lds + PG8_SB(b, h) + boff + n * 2048 + k * 1024); } while (0)
; #define PG8_MMA(ai, bj, At, Bt) do { __builtin_amdgcn_s_setprio(1); _Pragma("unroll") for (int m = 0; m < 4; ++m) _Pragma("unroll") for (int n = 0; n < 2; ++n) _Pragma("unroll") for (int k = 0; k < 2; ++k) \
;         acc[ai][bj][m][n] = mma16(Bt[n][k], At[m][k], acc[ai][bj][m][n]); __builtin_amdgcn_s_setprio(0); } while (0)
; template <class Epi, class Sched, bool ALIGN_EPI = false, bool SP2 = false>
; __device__ __forceinline__ void gemm_phase(PG8_LAS unsigned char* lds, const Gemm g, const Sched& S, const Epi& E, Stopwatch& sw) {
;     ...
;             const bool last = (t == nt - 2);
;             const char* a1 = cA + (size_t)(t + 1) * kstep;
;             const char* a2 = last ? nA : cA + (size_t)(t + 2) * kstep; const char* b2 = last ? nB : cB + (size_t)(t + 2) * kstep;
;             const char* a3 = a2 + kstep; const char* b3 = b2 + kstep;
;             if (last && has_next) S.a_ready(nxt);
;             if constexpr (SP2) {
;             int relax = __builtin_amdgcn_readfirstlane((int)((ui > 0) && (t == 0))); asm volatile("" : "+s"(relax));
;             PG8_LDB(B0, 0, 0); PG8_LDB(B1, 0, 1); PG8_SCHED; PG8_LDA(At, 0, 0); if (!relax) PG8_STAGE(PG8_SA(1, 1), a1 + hstep, voffA);
;             if (relax) PG8_WAIT_VN(8 + Epi::NST); else PG8_WAIT_V(8); PG8_WAIT_L(0); PG8_BAR; PG8_MMA(0, 0, At, B0); PG8_MMA(0, 1, At, B1); PG8_BAR; PG8_SCHED;
;             PG8_LDA(At, 0, 1); PG8_STAGE(PG8_SB(0, 0), b2, voffB); PG8_STAGE(PG8_SB(0, 1), b2 + hstep, voffB); PG8_STAGE(PG8_SA(0, 0), a2, voffA);
;             if (relax) PG8_WAIT_VN(8 + Epi::NST); else PG8_WAIT_V(8); PG8_WAIT_L(0); PG8_BAR; PG8_MMA(1, 0, At, B0); PG8_MMA(1, 1, At, B1); PG8_BAR; PG8_SCHED;
.LBB0_1231:
	s_add_u32 s40, s56, s60
	s_addc_u32 s41, s57, s61
	s_add_u32 s68, s40, 0x100
	s_addc_u32 s69, s41, 0
	s_add_u32 s62, s76, s60
	s_addc_u32 s63, s77, s61
	s_cmpk_eq_i32 s60, 0x3f00
	s_cselect_b64 s[64:65], -1, 0
	s_waitcnt lgkmcnt(0)
	s_and_b64 s[40:41], s[64:65], exec
	s_cselect_b32 s63, s49, s63
	s_cselect_b32 s62, s91, s62
	s_cselect_b32 s69, s51, s69
	s_cselect_b32 s68, s3, s68
	s_barrier
	s_setprio 1
	s_waitcnt lgkmcnt(0)
	v_mfma_f32_16x16x32_bf16 v[128:131], v[148:151], v[188:191], v[128:131]
	v_mfma_f32_16x16x32_bf16 v[124:127], v[156:159], v[188:191], v[124:127]
	v_mfma_f32_16x16x32_bf16 v[112:115], v[148:151], v[180:183], v[112:115]
	v_mfma_f32_16x16x32_bf16 v[108:111], v[156:159], v[180:183], v[108:111]
	v_mfma_f32_16x16x32_bf16 v[96:99], v[148:151], v[172:175], v[96:99]
	v_mfma_f32_16x16x32_bf16 v[92:95], v[156:159], v[172:175], v[92:95]
	v_mfma_f32_16x16x32_bf16 v[80:83], v[148:151], v[164:167], v[80:83]
	v_mfma_f32_16x16x32_bf16 v[76:79], v[156:159], v[164:167], v[76:79]
	v_mfma_f32_16x16x32_bf16 v[128:131], v[152:155], v[192:195], v[128:131]
	v_mfma_f32_16x16x32_bf16 v[124:127], v[160:163], v[192:195], v[124:127]
	v_mfma_f32_16x16x32_bf16 v[112:115], v[152:155], v[184:187], v[112:115]
	v_mfma_f32_16x16x32_bf16 v[108:111], v[160:163], v[184:187], v[108:111]
	v_mfma_f32_16x16x32_bf16 v[96:99], v[152:155], v[176:179], v[96:99]
	v_mfma_f32_16x16x32_bf16 v[92:95], v[160:163], v[176:179], v[92:95]
	v_mfma_f32_16x16x32_bf16 v[80:83], v[152:155], v[168:171], v[80:83]
	v_mfma_f32_16x16x32_bf16 v[76:79], v[160:163], v[168:171], v[76:79]
	v_mfma_f32_16x16x32_bf16 v[120:123], v[132:135], v[188:191], v[120:123]
	v_mfma_f32_16x16x32_bf16 v[116:119], v[140:143], v[188:191], v[116:119]
	v_mfma_f32_16x16x32_bf16 v[104:107], v[132:135], v[180:183], v[104:107]
	v_mfma_f32_16x16x32_bf16 v[100:103], v[140:143], v[180:183], v[100:103]
	v_mfma_f32_16x16x32_bf16 v[88:91], v[132:135], v[172:175], v[88:91]
	v_mfma_f32_16x16x32_bf16 v[84:87], v[140:143], v[172:175], v[84:87]
	v_mfma_f32_16x16x32_bf16 v[72:75], v[132:135], v[164:167], v[72:75]
	v_mfma_f32_16x16x32_bf16 v[68:71], v[140:143], v[164:167], v[68:71]
	v_mfma_f32_16x16x32_bf16 v[120:123], v[136:139], v[192:195], v[120:123]
	v_mfma_f32_16x16x32_bf16 v[116:119], v[144:147], v[192:195], v[116:119]
	v_mfma_f32_16x16x32_bf16 v[104:107], v[136:139], v[184:187], v[104:107]
	v_mfma_f32_16x16x32_bf16 v[100:103], v[144:147], v[184:187], v[100:103]
	v_mfma_f32_16x16x32_bf16 v[88:91], v[136:139], v[176:179], v[88:91]
	v_mfma_f32_16x16x32_bf16 v[84:87], v[144:147], v[176:179], v[84:87]
	v_mfma_f32_16x16x32_bf16 v[72:75], v[136:139], v[168:171], v[72:75]
	v_mfma_f32_16x16x32_bf16 v[68:71], v[144:147], v[168:171], v[68:71]
	s_setprio 0
	s_barrier
	s_mov_b32 m0, s18
	v_lshl_add_u64 v[218:219], s[62:63], 0, v[2:3]
	s_add_u32 s40, s62, 0x200000
	ds_read_b128 v[188:191], v228 offset:16384
	ds_read_b128 v[192:195], v228 offset:17408
	ds_read_b128 v[180:183], v228 offset:18432
	ds_read_b128 v[184:187], v228 offset:19456
	ds_read_b128 v[172:175], v228 offset:20480
	ds_read_b128 v[176:179], v228 offset:21504
	ds_read_b128 v[164:167], v228 offset:22528
	ds_read_b128 v[168:171], v228 offset:23552
	global_load_lds_dwordx4 v[218:219], off
	v_lshl_add_u64 v[220:221], s[62:63], 0, v[196:197]
	s_mov_b32 m0, s19
	s_addc_u32 s41, s63, 0
	global_load_lds_dwordx4 v[220:221], off
	v_lshl_add_u64 v[222:223], s[40:41], 0, v[2:3]
	s_mov_b32 m0, s24
	v_lshl_add_u64 v[224:225], s[68:69], 0, v[202:203]
	global_load_lds_dwordx4 v[222:223], off
	v_lshl_add_u64 v[222:223], s[40:41], 0, v[196:197]
	s_mov_b32 m0, s25
	v_cndmask_b32_e64 v229, 0, 1, s[74:75]
	global_load_lds_dwordx4 v[222:223], off
	v_lshl_add_u64 v[222:223], s[68:69], 0, v[204:205]
	s_mov_b32 m0, s16
	v_cmp_ne_u32_e64 s[40:41], 1, v229
	global_load_lds_dwordx4 v[222:223], off
	s_mov_b32 m0, s31
	s_andn2_b64 vcc, exec, s[74:75]
	global_load_lds_dwordx4 v[224:225], off
	s_cbranch_vccnz .LBB0_1240
	s_waitcnt vmcnt(32)
	s_cbranch_execnz .LBB0_1234

; #define PG8_STAGE(bufoff, gbase, voff) do { _Pragma("unroll") for (int _i = 0; _i < 2; ++_i) \
;         __builtin_amdgcn_global_load_lds((const unsigned*)((const char*)(gbase) + (voff)[_i]), (PG8_LAS unsigned*)(lds + (bufoff) + ldsw + _i * 8192), 16, 0, 0); } while (0)
; #define PG8_LDA(dst, b, h) do { _Pragma("unroll") for (int m = 0; m < 4; ++m) _Pragma("unroll") for (int k = 0; k < 2; ++k) dst[m][k] = *(const PG8_LAS bf16x8*)(lds + PG8_SA(b, h) + aoff + m * 2048 + k * 1024); } while (0)
; #define PG8_LDB(dst, b, h) do { _Pragma("unroll") for (int n = 0; n < 2; ++n) _Pragma("unroll") for (int k = 0; k < 2; ++k) dst[n][k] = *(const PG8_LAS bf16x8*)(lds + PG8_SB(b, h) + boff + n * 2048 + k * 1024); } while (0)
; #define PG8_MMA(ai, bj, At, Bt) do { __builtin_amdgcn_s_setprio(1); _Pragma("unroll") for (int m = 0; m < 4; ++m) _Pragma("unroll") for (int n = 0; n < 2; ++n) _Pragma("unroll") for (int k = 0; k < 2; ++k) \
;         acc[ai][bj][m][n] = mma16(Bt[n][k], At[m][k], acc[ai][bj][m][n]); __builtin_amdgcn_s_setprio(0); } while (0)
; #define PG8_WAIT_V(n) asm volatile("s_waitcnt vmcnt(" #n ")" ::: "memory")
; #define PG8_WAIT_VN(n) asm volatile("s_waitcnt vmcnt(%0)" :: "n"(n) : "memory")
; #define PG8_WAIT_L(n) asm volatile("s_waitcnt lgkmcnt(" #n ")" ::: "memory")
; #define PG8_BAR __builtin_amdgcn_s_barrier()
; #define PG8_SCHED __builtin_amdgcn_sched_barrier(0)
; template <class Epi, class Sched, bool ALIGN_EPI = false, bool SP2 = false>
; __device__ __forceinline__ void gemm_phase(PG8_LAS unsigned char* lds, const Gemm g, const Sched& S, const Epi& E, Stopwatch& sw) {
;     ...
;             if (relax) PG8_WAIT_VN(8 + Epi::NST); else PG8_WAIT_V(8); PG8_WAIT_L(0); PG8_BAR; PG8_MMA(1, 0, At, B0); PG8_MMA(1, 1, At, B1); PG8_BAR; PG8_SCHED;
;             PG8_LDB(B0, 1, 0); PG8_LDB(B1, 1, 1); PG8_SCHED; PG8_LDA(At, 1, 0); PG8_STAGE(PG8_SA(0, 1), a2 + hstep, voffA);
;             if (relax) PG8_WAIT_VN(8 + Epi::NST); else PG8_WAIT_V(8); PG8_WAIT_L(0); PG8_BAR; PG8_MMA(0, 0, At, B0); PG8_MMA(0, 1, At, B1); PG8_BAR; PG8_SCHED;
.LBB0_1234:
	s_waitcnt lgkmcnt(0)
	s_barrier
	s_setprio 1
	s_waitcnt lgkmcnt(0)
	v_mfma_f32_16x16x32_bf16 v[64:67], v[148:151], v[188:191], v[64:67]
	v_mfma_f32_16x16x32_bf16 v[60:63], v[156:159], v[188:191], v[60:63]
	v_mfma_f32_16x16x32_bf16 v[48:51], v[148:151], v[180:183], v[48:51]
	v_mfma_f32_16x16x32_bf16 v[44:47], v[156:159], v[180:183], v[44:47]
	v_mfma_f32_16x16x32_bf16 v[32:35], v[148:151], v[172:175], v[32:35]
	v_mfma_f32_16x16x32_bf16 v[28:31], v[156:159], v[172:175], v[28:31]
	v_mfma_f32_16x16x32_bf16 v[16:19], v[148:151], v[164:167], v[16:19]
	v_mfma_f32_16x16x32_bf16 v[12:15], v[156:159], v[164:167], v[12:15]
	v_mfma_f32_16x16x32_bf16 v[64:67], v[152:155], v[192:195], v[64:67]
	v_mfma_f32_16x16x32_bf16 v[60:63], v[160:163], v[192:195], v[60:63]
	v_mfma_f32_16x16x32_bf16 v[48:51], v[152:155], v[184:187], v[48:51]
	v_mfma_f32_16x16x32_bf16 v[44:47], v[160:163], v[184:187], v[44:47]
	v_mfma_f32_16x16x32_bf16 v[32:35], v[152:155], v[176:179], v[32:35]
	v_mfma_f32_16x16x32_bf16 v[28:31], v[160:163], v[176:179], v[28:31]
	v_mfma_f32_16x16x32_bf16 v[16:19], v[152:155], v[168:171], v[16:19]
	v_mfma_f32_16x16x32_bf16 v[12:15], v[160:163], v[168:171], v[12:15]
	v_mfma_f32_16x16x32_bf16 v[56:59], v[132:135], v[188:191], v[56:59]
	v_mfma_f32_16x16x32_bf16 v[52:55], v[140:143], v[188:191], v[52:55]
	v_mfma_f32_16x16x32_bf16 v[40:43], v[132:135], v[180:183], v[40:43]
	v_mfma_f32_16x16x32_bf16 v[36:39], v[140:143], v[180:183], v[36:39]
	v_mfma_f32_16x16x32_bf16 v[24:27], v[132:135], v[172:175], v[24:27]
	v_mfma_f32_16x16x32_bf16 v[20:23], v[140:143], v[172:175], v[20:23]
	v_mfma_f32_16x16x32_bf16 v[8:11], v[132:135], v[164:167], v[8:11]
	v_mfma_f32_16x16x32_bf16 v[4:7], v[140:143], v[164:167], v[4:7]
	v_mfma_f32_16x16x32_bf16 v[56:59], v[136:139], v[192:195], v[56:59]
	v_mfma_f32_16x16x32_bf16 v[52:55], v[144:147], v[192:195], v[52:55]
	v_mfma_f32_16x16x32_bf16 v[40:43], v[136:139], v[184:187], v[40:43]
	v_mfma_f32_16x16x32_bf16 v[36:39], v[144:147], v[184:187], v[36:39]
	v_mfma_f32_16x16x32_bf16 v[24:27], v[136:139], v[176:179], v[24:27]
	v_mfma_f32_16x16x32_bf16 v[20:23], v[144:147], v[176:179], v[20:23]
	v_mfma_f32_16x16x32_bf16 v[8:11], v[136:139], v[168:171], v[8:11]
	v_mfma_f32_16x16x32_bf16 v[4:7], v[144:147], v[168:171], v[4:7]
	s_setprio 0
	s_barrier
	v_add_u32_e32 v132, 0x18000, v227
	v_add_u32_e32 v144, 0x1c000, v227
	ds_read_b128 v[148:151], v132
	ds_read_b128 v[152:155], v132 offset:1024
	ds_read_b128 v[156:159], v132 offset:2048
	ds_read_b128 v[160:163], v132 offset:3072
	ds_read_b128 v[132:135], v144
	ds_read_b128 v[136:139], v144 offset:1024
	ds_read_b128 v[140:143], v144 offset:2048
	ds_read_b128 v[144:147], v144 offset:3072
	s_add_u32 s68, s68, 0x200000
	s_addc_u32 s69, s69, 0
	s_mov_b32 m0, s72
	v_lshl_add_u64 v[230:231], s[68:69], 0, v[204:205]
	ds_read_b128 v[188:191], v228 offset:32768
	ds_read_b128 v[192:195], v228 offset:33792
	ds_read_b128 v[180:183], v228 offset:34816
	ds_read_b128 v[184:187], v228 offset:35840
	ds_read_b128 v[172:175], v228 offset:36864
	ds_read_b128 v[176:179], v228 offset:37888
	ds_read_b128 v[164:167], v228 offset:38912
	ds_read_b128 v[168:171], v228 offset:39936
	global_load_lds_dwordx4 v[230:231], off
	v_lshl_add_u64 v[230:231], s[68:69], 0, v[202:203]
	s_mov_b32 m0, s73
	s_and_b64 vcc, exec, s[40:41]
	global_load_lds_dwordx4 v[230:231], off
	s_mov_b64 s[74:75], s[10:11]
	s_cbranch_vccnz .LBB0_1241
	s_waitcnt vmcnt(32)
	s_cbranch_execnz .LBB0_1237

; #define PG8_STAGE(bufoff, gbase, voff) do { _Pragma("unroll") for (int _i = 0; _i < 2; ++_i) \
;         __builtin_amdgcn_global_load_lds((const unsigned*)((const char*)(gbase) + (voff)[_i]), (PG8_LAS unsigned*)(lds + (bufoff) + ldsw + _i * 8192), 16, 0, 0); } while (0)
; #define PG8_LDA(dst, b, h) do { _Pragma("unroll") for (int m = 0; m < 4; ++m) _Pragma("unroll") for (int k = 0; k < 2; ++k) dst[m][k] = *(const PG8_LAS bf16x8*)(lds + PG8_SA(b, h) + aoff + m * 2048 + k * 1024); } while (0)
; #define PG8_MMA(ai, bj, At, Bt) do { __builtin_amdgcn_s_setprio(1); _Pragma("unroll") for (int m = 0; m < 4; ++m) _Pragma("unroll") for (int n = 0; n < 2; ++n) _Pragma("unroll") for (int k = 0; k < 2; ++k) \
;         acc[ai][bj][m][n] = mma16(Bt[n][k], At[m][k], acc[ai][bj][m][n]); __builtin_amdgcn_s_setprio(0); } while (0)
; #define PG8_WAIT_V(n) asm volatile("s_waitcnt vmcnt(" #n ")" ::: "memory")
; #define PG8_WAIT_VN(n) asm volatile("s_waitcnt vmcnt(%0)" :: "n"(n) : "memory")
; #define PG8_WAIT_L(n) asm volatile("s_waitcnt lgkmcnt(" #n ")" ::: "memory")
; #define PG8_BAR __builtin_amdgcn_s_barrier()
; #define PG8_SCHED __builtin_amdgcn_sched_barrier(0)
; template <class Epi, class Sched, bool ALIGN_EPI = false, bool SP2 = false>
; __device__ __forceinline__ void gemm_phase(PG8_LAS unsigned char* lds, const Gemm g, const Sched& S, const Epi& E, Stopwatch& sw) {
;     ...
;             if (relax) PG8_WAIT_VN(8 + Epi::NST); else PG8_WAIT_V(8); PG8_WAIT_L(0); PG8_BAR; PG8_MMA(0, 0, At, B0); PG8_MMA(0, 1, At, B1); PG8_BAR; PG8_SCHED;
;             PG8_LDA(At, 1, 1); PG8_STAGE(PG8_SB(1, 0), b3, voffB); PG8_STAGE(PG8_SB(1, 1), b3 + hstep, voffB); PG8_STAGE(PG8_SA(1, 0), a3, voffA);
;             PG8_WAIT_V(8); PG8_WAIT_L(0); PG8_BAR; PG8_MMA(1, 0, At, B0); PG8_MMA(1, 1, At, B1); PG8_BAR; PG8_SCHED;
;             if (last && has_next) PG8_STAGE(PG8_SA(1, 1), a3 + hstep, voffA);
.LBB0_1237:
	s_waitcnt lgkmcnt(0)
	s_and_b64 s[40:41], s[38:39], s[64:65]
	s_barrier
	s_setprio 1
	s_waitcnt lgkmcnt(0)
	v_mfma_f32_16x16x32_bf16 v[128:131], v[148:151], v[188:191], v[128:131]
	v_mfma_f32_16x16x32_bf16 v[124:127], v[156:159], v[188:191], v[124:127]
	v_mfma_f32_16x16x32_bf16 v[112:115], v[148:151], v[180:183], v[112:115]
	v_mfma_f32_16x16x32_bf16 v[108:111], v[156:159], v[180:183], v[108:111]
	v_mfma_f32_16x16x32_bf16 v[96:99], v[148:151], v[172:175], v[96:99]
	v_mfma_f32_16x16x32_bf16 v[92:95], v[156:159], v[172:175], v[92:95]
	v_mfma_f32_16x16x32_bf16 v[80:83], v[148:151], v[164:167], v[80:83]
	v_mfma_f32_16x16x32_bf16 v[76:79], v[156:159], v[164:167], v[76:79]
	v_mfma_f32_16x16x32_bf16 v[128:131], v[152:155], v[192:195], v[128:131]
	v_mfma_f32_16x16x32_bf16 v[124:127], v[160:163], v[192:195], v[124:127]
	v_mfma_f32_16x16x32_bf16 v[112:115], v[152:155], v[184:187], v[112:115]
	v_mfma_f32_16x16x32_bf16 v[108:111], v[160:163], v[184:187], v[108:111]
	v_mfma_f32_16x16x32_bf16 v[96:99], v[152:155], v[176:179], v[96:99]
	v_mfma_f32_16x16x32_bf16 v[92:95], v[160:163], v[176:179], v[92:95]
	v_mfma_f32_16x16x32_bf16 v[80:83], v[152:155], v[168:171], v[80:83]
	v_mfma_f32_16x16x32_bf16 v[76:79], v[160:163], v[168:171], v[76:79]
	v_mfma_f32_16x16x32_bf16 v[120:123], v[132:135], v[188:191], v[120:123]
	v_mfma_f32_16x16x32_bf16 v[116:119], v[140:143], v[188:191], v[116:119]
	v_mfma_f32_16x16x32_bf16 v[104:107], v[132:135], v[180:183], v[104:107]
	v_mfma_f32_16x16x32_bf16 v[100:103], v[140:143], v[180:183], v[100:103]
	v_mfma_f32_16x16x32_bf16 v[88:91], v[132:135], v[172:175], v[88:91]
	v_mfma_f32_16x16x32_bf16 v[84:87], v[140:143], v[172:175], v[84:87]
	v_mfma_f32_16x16x32_bf16 v[72:75], v[132:135], v[164:167], v[72:75]
	v_mfma_f32_16x16x32_bf16 v[68:71], v[140:143], v[164:167], v[68:71]
	v_mfma_f32_16x16x32_bf16 v[120:123], v[136:139], v[192:195], v[120:123]
	v_mfma_f32_16x16x32_bf16 v[116:119], v[144:147], v[192:195], v[116:119]
	v_mfma_f32_16x16x32_bf16 v[104:107], v[136:139], v[184:187], v[104:107]
	v_mfma_f32_16x16x32_bf16 v[100:103], v[144:147], v[184:187], v[100:103]
	v_mfma_f32_16x16x32_bf16 v[88:91], v[136:139], v[176:179], v[88:91]
	v_mfma_f32_16x16x32_bf16 v[84:87], v[144:147], v[176:179], v[84:87]
	v_mfma_f32_16x16x32_bf16 v[72:75], v[136:139], v[168:171], v[72:75]
	v_mfma_f32_16x16x32_bf16 v[68:71], v[144:147], v[168:171], v[68:71]
	s_setprio 0
	s_barrier
	s_mov_b32 m0, s79
	v_lshl_add_u64 v[218:219], v[218:219], 0, s[20:21]
	s_add_u32 s62, s62, 0x200080
	ds_read_b128 v[164:167], v228 offset:49152
	ds_read_b128 v[168:171], v228 offset:50176
	ds_read_b128 v[172:175], v228 offset:51200
	ds_read_b128 v[176:179], v228 offset:52224
	ds_read_b128 v[180:183], v228 offset:53248
	ds_read_b128 v[184:187], v228 offset:54272
	ds_read_b128 v[188:191], v228 offset:55296
	ds_read_b128 v[192:195], v228 offset:56320
	global_load_lds_dwordx4 v[218:219], off
	v_lshl_add_u64 v[218:219], v[220:221], 0, s[20:21]
	s_mov_b32 m0, s80
	s_addc_u32 s63, s63, 0
	global_load_lds_dwordx4 v[218:219], off
	v_lshl_add_u64 v[218:219], s[62:63], 0, v[2:3]
	s_mov_b32 m0, s83
	s_nop 0
	global_load_lds_dwordx4 v[218:219], off
	v_lshl_add_u64 v[218:219], s[62:63], 0, v[196:197]
	s_mov_b32 m0, s90
	s_nop 0
	global_load_lds_dwordx4 v[218:219], off
	v_lshl_add_u64 v[218:219], v[222:223], 0, s[20:21]
	s_mov_b32 m0, s81
	s_nop 0
	global_load_lds_dwordx4 v[218:219], off
	v_lshl_add_u64 v[218:219], v[224:225], 0, s[20:21]
	s_mov_b32 m0, s82
	s_nop 0
	global_load_lds_dwordx4 v[218:219], off
	s_waitcnt vmcnt(8)
	s_waitcnt lgkmcnt(0)
	s_barrier
	s_setprio 1
	s_waitcnt lgkmcnt(0)
	v_mfma_f32_16x16x32_bf16 v[64:67], v[148:151], v[164:167], v[64:67]
	v_mfma_f32_16x16x32_bf16 v[60:63], v[156:159], v[164:167], v[60:63]
	v_mfma_f32_16x16x32_bf16 v[48:51], v[148:151], v[172:175], v[48:51]
	v_mfma_f32_16x16x32_bf16 v[44:47], v[156:159], v[172:175], v[44:47]
	v_mfma_f32_16x16x32_bf16 v[32:35], v[148:151], v[180:183], v[32:35]
	v_mfma_f32_16x16x32_bf16 v[28:31], v[156:159], v[180:183], v[28:31]
	v_mfma_f32_16x16x32_bf16 v[16:19], v[148:151], v[188:191], v[16:19]
	v_mfma_f32_16x16x32_bf16 v[12:15], v[156:159], v[188:191], v[12:15]
	v_mfma_f32_16x16x32_bf16 v[64:67], v[152:155], v[168:171], v[64:67]
	v_mfma_f32_16x16x32_bf16 v[60:63], v[160:163], v[168:171], v[60:63]
	v_mfma_f32_16x16x32_bf16 v[48:51], v[152:155], v[176:179], v[48:51]
	v_mfma_f32_16x16x32_bf16 v[44:47], v[160:163], v[176:179], v[44:47]
	v_mfma_f32_16x16x32_bf16 v[32:35], v[152:155], v[184:187], v[32:35]
	v_mfma_f32_16x16x32_bf16 v[28:31], v[160:163], v[184:187], v[28:31]
	v_mfma_f32_16x16x32_bf16 v[16:19], v[152:155], v[192:195], v[16:19]
	v_mfma_f32_16x16x32_bf16 v[12:15], v[160:163], v[192:195], v[12:15]
	v_mfma_f32_16x16x32_bf16 v[56:59], v[132:135], v[164:167], v[56:59]
	v_mfma_f32_16x16x32_bf16 v[52:55], v[140:143], v[164:167], v[52:55]
	v_mfma_f32_16x16x32_bf16 v[40:43], v[132:135], v[172:175], v[40:43]
	v_mfma_f32_16x16x32_bf16 v[36:39], v[140:143], v[172:175], v[36:39]
	v_mfma_f32_16x16x32_bf16 v[24:27], v[132:135], v[180:183], v[24:27]
	v_mfma_f32_16x16x32_bf16 v[20:23], v[140:143], v[180:183], v[20:23]
	v_mfma_f32_16x16x32_bf16 v[8:11], v[132:135], v[188:191], v[8:11]
	v_mfma_f32_16x16x32_bf16 v[4:7], v[140:143], v[188:191], v[4:7]
	v_mfma_f32_16x16x32_bf16 v[56:59], v[136:139], v[168:171], v[56:59]
	v_mfma_f32_16x16x32_bf16 v[52:55], v[144:147], v[168:171], v[52:55]
	v_mfma_f32_16x16x32_bf16 v[40:43], v[136:139], v[176:179], v[40:43]
	v_mfma_f32_16x16x32_bf16 v[36:39], v[144:147], v[176:179], v[36:39]
	v_mfma_f32_16x16x32_bf16 v[24:27], v[136:139], v[184:187], v[24:27]
	v_mfma_f32_16x16x32_bf16 v[20:23], v[144:147], v[184:187], v[20:23]
	v_mfma_f32_16x16x32_bf16 v[8:11], v[136:139], v[192:195], v[8:11]
	v_mfma_f32_16x16x32_bf16 v[4:7], v[144:147], v[192:195], v[4:7]
	s_setprio 0
	s_barrier
	s_andn2_b64 vcc, exec, s[40:41]
	s_cbranch_vccnz .LBB0_1227
	s_add_i32 m0, s16, 0xc000
	s_nop 0
	global_load_lds_dwordx4 v[212:213], off
	s_add_i32 m0, s16, 0xe000
	s_nop 0
	global_load_lds_dwordx4 v[210:211], off
	s_branch .LBB0_1227
